# finalize loop head: counted vmcnt(4) instead of draining the previous row's 4 output stores; explicit drain before loop entry and on the skip path
# baseline (speedup 1.0000x reference)
; __device__ __forceinline__ void p5_finalize(const Ctx& X, const P5In& I) {
;     P5Par P;
;     { const float a = wave_sum(I.lamp[X.lane] * I.lamp[64 + X.lane]), b = wave_sum(I.lamp[128 + X.lane] * I.lamp[192 + X.lane]); P.lam = __expf(a) - __expf(b) + I.lambda_init; }
; #pragma unroll
;     for (int g = 0; g < 2; ++g) { const int ch = g * 512 + 8 * X.lane; P.D[g] = I.d_skip[ch >> 6]; P.gs[g][0] = *(const f32x4*)(I.ssd_g + ch); P.gs[g][1] = *(const f32x4*)(I.ssd_g + ch + 4); }
;     P.gm[0] = *(const f32x4*)(I.moba_g + 8 * X.lane); P.gm[1] = *(const f32x4*)(I.moba_g + 8 * X.lane + 4);
;     P.gd[0] = *(const f32x4*)(I.subln_g + 8 * (X.lane & 15)); P.gd[1] = *(const f32x4*)(I.subln_g + 8 * (X.lane & 15) + 4);
;     P5Row A, B;
;     p5_load(A, I, X.gw < NTOK ? X.gw : NTOK - 1, X.lane);
;     for (int t = X.gw; t < NTOK; t += 2 * X.ngw) { const int t1 = t + X.ngw, t2 = t + 2 * X.ngw;
.LBB0_1771:
	s_cmp_lt_i32 s40, 8
	s_cselect_b64 s[0:1], -1, 0
	s_add_u32 s64, s88, 0x3f200000
	s_addc_u32 s65, s89, 0
	s_and_b64 s[4:5], s[0:1], s[4:5]
	s_andn2_b64 vcc, exec, s[4:5]
	s_cbranch_vccnz .LBB0_1778
	v_mov_b32_e32 v1, v0
	v_readlane_b32 s4, v254, 60
	v_and_b32_e32 v34, 63, v1
	s_waitcnt vmcnt(0)
	v_lshlrev_b32_e32 v2, 2, v34
	v_readlane_b32 s18, v255, 10
	v_readlane_b32 s19, v255, 11
	s_nop 4
	global_load_dword v3, v2, s[18:19]
	global_load_dword v4, v2, s[18:19] offset:256
	global_load_dword v5, v2, s[18:19] offset:512
	s_nop 0
	global_load_dword v2, v2, s[18:19] offset:768
	v_mbcnt_lo_u32_b32 v6, -1, 0
	v_readlane_b32 s5, v254, 61
	v_mbcnt_hi_u32_b32 v6, -1, v6
	v_readfirstlane_b32 s5, v1
	v_and_b32_e32 v1, 64, v6
	v_xor_b32_e32 v7, 1, v6
	v_add_u32_e32 v13, 64, v1
	v_cmp_lt_i32_e32 vcc, v7, v13
	v_xor_b32_e32 v8, 2, v6
	v_xor_b32_e32 v9, 4, v6
	v_cndmask_b32_e32 v1, v6, v7, vcc
	v_lshlrev_b32_e32 v1, 2, v1
	v_cmp_lt_i32_e32 vcc, v8, v13
	v_xor_b32_e32 v10, 8, v6
	v_xor_b32_e32 v11, 16, v6
	v_cndmask_b32_e32 v8, v6, v8, vcc
	v_lshlrev_b32_e32 v138, 2, v8
	v_cmp_lt_i32_e32 vcc, v9, v13
	v_xor_b32_e32 v12, 32, v6
	s_lshl_b32 s4, s2, 3
	s_ashr_i32 s5, s5, 6
	s_add_i32 s4, s5, s4
	s_cmpk_gt_i32 s4, 0x1fff
	v_readlane_b32 s6, v254, 62
	v_readlane_b32 s7, v254, 63
	v_readlane_b32 s8, v255, 0
	v_readlane_b32 s9, v255, 1
	v_readlane_b32 s10, v255, 2
	v_readlane_b32 s11, v255, 3
	v_readlane_b32 s12, v255, 4
	v_readlane_b32 s13, v255, 5
	v_readlane_b32 s14, v255, 6
	v_readlane_b32 s15, v255, 7
	v_readlane_b32 s16, v255, 8
	v_readlane_b32 s17, v255, 9
	s_waitcnt vmcnt(2)
	v_mul_f32_e32 v7, v3, v4
	ds_bpermute_b32 v7, v1, v7
	s_waitcnt vmcnt(0)
	v_mul_f32_e32 v14, v5, v2
	ds_bpermute_b32 v14, v1, v14
	s_waitcnt lgkmcnt(0)
	v_fmac_f32_e32 v7, v3, v4
	v_cndmask_b32_e32 v4, v6, v9, vcc
	v_fmac_f32_e32 v14, v5, v2
	ds_bpermute_b32 v2, v138, v7
	ds_bpermute_b32 v3, v138, v14
	v_lshlrev_b32_e32 v139, 2, v4
	v_cmp_lt_i32_e32 vcc, v10, v13
	s_waitcnt lgkmcnt(1)
	v_add_f32_e32 v2, v7, v2
	s_waitcnt lgkmcnt(0)
	v_add_f32_e32 v3, v14, v3
	ds_bpermute_b32 v4, v139, v2
	ds_bpermute_b32 v5, v139, v3
	v_cndmask_b32_e32 v7, v6, v10, vcc
	v_lshlrev_b32_e32 v140, 2, v7
	v_cmp_lt_i32_e32 vcc, v11, v13
	s_waitcnt lgkmcnt(1)
	v_add_f32_e32 v2, v2, v4
	s_waitcnt lgkmcnt(0)
	v_add_f32_e32 v3, v3, v5
	ds_bpermute_b32 v4, v140, v2
	ds_bpermute_b32 v5, v140, v3
	v_cndmask_b32_e32 v7, v6, v11, vcc
	v_lshlrev_b32_e32 v141, 2, v7
	v_cmp_lt_i32_e32 vcc, v12, v13
	s_waitcnt lgkmcnt(1)
	v_add_f32_e32 v2, v2, v4
	s_waitcnt lgkmcnt(0)
	v_add_f32_e32 v3, v3, v5
	ds_bpermute_b32 v4, v141, v2
	ds_bpermute_b32 v5, v141, v3
	v_cndmask_b32_e32 v6, v6, v12, vcc
	v_lshlrev_b32_e32 v142, 2, v6
	s_waitcnt lgkmcnt(1)
	v_add_f32_e32 v63, v2, v4
	s_waitcnt lgkmcnt(0)
	v_add_f32_e32 v62, v3, v5
	ds_bpermute_b32 v65, v142, v63
	ds_bpermute_b32 v64, v142, v62
	s_cbranch_scc1 .LBB0_1778
	s_load_dword s14, s[96:97], 0xf8
	s_ashr_i32 s5, s4, 31
	s_lshl_b64 s[6:7], s[4:5], 10
	s_lshl_b64 s[8:9], s[4:5], 11
	v_mov_b32_e32 v125, 0
	s_waitcnt lgkmcnt(0)
	s_lshl_b32 s22, s14, 3
	s_add_u32 s8, s86, s8
	v_lshlrev_b32_e32 v66, 5, v34
	s_addc_u32 s9, s87, s9
	v_and_b32_e32 v70, 0x600, v66
	v_mov_b32_e32 v71, v125
	s_add_u32 s6, s90, s6
	v_lshlrev_b32_e32 v122, 3, v34
	v_lshrrev_b32_e32 v2, 1, v34
	v_lshlrev_b32_e32 v68, 4, v34
	v_lshl_add_u64 v[34:35], s[8:9], 0, v[70:71]
	s_addc_u32 s7, s91, s7
	s_mul_i32 s8, s4, 0x2c00
	s_mul_hi_i32 s9, s4, 0x2c00
	s_add_u32 s8, s42, s8
	s_addc_u32 s9, s43, s9
	s_mul_i32 s10, s4, 0xc00
	v_readlane_b32 s16, v254, 49
	s_mul_hi_i32 s11, s4, 0xc00
	v_readlane_b32 s17, v254, 50
	s_add_u32 s10, s16, s10
	v_and_b32_e32 v124, 0x78, v122
	s_addc_u32 s11, s17, s11
	s_lshl_b64 s[12:13], s[4:5], 12
	v_readlane_b32 s18, v254, 53
	v_readlane_b32 s68, v254, 60
	v_readlane_b32 s44, v254, 31
	v_lshlrev_b32_e32 v72, 1, v124
	v_mov_b32_e32 v73, v125
	v_readlane_b32 s19, v254, 54
	s_add_u32 s12, s18, s12
	v_and_b32_e32 v3, 28, v2
	v_bitop3_b32 v2, v2, 60, 32 bitop3:0xc8
	v_readlane_b32 s76, v255, 4
	v_readlane_b32 s77, v255, 5
	v_readlane_b32 s78, v255, 6
	v_readlane_b32 s79, v255, 7
	v_lshlrev_b32_e32 v6, 2, v124
	v_readlane_b32 s45, v254, 32
	v_lshl_add_u64 v[38:39], v[34:35], 0, v[72:73]
	s_addc_u32 s13, s19, s13
	v_readlane_b32 s80, v255, 8
	v_readlane_b32 s81, v255, 9
	global_load_dword v143, v3, s[76:77]
	global_load_dword v144, v2, s[76:77]
	s_nop 0
	global_load_dwordx4 v[2:5], v6, s[44:45]
	s_nop 0
	global_load_dwordx4 v[6:9], v6, s[44:45] offset:16
	s_nop 0
	global_load_dwordx4 v[10:13], v66, s[78:79] offset:2048
	global_load_dwordx4 v[14:17], v66, s[78:79] offset:2064
	global_load_dwordx4 v[18:21], v66, s[80:81]
	global_load_dwordx4 v[22:25], v66, s[78:79]
	global_load_dwordx4 v[26:29], v66, s[80:81] offset:16
	global_load_dwordx4 v[30:33], v66, s[78:79] offset:16
	global_load_dwordx4 v[34:37], v[38:39], off offset:256
	s_nop 0
	global_load_dwordx4 v[38:41], v[38:39], off
	v_add_f32_e32 v63, v63, v65
	global_load_dwordx4 v[50:53], v68, s[10:11] offset:1024
	global_load_dwordx4 v[46:49], v66, s[12:13] offset:2064
	global_load_dwordx4 v[58:61], v66, s[12:13] offset:2048
	global_load_dwordx4 v[42:45], v68, s[6:7]
	global_load_dwordx4 v[82:85], v68, s[8:9]
	global_load_dwordx4 v[54:57], v68, s[8:9] offset:1024
	global_load_dwordx4 v[78:81], v68, s[10:11]
	global_load_dwordx4 v[74:77], v66, s[12:13] offset:16
	global_load_dwordx4 v[98:101], v66, s[12:13]
	v_add_f32_e32 v62, v62, v64
	v_mul_f32_e32 v63, 0x3fb8aa3b, v63
	v_mul_f32_e32 v62, 0x3fb8aa3b, v62
	v_exp_f32_e32 v63, v63
	v_exp_f32_e32 v62, v62
	v_mov_b32_e32 v67, v125
	v_mov_b32_e32 v69, v125
	v_mov_b32_e32 v123, v125
	v_sub_f32_e32 v62, v63, v62
	v_add_f32_e32 v145, 0x3e4ccccd, v62
	v_lshl_add_u64 v[62:63], s[86:87], 0, v[70:71]
	v_lshl_add_u64 v[126:127], s[90:91], 0, v[68:69]
	v_and_b32_e32 v128, 0x180, v122
	v_mov_b32_e32 v129, v125
	v_lshl_add_u64 v[130:131], s[18:19], 0, v[66:67]
	v_lshl_add_u64 v[132:133], s[16:17], 0, v[68:69]
	v_lshl_add_u64 v[134:135], s[42:43], 0, v[68:69]
	v_lshl_add_u64 v[136:137], v[62:63], 0, v[72:73]
	s_lshl_b32 s23, s14, 4
	v_mov_b32_e32 v146, 0x358637bd
	s_mov_b32 s24, 0xf800000
	v_mov_b32_e32 v147, 0x260
	s_mov_b32 s25, 0xc3e00000
	s_mov_b32 s26, 0x3f4ccccd
	v_mov_b32_e32 v148, 0xc00
	v_mov_b32_e32 v149, 0x2c00
	v_mov_b32_e32 v150, 0x43e00000
	v_readlane_b32 s69, v254, 61
	v_readlane_b32 s70, v254, 62
	v_readlane_b32 s71, v254, 63
	v_readlane_b32 s72, v255, 0
	v_readlane_b32 s73, v255, 1
	v_readlane_b32 s74, v255, 2
	v_readlane_b32 s75, v255, 3
	v_readlane_b32 s82, v255, 10
	v_readlane_b32 s83, v255, 11
	v_readlane_b32 s46, v254, 33
	v_readlane_b32 s47, v254, 34
	v_readlane_b32 s48, v254, 35
	v_readlane_b32 s49, v254, 36
	v_readlane_b32 s50, v254, 37
	v_readlane_b32 s51, v254, 38
	v_readlane_b32 s52, v254, 39
	v_readlane_b32 s53, v254, 40
	v_readlane_b32 s54, v254, 41
	v_readlane_b32 s55, v254, 42
	v_readlane_b32 s56, v254, 43
	v_readlane_b32 s57, v254, 44
	v_readlane_b32 s58, v254, 45
	v_readlane_b32 s59, v254, 46
	s_waitcnt vmcnt(0)
	s_branch .LBB0_1775

; __device__ __forceinline__ float bflo(unsigned w) { return __uint_as_float(w << 16); }
; __device__ __forceinline__ float bfhi(unsigned w) { return __uint_as_float(w & 0xffff0000u); }
; __device__ __forceinline__ float siluf(float a) { return a / (1.0f + __expf(-a)); }
; __device__ __forceinline__ void p5_item(const P5Row& R, const P5In& I, const P5Par& P, int t, int lane) {
; #pragma unroll
;     for (int g = 0; g < 2; ++g) { const int ch = g * 512 + 8 * lane;
;         const f32x4 y0 = R.ya[g], y1 = R.yb[g]; const v4u xv = R.xr[g], zv = R.zr[g];
;         const float D = P.D[g];
;         float v[8];
;         v[0] = (y0[0] + D * bflo(xv.x)) * siluf(bflo(zv.x)); v[1] = (y0[1] + D * bfhi(xv.x)) * siluf(bfhi(zv.x));
;         v[2] = (y0[2] + D * bflo(xv.y)) * siluf(bflo(zv.y)); v[3] = (y0[3] + D * bfhi(xv.y)) * siluf(bfhi(zv.y));
;         v[4] = (y1[0] + D * bflo(xv.z)) * siluf(bflo(zv.z)); v[5] = (y1[1] + D * bfhi(xv.z)) * siluf(bfhi(zv.z));
;         v[6] = (y1[2] + D * bflo(xv.w)) * siluf(bflo(zv.w)); v[7] = (y1[3] + D * bfhi(xv.w)) * siluf(bfhi(zv.w));
;         float s = 0.f;
; #pragma unroll
;         for (int i = 0; i < 8; ++i) s += v[i] * v[i];
;         s = wave_sum(s); const float r = 1.0f / sqrtf(s * (1.0f / 512.0f) + EPSF);
.LBB0_1775:
	s_waitcnt vmcnt(4)
	v_lshlrev_b32_e32 v62, 16, v82
	v_mul_f32_e32 v63, 0xbfb8aa3b, v62
	v_exp_f32_e32 v63, v63
	s_waitcnt vmcnt(4)
	v_lshlrev_b32_e32 v66, 16, v78
	s_waitcnt vmcnt(4)
	v_fma_f32 v66, v143, v66, v98
	s_add_i32 s6, s4, s22
	v_add_f32_e32 v63, 1.0, v63
	v_div_scale_f32 v64, s[8:9], v63, v63, v62
	v_rcp_f32_e32 v65, v64
	s_add_i32 s7, s23, s4
	s_cmpk_lt_i32 s6, 0x2000
	s_cselect_b32 s20, s6, 0x1fff
	v_fma_f32 v67, -v64, v65, 1.0
	v_fmac_f32_e32 v65, v67, v65
	v_div_scale_f32 v67, vcc, v62, v63, v62
	v_mul_f32_e32 v68, v67, v65
	v_fma_f32 v69, -v64, v68, v67
	v_fmac_f32_e32 v68, v69, v65
	v_fma_f32 v64, -v64, v68, v67
	v_and_b32_e32 v67, 0xffff0000, v82
	v_mul_f32_e32 v69, 0xbfb8aa3b, v67
	v_exp_f32_e32 v69, v69
	v_div_fmas_f32 v64, v64, v65, v68
	v_div_fixup_f32 v62, v64, v63, v62
	v_mul_f32_e32 v82, v62, v66
	v_add_f32_e32 v63, 1.0, v69
	v_div_scale_f32 v64, s[8:9], v63, v63, v67
	v_rcp_f32_e32 v65, v64
	v_and_b32_e32 v62, 0xffff0000, v78
	v_fma_f32 v62, v143, v62, v99
	s_ashr_i32 s21, s20, 31
	v_fma_f32 v66, -v64, v65, 1.0
	v_fmac_f32_e32 v65, v66, v65
	v_div_scale_f32 v66, vcc, v67, v63, v67
	v_mul_f32_e32 v68, v66, v65
	v_fma_f32 v69, -v64, v68, v66
	v_fmac_f32_e32 v68, v69, v65
	v_fma_f32 v64, -v64, v68, v66
	v_lshlrev_b32_e32 v66, 16, v83
	v_mul_f32_e32 v69, 0xbfb8aa3b, v66
	v_exp_f32_e32 v69, v69
	v_div_fmas_f32 v64, v64, v65, v68
	v_div_fixup_f32 v63, v64, v63, v67
	v_mul_f32_e32 v78, v63, v62
	v_add_f32_e32 v64, 1.0, v69
	v_div_scale_f32 v65, s[8:9], v64, v64, v66
	v_rcp_f32_e32 v67, v65
	v_lshlrev_b32_e32 v62, 16, v79
	v_fma_f32 v62, v143, v62, v100
	s_ashr_i32 s5, s4, 31
	v_fma_f32 v63, -v65, v67, 1.0
	v_fmac_f32_e32 v67, v63, v67
	v_div_scale_f32 v63, vcc, v66, v64, v66
	v_mul_f32_e32 v68, v63, v67
	v_fma_f32 v69, -v65, v68, v63
	v_fmac_f32_e32 v68, v69, v67
	v_fma_f32 v63, -v65, v68, v63
	v_and_b32_e32 v65, 0xffff0000, v83
	v_mul_f32_e32 v69, 0xbfb8aa3b, v65
	v_exp_f32_e32 v69, v69
	v_div_fmas_f32 v63, v63, v67, v68
	v_div_fixup_f32 v63, v63, v64, v66
	v_mul_f32_e32 v83, v63, v62
	v_add_f32_e32 v64, 1.0, v69
	v_div_scale_f32 v66, s[8:9], v64, v64, v65
	v_rcp_f32_e32 v67, v66
	v_and_b32_e32 v62, 0xffff0000, v79
	v_fmac_f32_e32 v101, v143, v62
	s_lshl_b64 s[28:29], s[20:21], 10
	v_fma_f32 v62, -v66, v67, 1.0
	v_fmac_f32_e32 v67, v62, v67
	v_div_scale_f32 v62, vcc, v65, v64, v65
	v_mul_f32_e32 v63, v62, v67
	v_fma_f32 v68, -v66, v63, v62
	v_fmac_f32_e32 v63, v68, v67
	v_fma_f32 v62, -v66, v63, v62
	v_lshlrev_b32_e32 v66, 16, v84
	v_mul_f32_e32 v68, 0xbfb8aa3b, v66
	v_exp_f32_e32 v68, v68
	v_div_fmas_f32 v62, v62, v67, v63
	v_div_fixup_f32 v62, v62, v64, v65
	v_mul_f32_e32 v79, v62, v101
	v_add_f32_e32 v63, 1.0, v68
	v_div_scale_f32 v64, s[8:9], v63, v63, v66
	v_rcp_f32_e32 v65, v64
	v_lshlrev_b32_e32 v62, 16, v80
	v_fma_f32 v62, v143, v62, v74
	s_lshl_b64 s[30:31], s[20:21], 12
	v_fma_f32 v67, -v64, v65, 1.0
	v_fmac_f32_e32 v65, v67, v65
	v_div_scale_f32 v67, vcc, v66, v63, v66
	v_mul_f32_e32 v68, v67, v65
	v_fma_f32 v69, -v64, v68, v67
	v_fmac_f32_e32 v68, v69, v65
	v_fma_f32 v64, -v64, v68, v67
	v_and_b32_e32 v67, 0xffff0000, v84
	v_mul_f32_e32 v69, 0xbfb8aa3b, v67
	v_exp_f32_e32 v69, v69
	v_div_fmas_f32 v64, v64, v65, v68
	v_div_fixup_f32 v63, v64, v63, v66
	v_mul_f32_e32 v74, v63, v62
	v_add_f32_e32 v64, 1.0, v69
	v_div_scale_f32 v65, s[8:9], v64, v64, v67
	v_rcp_f32_e32 v66, v65
	v_and_b32_e32 v62, 0xffff0000, v80
	v_fma_f32 v62, v143, v62, v75
	s_lshl_b64 s[34:35], s[20:21], 11
	v_fma_f32 v63, -v65, v66, 1.0
	v_fmac_f32_e32 v66, v63, v66
	v_div_scale_f32 v63, vcc, v67, v64, v67
	v_mul_f32_e32 v68, v63, v66
	v_fma_f32 v69, -v65, v68, v63
	v_fmac_f32_e32 v68, v69, v66
	v_fma_f32 v63, -v65, v68, v63
	v_lshlrev_b32_e32 v65, 16, v85
	v_mul_f32_e32 v69, 0xbfb8aa3b, v65
	v_exp_f32_e32 v69, v69
	v_div_fmas_f32 v63, v63, v66, v68
	v_div_fixup_f32 v63, v63, v64, v67
	v_mul_f32_e32 v75, v63, v62
	v_add_f32_e32 v64, 1.0, v69
	v_div_scale_f32 v66, s[8:9], v64, v64, v65
	v_rcp_f32_e32 v67, v66
	v_lshlrev_b32_e32 v62, 16, v81
	v_fma_f32 v62, v143, v62, v76
	s_lshl_b64 s[4:5], s[4:5], 11
	v_fma_f32 v63, -v66, v67, 1.0
	v_fmac_f32_e32 v67, v63, v67
	v_div_scale_f32 v63, vcc, v65, v64, v65
	v_mul_f32_e32 v68, v63, v67
	v_fma_f32 v69, -v66, v68, v63
	v_fmac_f32_e32 v68, v69, v67
	v_fma_f32 v63, -v66, v68, v63
	v_and_b32_e32 v66, 0xffff0000, v85
	v_mul_f32_e32 v69, 0xbfb8aa3b, v66
	v_exp_f32_e32 v69, v69
	v_div_fmas_f32 v63, v63, v67, v68
	v_div_fixup_f32 v63, v63, v64, v65
	v_mul_f32_e32 v76, v63, v62
	v_add_f32_e32 v64, 1.0, v69
	v_div_scale_f32 v65, s[8:9], v64, v64, v66
	v_rcp_f32_e32 v67, v65
	v_and_b32_e32 v62, 0xffff0000, v81
	v_fmac_f32_e32 v77, v143, v62
	s_add_u32 s14, s64, s4
	v_fma_f32 v62, -v65, v67, 1.0
	v_fmac_f32_e32 v67, v62, v67
	v_div_scale_f32 v62, vcc, v66, v64, v66
	v_mul_f32_e32 v63, v62, v67
	v_fma_f32 v68, -v65, v63, v62
	v_fmac_f32_e32 v63, v68, v67
	v_fma_f32 v62, -v65, v63, v62
	v_div_fmas_f32 v62, v62, v67, v63
	v_div_fixup_f32 v62, v62, v64, v66
	v_mul_f32_e32 v77, v62, v77
	v_mul_f32_e32 v62, v78, v78
	v_fmac_f32_e32 v62, v82, v82
	v_fmac_f32_e32 v62, v83, v83
	v_fmac_f32_e32 v62, v79, v79
	v_fmac_f32_e32 v62, v74, v74
	v_fmac_f32_e32 v62, v75, v75
	v_fmac_f32_e32 v62, v76, v76
	v_fmac_f32_e32 v62, v77, v77
	ds_bpermute_b32 v63, v1, v62
	s_addc_u32 s15, s65, s5
	v_mad_i64_i32 v[66:67], s[4:5], s20, v149, v[134:135]
	s_min_i32 s12, s7, 0x1fff
	s_waitcnt lgkmcnt(0)
	v_add_f32_e32 v62, v62, v63
	ds_bpermute_b32 v63, v138, v62
	s_ashr_i32 s13, s12, 31
	s_lshl_b64 s[16:17], s[12:13], 12
	s_lshl_b64 s[8:9], s[12:13], 10
	s_lshl_b64 s[10:11], s[12:13], 11
	s_waitcnt lgkmcnt(0)
; __device__ __forceinline__ float bflo(unsigned w) { return __uint_as_float(w << 16); }
; __device__ __forceinline__ float bfhi(unsigned w) { return __uint_as_float(w & 0xffff0000u); }
; __device__ __forceinline__ float siluf(float a) { return a / (1.0f + __expf(-a)); }
; __device__ __forceinline__ void p5_load(P5Row& R, const P5In& I, int t, int lane) {
; #pragma unroll
;     for (int g = 0; g < 2; ++g) { const int ch = g * 512 + 8 * lane;
;         R.ya[g] = *(const f32x4*)(I.yraw + (size_t)t * 1024 + ch); R.yb[g] = *(const f32x4*)(I.yraw + (size_t)t * 1024 + ch + 4);
;         R.xr[g] = *(const v4u*)(I.xc + (size_t)t * 1536 + ch); R.zr[g] = *(const v4u*)(I.proj + (size_t)t * NPROJ + C_Z + ch); }
;     R.m4 = *(const v4u*)(I.moba + (size_t)t * 512 + 8 * lane);
;     const int dh = lane >> 4, dd = 8 * (lane & 15);
;     R.a4 = *(const v4u*)(I.diff + (size_t)t * 1024 + (dh * 2 + 0) * 128 + dd); R.b4 = *(const v4u*)(I.diff + (size_t)t * 1024 + (dh * 2 + 1) * 128 + dd);
; }
; __device__ __forceinline__ void p5_item(const P5Row& R, const P5In& I, const P5Par& P, int t, int lane) {
;     ...
;     for (int g = 0; g < 2; ++g) { const int ch = g * 512 + 8 * lane;
;         const f32x4 y0 = R.ya[g], y1 = R.yb[g]; const v4u xv = R.xr[g], zv = R.zr[g];
;         const float D = P.D[g];
;         float v[8];
;         v[0] = (y0[0] + D * bflo(xv.x)) * siluf(bflo(zv.x)); v[1] = (y0[1] + D * bfhi(xv.x)) * siluf(bfhi(zv.x));
;         v[2] = (y0[2] + D * bflo(xv.y)) * siluf(bflo(zv.y)); v[3] = (y0[3] + D * bfhi(xv.y)) * siluf(bfhi(zv.y));
;         v[4] = (y1[0] + D * bflo(xv.z)) * siluf(bflo(zv.z)); v[5] = (y1[1] + D * bfhi(xv.z)) * siluf(bfhi(zv.z));
;         v[6] = (y1[2] + D * bflo(xv.w)) * siluf(bflo(zv.w)); v[7] = (y1[3] + D * bfhi(xv.w)) * siluf(bfhi(zv.w));
;         float s = 0.f;
; #pragma unroll
;         for (int i = 0; i < 8; ++i) s += v[i] * v[i];
;         s = wave_sum(s); const float r = 1.0f / sqrtf(s * (1.0f / 512.0f) + EPSF);
	v_add_f32_e32 v62, v62, v63
	ds_bpermute_b32 v63, v139, v62
	s_cmpk_gt_i32 s6, 0x1fff
	s_waitcnt lgkmcnt(0)
	v_add_f32_e32 v64, v62, v63
	ds_bpermute_b32 v65, v140, v64
	v_lshl_add_u64 v[62:63], v[130:131], 0, s[30:31]
	global_load_dwordx4 v[106:109], v[62:63], off offset:16
	global_load_dwordx4 v[118:121], v[62:63], off
	s_waitcnt lgkmcnt(0)
	v_add_f32_e32 v68, v64, v65
	ds_bpermute_b32 v69, v141, v68
	v_mad_i64_i32 v[64:65], s[4:5], s20, v148, v[132:133]
	global_load_dwordx4 v[86:89], v[62:63], off offset:2064
	global_load_dwordx4 v[102:105], v[62:63], off offset:2048
	global_load_dwordx4 v[110:113], v[64:65], off
	global_load_dwordx4 v[90:93], v[64:65], off offset:1024
	global_load_dwordx4 v[114:117], v[66:67], off
	global_load_dwordx4 v[94:97], v[66:67], off offset:1024
	s_waitcnt lgkmcnt(0)
	v_add_f32_e32 v68, v68, v69
	ds_bpermute_b32 v69, v142, v68
	v_lshl_add_u64 v[66:67], v[136:137], 0, s[34:35]
	s_waitcnt lgkmcnt(0)
	v_add_f32_e32 v62, v68, v69
	v_fmamk_f32 v62, v62, 0x3b000000, v146
	v_mul_f32_e32 v63, 0x4f800000, v62
	v_cmp_gt_f32_e32 vcc, s24, v62
	s_nop 1
	v_cndmask_b32_e32 v64, v62, v63, vcc
	v_sqrt_f32_e32 v65, v64
	v_lshl_add_u64 v[62:63], v[126:127], 0, s[28:29]
	v_add_u32_e32 v68, -1, v65
	v_fma_f32 v69, -v68, v65, v64
	v_cmp_ge_f32_e64 s[4:5], 0, v69
	v_add_u32_e32 v69, 1, v65
	s_nop 0
	v_cndmask_b32_e64 v68, v65, v68, s[4:5]
	v_fma_f32 v65, -v69, v65, v64
	v_cmp_lt_f32_e64 s[4:5], 0, v65
	s_nop 1
	v_cndmask_b32_e64 v65, v68, v69, s[4:5]
	v_mul_f32_e32 v68, 0x37800000, v65
	v_cndmask_b32_e32 v65, v65, v68, vcc
	v_cmp_class_f32_e32 vcc, v64, v147
	s_nop 1
	v_cndmask_b32_e32 v80, v65, v64, vcc
	v_div_scale_f32 v81, s[4:5], v80, v80, 1.0
	v_rcp_f32_e32 v84, v81
	global_load_dwordx4 v[70:73], v[62:63], off
	s_nop 0
	global_load_dwordx4 v[62:65], v[66:67], off
	s_nop 0
	global_load_dwordx4 v[66:69], v[66:67], off offset:256
	v_fma_f32 v85, -v81, v84, 1.0
	v_fmac_f32_e32 v84, v85, v84
	v_div_scale_f32 v85, vcc, 1.0, v80, 1.0
	v_mul_f32_e32 v98, v85, v84
	v_fma_f32 v99, -v81, v98, v85
	v_fmac_f32_e32 v98, v99, v84
	v_fma_f32 v81, -v81, v98, v85
	v_lshlrev_b32_e32 v85, 16, v54
	v_mul_f32_e32 v99, 0xbfb8aa3b, v85
	v_exp_f32_e32 v99, v99
	v_div_fmas_f32 v81, v81, v84, v98
	v_div_fixup_f32 v80, v81, v80, 1.0
	v_and_b32_e32 v54, 0xffff0000, v54
	v_add_f32_e32 v81, 1.0, v99
	v_div_scale_f32 v84, s[4:5], v81, v81, v85
	v_rcp_f32_e32 v98, v84
	v_lshlrev_b32_e32 v99, 16, v50
	v_fma_f32 v58, v144, v99, v58
	v_and_b32_e32 v50, 0xffff0000, v50
	v_fma_f32 v99, -v84, v98, 1.0
	v_fmac_f32_e32 v98, v99, v98
	v_div_scale_f32 v99, vcc, v85, v81, v85
	v_mul_f32_e32 v100, v99, v98
	v_fma_f32 v101, -v84, v100, v99
	v_fmac_f32_e32 v100, v101, v98
	v_fma_f32 v84, -v84, v100, v99
	v_mul_f32_e32 v99, 0xbfb8aa3b, v54
	v_exp_f32_e32 v99, v99
	v_div_fmas_f32 v84, v84, v98, v100
	v_div_fixup_f32 v81, v84, v81, v85
	v_fma_f32 v50, v144, v50, v59
	v_add_f32_e32 v84, 1.0, v99
	v_div_scale_f32 v85, s[4:5], v84, v84, v54
	v_rcp_f32_e32 v98, v85
	v_mul_f32_e32 v58, v81, v58
	v_mul_f32_e32 v80, 0x41000000, v80
	v_fma_f32 v59, -v85, v98, 1.0
	v_fmac_f32_e32 v98, v59, v98
	v_div_scale_f32 v59, vcc, v54, v84, v54
	v_mul_f32_e32 v81, v59, v98
	v_fma_f32 v99, -v85, v81, v59
	v_fmac_f32_e32 v81, v99, v98
	v_fma_f32 v59, -v85, v81, v59
	v_lshlrev_b32_e32 v85, 16, v55
	v_mul_f32_e32 v99, 0xbfb8aa3b, v85
	v_exp_f32_e32 v99, v99
	v_div_fmas_f32 v59, v59, v98, v81
	v_div_fixup_f32 v54, v59, v84, v54
	v_mul_f32_e32 v50, v54, v50
	v_add_f32_e32 v59, 1.0, v99
	v_div_scale_f32 v81, s[4:5], v59, v59, v85
	v_rcp_f32_e32 v84, v81
	v_lshlrev_b32_e32 v54, 16, v51
	v_fma_f32 v54, v144, v54, v60
	v_and_b32_e32 v55, 0xffff0000, v55
	v_fma_f32 v60, -v81, v84, 1.0
	v_fmac_f32_e32 v84, v60, v84
	v_div_scale_f32 v60, vcc, v85, v59, v85
	v_mul_f32_e32 v98, v60, v84
	v_fma_f32 v99, -v81, v98, v60
	v_fmac_f32_e32 v98, v99, v84
	v_fma_f32 v60, -v81, v98, v60
	v_mul_f32_e32 v81, 0xbfb8aa3b, v55
	v_exp_f32_e32 v81, v81
	v_div_fmas_f32 v60, v60, v84, v98
	v_div_fixup_f32 v59, v60, v59, v85
	v_and_b32_e32 v51, 0xffff0000, v51
	v_add_f32_e32 v60, 1.0, v81
	v_div_scale_f32 v81, s[4:5], v60, v60, v55
	v_rcp_f32_e32 v84, v81
	v_fmac_f32_e32 v61, v144, v51
	v_mul_f32_e32 v54, v59, v54
	v_fma_f32 v51, -v81, v84, 1.0
	v_fmac_f32_e32 v84, v51, v84
	v_div_scale_f32 v51, vcc, v55, v60, v55
	v_mul_f32_e32 v59, v51, v84
	v_fma_f32 v85, -v81, v59, v51
	v_fmac_f32_e32 v59, v85, v84
	v_fma_f32 v51, -v81, v59, v51
	v_lshlrev_b32_e32 v81, 16, v56
	v_mul_f32_e32 v85, 0xbfb8aa3b, v81
	v_exp_f32_e32 v85, v85
	v_div_fmas_f32 v51, v51, v84, v59
	v_div_fixup_f32 v51, v51, v60, v55
	v_mul_f32_e32 v51, v51, v61
	v_add_f32_e32 v55, 1.0, v85
	v_div_scale_f32 v59, s[4:5], v55, v55, v81
	v_rcp_f32_e32 v60, v59
	v_lshlrev_b32_e32 v61, 16, v52
	v_fma_f32 v46, v144, v61, v46
	v_and_b32_e32 v56, 0xffff0000, v56
	v_fma_f32 v61, -v59, v60, 1.0
	v_fmac_f32_e32 v60, v61, v60
	v_div_scale_f32 v61, vcc, v81, v55, v81
	v_mul_f32_e32 v84, v61, v60
	v_fma_f32 v85, -v59, v84, v61
	v_fmac_f32_e32 v84, v85, v60
	v_fma_f32 v59, -v59, v84, v61
	v_mul_f32_e32 v61, 0xbfb8aa3b, v56
	v_exp_f32_e32 v61, v61
	v_div_fmas_f32 v59, v59, v60, v84
	v_div_fixup_f32 v55, v59, v55, v81
	v_mul_f32_e32 v55, v55, v46
	v_add_f32_e32 v59, 1.0, v61
	v_div_scale_f32 v60, s[4:5], v59, v59, v56
	v_rcp_f32_e32 v61, v60
	v_and_b32_e32 v46, 0xffff0000, v52
	v_fma_f32 v46, v144, v46, v47
	v_fma_f32 v47, -v60, v61, 1.0
	v_fmac_f32_e32 v61, v47, v61
	v_div_scale_f32 v47, vcc, v56, v59, v56
	v_mul_f32_e32 v52, v47, v61
	v_fma_f32 v81, -v60, v52, v47
	v_fmac_f32_e32 v52, v81, v61
	v_fma_f32 v47, -v60, v52, v47
	v_lshlrev_b32_e32 v60, 16, v57
	v_mul_f32_e32 v81, 0xbfb8aa3b, v60
; __device__ __forceinline__ float bflo(unsigned w) { return __uint_as_float(w << 16); }
; __device__ __forceinline__ float bfhi(unsigned w) { return __uint_as_float(w & 0xffff0000u); }
; __device__ __forceinline__ void p5_item(const P5Row& R, const P5In& I, const P5Par& P, int t, int lane) {
;     ...
;         float s = 0.f;
; #pragma unroll
;         for (int i = 0; i < 8; ++i) s += v[i] * v[i];
;         s = wave_sum(s); const float r = 1.0f / sqrtf(s * (1.0f / 512.0f) + EPSF);
;         p5_put8(I, (size_t)t * DM + ch, v, r, P.gs[g][0], P.gs[g][1]); }
;     { const int ch = 8 * lane; const v4u r4 = R.m4;
;       float v[8] = {bflo(r4.x), bfhi(r4.x), bflo(r4.y), bfhi(r4.y), bflo(r4.z), bfhi(r4.z), bflo(r4.w), bfhi(r4.w)}; float s = 0.f;
; #pragma unroll
;       for (int i = 0; i < 8; ++i) s += v[i] * v[i];
;       s += __shfl_xor(s, 1); s += __shfl_xor(s, 2); s += __shfl_xor(s, 4);
;       const float r = 1.0f / sqrtf(s * (1.0f / 64.0f) + EPSF);
;       p5_put8(I, (size_t)t * DM + 1024 + ch, v, r, P.gm[0], P.gm[1]); }
	v_exp_f32_e32 v81, v81
	v_div_fmas_f32 v47, v47, v61, v52
	v_div_fixup_f32 v47, v47, v59, v56
	v_mul_f32_e32 v61, v47, v46
	v_add_f32_e32 v52, 1.0, v81
	v_div_scale_f32 v56, s[4:5], v52, v52, v60
	v_rcp_f32_e32 v59, v56
	v_lshlrev_b32_e32 v46, 16, v53
	v_fma_f32 v46, v144, v46, v48
	v_fma_f32 v47, -v56, v59, 1.0
	v_fmac_f32_e32 v59, v47, v59
	v_div_scale_f32 v47, vcc, v60, v52, v60
	v_mul_f32_e32 v48, v47, v59
	v_fma_f32 v81, -v56, v48, v47
	v_fmac_f32_e32 v48, v81, v59
	v_fma_f32 v47, -v56, v48, v47
	v_and_b32_e32 v56, 0xffff0000, v57
	v_mul_f32_e32 v57, 0xbfb8aa3b, v56
	v_exp_f32_e32 v57, v57
	v_div_fmas_f32 v47, v47, v59, v48
	v_div_fixup_f32 v47, v47, v52, v60
	v_mul_f32_e32 v59, v47, v46
	v_add_f32_e32 v48, 1.0, v57
	v_div_scale_f32 v52, s[4:5], v48, v48, v56
	v_rcp_f32_e32 v57, v52
	v_and_b32_e32 v46, 0xffff0000, v53
	v_fmac_f32_e32 v49, v144, v46
	v_fma_f32 v46, -v52, v57, 1.0
	v_fmac_f32_e32 v57, v46, v57
	v_div_scale_f32 v46, vcc, v56, v48, v56
	v_mul_f32_e32 v47, v46, v57
	v_fma_f32 v53, -v52, v47, v46
	v_fmac_f32_e32 v47, v53, v57
	v_fma_f32 v46, -v52, v47, v46
	v_div_fmas_f32 v46, v46, v57, v47
	v_div_fixup_f32 v46, v46, v48, v56
	v_mul_f32_e32 v49, v46, v49
	v_mul_f32_e32 v46, v50, v50
	v_fmac_f32_e32 v46, v58, v58
	v_fmac_f32_e32 v46, v54, v54
	v_fmac_f32_e32 v46, v51, v51
	v_fmac_f32_e32 v46, v55, v55
	v_fmac_f32_e32 v46, v61, v61
	v_fmac_f32_e32 v46, v59, v59
	v_fmac_f32_e32 v46, v49, v49
	ds_bpermute_b32 v47, v1, v46
	v_mul_f32_e32 v48, v82, v80
	v_mul_f32_e32 v52, v78, v80
	v_mul_f32_e32 v48, v22, v48
	v_mul_f32_e32 v52, v23, v52
	s_waitcnt lgkmcnt(0)
	v_add_f32_e32 v46, v46, v47
	ds_bpermute_b32 v47, v138, v46
	v_med3_f32 v48, v48, s25, v150
	v_med3_f32 v52, v52, s25, v150
	v_mul_f32_e32 v53, v83, v80
	v_mul_f32_e32 v56, v79, v80
	s_waitcnt lgkmcnt(0)
	v_add_f32_e32 v47, v46, v47
	ds_bpermute_b32 v57, v139, v47
	v_mov_b32_e32 v46, 0
	v_cvt_pk_fp8_f32 v46, v48, v52
	v_mul_f32_e32 v53, v24, v53
	v_mul_f32_e32 v56, v25, v56
	s_waitcnt lgkmcnt(0)
	v_add_f32_e32 v47, v47, v57
	ds_bpermute_b32 v48, v140, v47
	v_med3_f32 v52, v53, s25, v150
	v_med3_f32 v53, v56, s25, v150
	v_cvt_pk_fp8_f32 v46, v52, v53 op_sel:[0,0,1]
	v_mul_f32_e32 v52, v74, v80
	s_waitcnt lgkmcnt(0)
	v_add_f32_e32 v47, v47, v48
	ds_bpermute_b32 v48, v141, v47
	v_mul_f32_e32 v53, v75, v80
	v_mul_f32_e32 v52, v30, v52
	v_mul_f32_e32 v53, v31, v53
	v_med3_f32 v52, v52, s25, v150
	s_waitcnt lgkmcnt(0)
	v_add_f32_e32 v47, v47, v48
	ds_bpermute_b32 v48, v142, v47
	v_med3_f32 v53, v53, s25, v150
	v_mul_f32_e32 v56, v76, v80
	v_mul_f32_e32 v57, v77, v80
	v_mul_f32_e32 v56, v32, v56
	s_waitcnt lgkmcnt(0)
	v_add_f32_e32 v47, v47, v48
	v_fmamk_f32 v47, v47, 0x3b000000, v146
	v_mul_f32_e32 v48, 0x4f800000, v47
	v_cmp_gt_f32_e32 vcc, s24, v47
	v_mul_f32_e32 v57, v33, v57
	v_med3_f32 v56, v56, s25, v150
	v_cndmask_b32_e32 v48, v47, v48, vcc
	v_sqrt_f32_e32 v60, v48
	v_mov_b32_e32 v47, 0
	v_cvt_pk_fp8_f32 v47, v52, v53
	v_med3_f32 v57, v57, s25, v150
	v_add_u32_e32 v52, -1, v60
	v_fma_f32 v53, -v52, v60, v48
	v_cmp_ge_f32_e64 s[4:5], 0, v53
	v_add_u32_e32 v53, 1, v60
	v_cvt_pk_fp8_f32 v47, v56, v57 op_sel:[0,0,1]
	v_cndmask_b32_e64 v52, v60, v52, s[4:5]
	v_fma_f32 v60, -v53, v60, v48
	v_cmp_lt_f32_e64 s[4:5], 0, v60
	s_nop 1
	v_cndmask_b32_e64 v52, v52, v53, s[4:5]
	v_mul_f32_e32 v53, 0x37800000, v52
	v_cndmask_b32_e32 v52, v52, v53, vcc
	v_cmp_class_f32_e32 vcc, v48, v147
	s_nop 1
	v_cndmask_b32_e32 v48, v52, v48, vcc
	v_div_scale_f32 v52, s[4:5], v48, v48, 1.0
	v_rcp_f32_e32 v53, v52
	s_nop 0
	v_fma_f32 v56, -v52, v53, 1.0
	v_fmac_f32_e32 v53, v56, v53
	v_div_scale_f32 v56, vcc, 1.0, v48, 1.0
	v_mul_f32_e32 v57, v56, v53
	v_fma_f32 v60, -v52, v57, v56
	v_fmac_f32_e32 v57, v60, v53
	v_fma_f32 v52, -v52, v57, v56
	v_div_fmas_f32 v52, v52, v53, v57
	v_div_fixup_f32 v48, v52, v48, 1.0
	v_mul_f32_e32 v52, 0x41000000, v48
	v_mul_f32_e32 v48, v58, v52
	v_mul_f32_e32 v50, v50, v52
	v_mul_f32_e32 v48, v10, v48
	v_mul_f32_e32 v50, v11, v50
	v_mul_f32_e32 v53, v54, v52
	v_med3_f32 v54, v48, s25, v150
	v_med3_f32 v50, v50, s25, v150
	v_mov_b32_e32 v48, 0
	v_cvt_pk_fp8_f32 v48, v54, v50
	v_mul_f32_e32 v51, v51, v52
	v_mul_f32_e32 v53, v12, v53
	v_mul_f32_e32 v50, v13, v51
	v_med3_f32 v51, v53, s25, v150
	v_med3_f32 v50, v50, s25, v150
	v_cvt_pk_fp8_f32 v48, v51, v50 op_sel:[0,0,1]
	v_and_b32_e32 v51, 0xffff0000, v42
	v_lshlrev_b32_e32 v50, 16, v42
	v_mul_f32_e32 v42, v51, v51
	v_lshlrev_b32_e32 v53, 16, v43
	v_fmac_f32_e32 v42, v50, v50
	v_and_b32_e32 v54, 0xffff0000, v43
	v_fmac_f32_e32 v42, v53, v53
	v_lshlrev_b32_e32 v56, 16, v44
	v_fmac_f32_e32 v42, v54, v54
	v_and_b32_e32 v44, 0xffff0000, v44
	v_fmac_f32_e32 v42, v56, v56
	v_lshlrev_b32_e32 v57, 16, v45
	v_fmac_f32_e32 v42, v44, v44
	v_and_b32_e32 v45, 0xffff0000, v45
	v_fmac_f32_e32 v42, v57, v57
	v_fmac_f32_e32 v42, v45, v45
	ds_bpermute_b32 v43, v1, v42
	v_mul_f32_e32 v55, v55, v52
	v_mul_f32_e32 v58, v61, v52
	v_mul_f32_e32 v55, v14, v55
	v_mul_f32_e32 v58, v15, v58
	s_waitcnt lgkmcnt(0)
	v_add_f32_e32 v42, v42, v43
	ds_bpermute_b32 v43, v138, v42
	v_mul_f32_e32 v49, v49, v52
	v_mul_f32_e32 v59, v59, v52
	v_mul_f32_e32 v52, v17, v49
	v_med3_f32 v55, v55, s25, v150
	s_waitcnt lgkmcnt(0)
	v_add_f32_e32 v42, v42, v43
	ds_bpermute_b32 v43, v139, v42
	v_med3_f32 v58, v58, s25, v150
	v_mov_b32_e32 v49, 0
	v_cvt_pk_fp8_f32 v49, v55, v58
	v_mul_f32_e32 v59, v16, v59
	s_waitcnt lgkmcnt(0)
; __device__ __forceinline__ void p5_item(const P5Row& R, const P5In& I, const P5Par& P, int t, int lane) {
;     ...
;     { const int ch = 8 * lane; const v4u r4 = R.m4;
;       float v[8] = {bflo(r4.x), bfhi(r4.x), bflo(r4.y), bfhi(r4.y), bflo(r4.z), bfhi(r4.z), bflo(r4.w), bfhi(r4.w)}; float s = 0.f;
; #pragma unroll
;       for (int i = 0; i < 8; ++i) s += v[i] * v[i];
;       s += __shfl_xor(s, 1); s += __shfl_xor(s, 2); s += __shfl_xor(s, 4);
;       const float r = 1.0f / sqrtf(s * (1.0f / 64.0f) + EPSF);
;       p5_put8(I, (size_t)t * DM + 1024 + ch, v, r, P.gm[0], P.gm[1]); }
;     { const int h = lane >> 4, d = 8 * (lane & 15); const v4u a4 = R.a4, b4 = R.b4; const float lam = P.lam;
;       float v[8] = {bflo(a4.x) - lam * bflo(b4.x), bfhi(a4.x) - lam * bfhi(b4.x), bflo(a4.y) - lam * bflo(b4.y), bfhi(a4.y) - lam * bfhi(b4.y),
;                     bflo(a4.z) - lam * bflo(b4.z), bfhi(a4.z) - lam * bfhi(b4.z), bflo(a4.w) - lam * bflo(b4.w), bfhi(a4.w) - lam * bfhi(b4.w)}; float s = 0.f;
; #pragma unroll
;       for (int i = 0; i < 8; ++i) s += v[i] * v[i];
;       s += __shfl_xor(s, 1); s += __shfl_xor(s, 2); s += __shfl_xor(s, 4); s += __shfl_xor(s, 8);
;       const float r = (1.0f - I.lambda_init) / sqrtf(s * (1.0f / 128.0f) + EPSF);
;       p5_put8(I, (size_t)t * DM + 1536 + h * 128 + d, v, r, P.gd[0], P.gd[1]); }
; }
; __device__ __forceinline__ void p5_finalize(const Ctx& X, const P5In& I) {
;     P5Par P;
;     { const float a = wave_sum(I.lamp[X.lane] * I.lamp[64 + X.lane]), b = wave_sum(I.lamp[128 + X.lane] * I.lamp[192 + X.lane]); P.lam = __expf(a) - __expf(b) + I.lambda_init; }
; #pragma unroll
;     for (int g = 0; g < 2; ++g) { const int ch = g * 512 + 8 * X.lane; P.D[g] = I.d_skip[ch >> 6]; P.gs[g][0] = *(const f32x4*)(I.ssd_g + ch); P.gs[g][1] = *(const f32x4*)(I.ssd_g + ch + 4); }
;     P.gm[0] = *(const f32x4*)(I.moba_g + 8 * X.lane); P.gm[1] = *(const f32x4*)(I.moba_g + 8 * X.lane + 4);
;     P.gd[0] = *(const f32x4*)(I.subln_g + 8 * (X.lane & 15)); P.gd[1] = *(const f32x4*)(I.subln_g + 8 * (X.lane & 15) + 4);
;     P5Row A, B;
;     p5_load(A, I, X.gw < NTOK ? X.gw : NTOK - 1, X.lane);
;     for (int t = X.gw; t < NTOK; t += 2 * X.ngw) { const int t1 = t + X.ngw, t2 = t + 2 * X.ngw;
;         p5_load(B, I, t1 < NTOK ? t1 : NTOK - 1, X.lane);
;         p5_item(A, I, P, t, X.lane);
;         p5_load(A, I, t2 < NTOK ? t2 : NTOK - 1, X.lane);
	v_add_f32_e32 v42, v42, v43
	v_fmamk_f32 v42, v42, 0x3c800000, v146
	v_mul_f32_e32 v43, 0x4f800000, v42
	v_cmp_gt_f32_e32 vcc, s24, v42
	v_med3_f32 v55, v59, s25, v150
	v_med3_f32 v52, v52, s25, v150
	v_cndmask_b32_e32 v42, v42, v43, vcc
	v_sqrt_f32_e32 v43, v42
	v_cvt_pk_fp8_f32 v49, v55, v52 op_sel:[0,0,1]
	v_add_u32_e32 v52, -1, v43
	v_fma_f32 v55, -v52, v43, v42
	v_cmp_ge_f32_e64 s[4:5], 0, v55
	v_add_u32_e32 v55, 1, v43
	s_nop 0
	v_cndmask_b32_e64 v52, v43, v52, s[4:5]
	v_fma_f32 v43, -v55, v43, v42
	v_cmp_lt_f32_e64 s[4:5], 0, v43
	s_nop 1
	v_cndmask_b32_e64 v43, v52, v55, s[4:5]
	v_mul_f32_e32 v52, 0x37800000, v43
	v_cndmask_b32_e32 v43, v43, v52, vcc
	v_cmp_class_f32_e32 vcc, v42, v147
	s_nop 1
	v_cndmask_b32_e32 v52, v43, v42, vcc
	v_div_scale_f32 v55, s[4:5], v52, v52, 1.0
	v_rcp_f32_e32 v58, v55
	v_lshl_add_u64 v[42:43], s[14:15], 0, v[122:123]
	global_store_dwordx2 v[42:43], v[46:47], off
	global_store_dwordx2 v[42:43], v[48:49], off offset:512
	v_fma_f32 v46, -v55, v58, 1.0
	v_fmac_f32_e32 v58, v46, v58
	v_div_scale_f32 v46, vcc, 1.0, v52, 1.0
	v_mul_f32_e32 v47, v46, v58
	v_fma_f32 v48, -v55, v47, v46
	v_fmac_f32_e32 v47, v48, v58
	v_fma_f32 v46, -v55, v47, v46
	v_div_fmas_f32 v46, v46, v58, v47
	v_div_fixup_f32 v46, v46, v52, 1.0
	v_mul_f32_e32 v46, 0x41000000, v46
	v_mul_f32_e32 v48, v46, v51
	v_lshlrev_b32_e32 v51, 16, v38
	v_lshlrev_b32_e32 v52, 16, v34
	v_and_b32_e32 v38, 0xffff0000, v38
	v_and_b32_e32 v34, 0xffff0000, v34
	v_fma_f32 v51, -v145, v52, v51
	v_fma_f32 v38, -v145, v34, v38
	v_lshlrev_b32_e32 v34, 16, v39
	v_lshlrev_b32_e32 v52, 16, v35
	v_fma_f32 v52, -v145, v52, v34
	v_and_b32_e32 v34, 0xffff0000, v39
	v_and_b32_e32 v35, 0xffff0000, v35
	v_fma_f32 v39, -v145, v35, v34
	v_lshlrev_b32_e32 v34, 16, v40
	v_lshlrev_b32_e32 v35, 16, v36
	v_mul_f32_e32 v49, v46, v53
	v_fma_f32 v53, -v145, v35, v34
	v_and_b32_e32 v34, 0xffff0000, v40
	v_and_b32_e32 v35, 0xffff0000, v36
	v_fma_f32 v40, -v145, v35, v34
	v_lshlrev_b32_e32 v34, 16, v41
	v_lshlrev_b32_e32 v35, 16, v37
	v_mul_f32_e32 v47, v46, v50
	v_mul_f32_e32 v50, v46, v54
	v_fma_f32 v54, -v145, v35, v34
	v_and_b32_e32 v34, 0xffff0000, v41
	v_and_b32_e32 v35, 0xffff0000, v37
	v_fma_f32 v37, -v145, v35, v34
	v_mul_f32_e32 v35, v38, v38
	v_fmac_f32_e32 v35, v51, v51
	v_fmac_f32_e32 v35, v52, v52
	v_fmac_f32_e32 v35, v39, v39
	v_fmac_f32_e32 v35, v53, v53
	v_fmac_f32_e32 v35, v40, v40
	v_fmac_f32_e32 v35, v54, v54
	v_fmac_f32_e32 v35, v37, v37
	ds_bpermute_b32 v36, v1, v35
	v_mul_f32_e32 v47, v18, v47
	v_mul_f32_e32 v48, v19, v48
	v_med3_f32 v41, v47, s25, v150
	v_med3_f32 v47, v48, s25, v150
	s_waitcnt lgkmcnt(0)
	v_add_f32_e32 v35, v35, v36
	ds_bpermute_b32 v36, v138, v35
	v_mov_b32_e32 v34, 0
	v_cvt_pk_fp8_f32 v34, v41, v47
	v_mul_f32_e32 v49, v20, v49
	v_mul_f32_e32 v50, v21, v50
	s_waitcnt lgkmcnt(0)
	v_add_f32_e32 v35, v35, v36
	ds_bpermute_b32 v36, v139, v35
	v_med3_f32 v41, v49, s25, v150
	v_med3_f32 v47, v50, s25, v150
	v_cvt_pk_fp8_f32 v34, v41, v47 op_sel:[0,0,1]
	v_mul_f32_e32 v41, v46, v56
	s_waitcnt lgkmcnt(0)
	v_add_f32_e32 v35, v35, v36
	ds_bpermute_b32 v36, v140, v35
	v_mul_f32_e32 v44, v46, v44
	v_mul_f32_e32 v47, v46, v57
	v_mul_f32_e32 v45, v46, v45
	v_mul_f32_e32 v41, v26, v41
	s_waitcnt lgkmcnt(0)
	v_add_f32_e32 v35, v35, v36
	v_fmamk_f32 v35, v35, 0x3c000000, v146
	v_mul_f32_e32 v36, 0x4f800000, v35
	v_cmp_gt_f32_e32 vcc, s24, v35
	v_mul_f32_e32 v44, v27, v44
	v_med3_f32 v41, v41, s25, v150
	v_cndmask_b32_e32 v36, v35, v36, vcc
	v_sqrt_f32_e32 v46, v36
	v_med3_f32 v44, v44, s25, v150
	v_mov_b32_e32 v35, 0
	v_cvt_pk_fp8_f32 v35, v41, v44
	v_add_u32_e32 v41, -1, v46
	v_fma_f32 v44, -v41, v46, v36
	v_cmp_ge_f32_e64 s[4:5], 0, v44
	v_add_u32_e32 v44, 1, v46
	v_mul_f32_e32 v47, v28, v47
	v_cndmask_b32_e64 v41, v46, v41, s[4:5]
	v_fma_f32 v46, -v44, v46, v36
	v_cmp_lt_f32_e64 s[4:5], 0, v46
	v_mul_f32_e32 v45, v29, v45
	v_med3_f32 v46, v47, s25, v150
	v_cndmask_b32_e64 v41, v41, v44, s[4:5]
	v_mul_f32_e32 v44, 0x37800000, v41
	v_cndmask_b32_e32 v41, v41, v44, vcc
	v_cmp_class_f32_e32 vcc, v36, v147
	v_med3_f32 v45, v45, s25, v150
	v_cvt_pk_fp8_f32 v35, v46, v45 op_sel:[0,0,1]
	v_cndmask_b32_e32 v36, v41, v36, vcc
	v_div_scale_f32 v41, s[4:5], v36, v36, s26
	v_rcp_f32_e32 v44, v41
	global_store_dwordx2 v[42:43], v[34:35], off offset:1024
	v_lshl_add_u64 v[34:35], s[14:15], 0, v[128:129]
	v_lshl_add_u64 v[34:35], v[34:35], 0, v[124:125]
	v_fma_f32 v45, -v41, v44, 1.0
	v_fmac_f32_e32 v44, v45, v44
	v_div_scale_f32 v45, vcc, s26, v36, s26
	v_mul_f32_e32 v46, v45, v44
	v_fma_f32 v47, -v41, v46, v45
	v_fmac_f32_e32 v46, v47, v44
	v_fma_f32 v41, -v41, v46, v45
	v_div_fmas_f32 v41, v41, v44, v46
	v_div_fixup_f32 v36, v41, v36, s26
	v_mul_f32_e32 v41, 0x41000000, v36
	v_mul_f32_e32 v36, v51, v41
	v_mul_f32_e32 v38, v38, v41
	v_mul_f32_e32 v36, v2, v36
	v_mul_f32_e32 v38, v3, v38
	v_med3_f32 v45, v36, s25, v150
	v_med3_f32 v38, v38, s25, v150
	v_mov_b32_e32 v36, 0
	v_cvt_pk_fp8_f32 v36, v45, v38
	v_mul_f32_e32 v44, v52, v41
	v_mul_f32_e32 v39, v39, v41
	v_mul_f32_e32 v44, v4, v44
	v_mul_f32_e32 v38, v5, v39
	v_med3_f32 v39, v44, s25, v150
	v_med3_f32 v38, v38, s25, v150
	v_cvt_pk_fp8_f32 v36, v39, v38 op_sel:[0,0,1]
	v_mul_f32_e32 v38, v53, v41
	v_mul_f32_e32 v39, v40, v41
	v_mul_f32_e32 v38, v6, v38
	v_mul_f32_e32 v39, v7, v39
	v_mul_f32_e32 v40, v54, v41
	v_mul_f32_e32 v41, v37, v41
	v_med3_f32 v38, v38, s25, v150
	v_med3_f32 v39, v39, s25, v150
	v_mov_b32_e32 v37, 0
	v_cvt_pk_fp8_f32 v37, v38, v39
	v_mul_f32_e32 v40, v8, v40
	v_mul_f32_e32 v38, v9, v41
	v_med3_f32 v39, v40, s25, v150
	v_med3_f32 v38, v38, s25, v150
	v_cvt_pk_fp8_f32 v37, v39, v38 op_sel:[0,0,1]
	v_mad_i64_i32 v[38:39], s[4:5], s12, v149, v[134:135]
	global_store_dwordx2 v[34:35], v[36:37], off offset:1536
	v_lshl_add_u64 v[34:35], v[130:131], 0, s[16:17]
	global_load_dwordx4 v[74:77], v[34:35], off offset:16
	global_load_dwordx4 v[98:101], v[34:35], off
	v_mad_i64_i32 v[36:37], s[4:5], s12, v148, v[132:133]
	global_load_dwordx4 v[46:49], v[34:35], off offset:2064
	global_load_dwordx4 v[58:61], v[34:35], off offset:2048
	global_load_dwordx4 v[78:81], v[36:37], off
	global_load_dwordx4 v[50:53], v[36:37], off offset:1024
	global_load_dwordx4 v[82:85], v[38:39], off
	global_load_dwordx4 v[54:57], v[38:39], off offset:1024
	v_lshl_add_u64 v[34:35], v[126:127], 0, s[8:9]
	v_lshl_add_u64 v[36:37], v[136:137], 0, s[10:11]
	global_load_dwordx4 v[42:45], v[34:35], off
	global_load_dwordx4 v[38:41], v[36:37], off
	s_nop 0
	global_load_dwordx4 v[34:37], v[36:37], off offset:256
	s_cbranch_scc1 .Lfin_skip0
; __device__ __forceinline__ float bflo(unsigned w) { return __uint_as_float(w << 16); }
; __device__ __forceinline__ float bfhi(unsigned w) { return __uint_as_float(w & 0xffff0000u); }
; __device__ __forceinline__ float siluf(float a) { return a / (1.0f + __expf(-a)); }
; __device__ __forceinline__ void p5_item(const P5Row& R, const P5In& I, const P5Par& P, int t, int lane) {
; #pragma unroll
;     for (int g = 0; g < 2; ++g) { const int ch = g * 512 + 8 * lane;
;         const f32x4 y0 = R.ya[g], y1 = R.yb[g]; const v4u xv = R.xr[g], zv = R.zr[g];
;         const float D = P.D[g];
;         float v[8];
;         v[0] = (y0[0] + D * bflo(xv.x)) * siluf(bflo(zv.x)); v[1] = (y0[1] + D * bfhi(xv.x)) * siluf(bfhi(zv.x));
;         v[2] = (y0[2] + D * bflo(xv.y)) * siluf(bflo(zv.y)); v[3] = (y0[3] + D * bfhi(xv.y)) * siluf(bfhi(zv.y));
;         v[4] = (y1[0] + D * bflo(xv.z)) * siluf(bflo(zv.z)); v[5] = (y1[1] + D * bfhi(xv.z)) * siluf(bfhi(zv.z));
;         v[6] = (y1[2] + D * bflo(xv.w)) * siluf(bflo(zv.w)); v[7] = (y1[3] + D * bfhi(xv.w)) * siluf(bfhi(zv.w));
;         float s = 0.f;
; #pragma unroll
;         for (int i = 0; i < 8; ++i) s += v[i] * v[i];
;         s = wave_sum(s); const float r = 1.0f / sqrtf(s * (1.0f / 512.0f) + EPSF);
	s_waitcnt vmcnt(19)
	v_lshlrev_b32_e32 v151, 16, v114
	v_mul_f32_e32 v152, 0xbfb8aa3b, v151
	v_exp_f32_e32 v152, v152
	v_lshlrev_b32_e32 v153, 16, v110
	v_fma_f32 v118, v143, v153, v118
	v_and_b32_e32 v114, 0xffff0000, v114
	v_add_f32_e32 v152, 1.0, v152
	v_div_scale_f32 v154, s[4:5], v152, v152, v151
	v_rcp_f32_e32 v155, v154
	v_div_scale_f32 v153, vcc, v151, v152, v151
	v_and_b32_e32 v110, 0xffff0000, v110
	v_fma_f32 v156, -v154, v155, 1.0
	v_fmac_f32_e32 v155, v156, v155
	v_mul_f32_e32 v156, v153, v155
	v_fma_f32 v157, -v154, v156, v153
	v_fmac_f32_e32 v156, v157, v155
	v_fma_f32 v153, -v154, v156, v153
	v_mul_f32_e32 v154, 0xbfb8aa3b, v114
	v_exp_f32_e32 v154, v154
	v_div_fmas_f32 v153, v153, v155, v156
	v_div_fixup_f32 v151, v153, v152, v151
	v_fma_f32 v110, v143, v110, v119
	v_add_f32_e32 v152, 1.0, v154
	v_div_scale_f32 v153, s[4:5], v152, v152, v114
	v_rcp_f32_e32 v154, v153
	v_mul_f32_e32 v118, v118, v151
	s_ashr_i32 s7, s6, 31
	s_lshl_b64 s[8:9], s[6:7], 11
	v_fma_f32 v119, -v153, v154, 1.0
	v_fmac_f32_e32 v154, v119, v154
	v_div_scale_f32 v119, vcc, v114, v152, v114
	v_mul_f32_e32 v151, v119, v154
	v_fma_f32 v155, -v153, v151, v119
	v_fmac_f32_e32 v151, v155, v154
	v_fma_f32 v119, -v153, v151, v119
	v_lshlrev_b32_e32 v153, 16, v115
	v_mul_f32_e32 v155, 0xbfb8aa3b, v153
	v_exp_f32_e32 v155, v155
	v_div_fmas_f32 v119, v119, v154, v151
	v_div_fixup_f32 v114, v119, v152, v114
	v_mul_f32_e32 v110, v110, v114
	v_add_f32_e32 v119, 1.0, v155
	v_div_scale_f32 v151, s[4:5], v119, v119, v153
	v_rcp_f32_e32 v152, v151
	v_lshlrev_b32_e32 v114, 16, v111
	v_fma_f32 v114, v143, v114, v120
	v_and_b32_e32 v115, 0xffff0000, v115
	v_fma_f32 v120, -v151, v152, 1.0
	v_fmac_f32_e32 v152, v120, v152
	v_div_scale_f32 v120, vcc, v153, v119, v153
	v_mul_f32_e32 v154, v120, v152
	v_fma_f32 v155, -v151, v154, v120
	v_fmac_f32_e32 v154, v155, v152
	v_fma_f32 v120, -v151, v154, v120
	v_mul_f32_e32 v151, 0xbfb8aa3b, v115
	v_exp_f32_e32 v151, v151
	v_div_fmas_f32 v120, v120, v152, v154
	v_div_fixup_f32 v119, v120, v119, v153
	v_and_b32_e32 v111, 0xffff0000, v111
	v_add_f32_e32 v120, 1.0, v151
	v_div_scale_f32 v151, s[4:5], v120, v120, v115
	v_rcp_f32_e32 v152, v151
	v_fmac_f32_e32 v121, v143, v111
	v_mul_f32_e32 v114, v114, v119
	s_add_u32 s8, s64, s8
	v_fma_f32 v111, -v151, v152, 1.0
	v_fmac_f32_e32 v152, v111, v152
	v_div_scale_f32 v111, vcc, v115, v120, v115
	v_mul_f32_e32 v119, v111, v152
	v_fma_f32 v153, -v151, v119, v111
	v_fmac_f32_e32 v119, v153, v152
	v_fma_f32 v111, -v151, v119, v111
	v_lshlrev_b32_e32 v151, 16, v116
	v_mul_f32_e32 v153, 0xbfb8aa3b, v151
	v_exp_f32_e32 v153, v153
	v_div_fmas_f32 v111, v111, v152, v119
	v_div_fixup_f32 v111, v111, v120, v115
	v_mul_f32_e32 v111, v121, v111
	v_add_f32_e32 v115, 1.0, v153
	v_div_scale_f32 v119, s[4:5], v115, v115, v151
	v_rcp_f32_e32 v120, v119
	v_lshlrev_b32_e32 v121, 16, v112
	v_fma_f32 v106, v143, v121, v106
	v_and_b32_e32 v116, 0xffff0000, v116
	v_fma_f32 v121, -v119, v120, 1.0
	v_fmac_f32_e32 v120, v121, v120
	v_div_scale_f32 v121, vcc, v151, v115, v151
	v_mul_f32_e32 v152, v121, v120
	v_fma_f32 v153, -v119, v152, v121
	v_fmac_f32_e32 v152, v153, v120
	v_fma_f32 v119, -v119, v152, v121
	v_mul_f32_e32 v121, 0xbfb8aa3b, v116
	v_exp_f32_e32 v121, v121
	v_div_fmas_f32 v119, v119, v120, v152
	v_div_fixup_f32 v115, v119, v115, v151
	v_and_b32_e32 v112, 0xffff0000, v112
	v_add_f32_e32 v119, 1.0, v121
	v_div_scale_f32 v120, s[4:5], v119, v119, v116
	v_rcp_f32_e32 v121, v120
	v_fma_f32 v107, v143, v112, v107
	v_mul_f32_e32 v106, v106, v115
	s_addc_u32 s9, s65, s9
	v_fma_f32 v112, -v120, v121, 1.0
	v_fmac_f32_e32 v121, v112, v121
	v_div_scale_f32 v112, vcc, v116, v119, v116
	v_mul_f32_e32 v115, v112, v121
	v_fma_f32 v151, -v120, v115, v112
	v_fmac_f32_e32 v115, v151, v121
	v_fma_f32 v112, -v120, v115, v112
	v_lshlrev_b32_e32 v120, 16, v117
	v_mul_f32_e32 v151, 0xbfb8aa3b, v120
	v_exp_f32_e32 v151, v151
	v_div_fmas_f32 v112, v112, v121, v115
	v_div_fixup_f32 v112, v112, v119, v116
	v_mul_f32_e32 v107, v107, v112
	v_add_f32_e32 v115, 1.0, v151
	v_div_scale_f32 v116, s[4:5], v115, v115, v120
	v_rcp_f32_e32 v119, v116
	v_lshlrev_b32_e32 v112, 16, v113
	v_fma_f32 v108, v143, v112, v108
	v_fma_f32 v112, -v116, v119, 1.0
	v_fmac_f32_e32 v119, v112, v119
	v_div_scale_f32 v112, vcc, v120, v115, v120
	v_mul_f32_e32 v121, v112, v119
	v_fma_f32 v151, -v116, v121, v112
	v_fmac_f32_e32 v121, v151, v119
	v_fma_f32 v112, -v116, v121, v112
	v_and_b32_e32 v116, 0xffff0000, v117
	v_mul_f32_e32 v117, 0xbfb8aa3b, v116
	v_exp_f32_e32 v117, v117
	v_div_fmas_f32 v112, v112, v119, v121
	v_div_fixup_f32 v112, v112, v115, v120
	v_mul_f32_e32 v108, v108, v112
	v_add_f32_e32 v115, 1.0, v117
	v_div_scale_f32 v117, s[4:5], v115, v115, v116
	v_rcp_f32_e32 v119, v117
	v_and_b32_e32 v112, 0xffff0000, v113
	v_fmac_f32_e32 v109, v143, v112
	v_fma_f32 v112, -v117, v119, 1.0
	v_fmac_f32_e32 v119, v112, v119
	v_div_scale_f32 v112, vcc, v116, v115, v116
	v_mul_f32_e32 v113, v112, v119
	v_fma_f32 v120, -v117, v113, v112
	v_fmac_f32_e32 v113, v120, v119
	v_fma_f32 v112, -v117, v113, v112
	v_div_fmas_f32 v112, v112, v119, v113
	v_div_fixup_f32 v112, v112, v115, v116
	v_mul_f32_e32 v109, v109, v112
	v_mul_f32_e32 v112, v110, v110
	v_fmac_f32_e32 v112, v118, v118
	v_fmac_f32_e32 v112, v114, v114
	v_fmac_f32_e32 v112, v111, v111
	v_fmac_f32_e32 v112, v106, v106
	v_fmac_f32_e32 v112, v107, v107
	v_fmac_f32_e32 v112, v108, v108
	v_fmac_f32_e32 v112, v109, v109
	ds_bpermute_b32 v113, v1, v112
	s_waitcnt lgkmcnt(0)
	v_add_f32_e32 v112, v112, v113
	ds_bpermute_b32 v113, v138, v112
	s_waitcnt lgkmcnt(0)
	v_add_f32_e32 v112, v112, v113
	ds_bpermute_b32 v113, v139, v112
	s_waitcnt lgkmcnt(0)
; __device__ __forceinline__ float bflo(unsigned w) { return __uint_as_float(w << 16); }
; __device__ __forceinline__ float bfhi(unsigned w) { return __uint_as_float(w & 0xffff0000u); }
; __device__ __forceinline__ float siluf(float a) { return a / (1.0f + __expf(-a)); }
; __device__ __forceinline__ void p5_item(const P5Row& R, const P5In& I, const P5Par& P, int t, int lane) {
;     ...
;     for (int g = 0; g < 2; ++g) { const int ch = g * 512 + 8 * lane;
;         const f32x4 y0 = R.ya[g], y1 = R.yb[g]; const v4u xv = R.xr[g], zv = R.zr[g];
;         const float D = P.D[g];
;         float v[8];
;         v[0] = (y0[0] + D * bflo(xv.x)) * siluf(bflo(zv.x)); v[1] = (y0[1] + D * bfhi(xv.x)) * siluf(bfhi(zv.x));
;         v[2] = (y0[2] + D * bflo(xv.y)) * siluf(bflo(zv.y)); v[3] = (y0[3] + D * bfhi(xv.y)) * siluf(bfhi(zv.y));
;         v[4] = (y1[0] + D * bflo(xv.z)) * siluf(bflo(zv.z)); v[5] = (y1[1] + D * bfhi(xv.z)) * siluf(bfhi(zv.z));
;         v[6] = (y1[2] + D * bflo(xv.w)) * siluf(bflo(zv.w)); v[7] = (y1[3] + D * bfhi(xv.w)) * siluf(bfhi(zv.w));
;         float s = 0.f;
; #pragma unroll
;         for (int i = 0; i < 8; ++i) s += v[i] * v[i];
;         s = wave_sum(s); const float r = 1.0f / sqrtf(s * (1.0f / 512.0f) + EPSF);
;         p5_put8(I, (size_t)t * DM + ch, v, r, P.gs[g][0], P.gs[g][1]); }
	v_add_f32_e32 v112, v112, v113
	ds_bpermute_b32 v113, v140, v112
	s_waitcnt lgkmcnt(0)
	v_add_f32_e32 v112, v112, v113
	ds_bpermute_b32 v113, v141, v112
	s_waitcnt lgkmcnt(0)
	v_add_f32_e32 v112, v112, v113
	ds_bpermute_b32 v113, v142, v112
	s_waitcnt lgkmcnt(0)
	v_add_f32_e32 v112, v112, v113
	v_fmamk_f32 v112, v112, 0x3b000000, v146
	v_mul_f32_e32 v113, 0x4f800000, v112
	v_cmp_gt_f32_e32 vcc, s24, v112
	s_nop 1
	v_cndmask_b32_e32 v112, v112, v113, vcc
	v_sqrt_f32_e32 v113, v112
	s_nop 0
	v_add_u32_e32 v115, -1, v113
	v_fma_f32 v116, -v115, v113, v112
	v_cmp_ge_f32_e64 s[4:5], 0, v116
	v_add_u32_e32 v116, 1, v113
	s_nop 0
	v_cndmask_b32_e64 v115, v113, v115, s[4:5]
	v_fma_f32 v113, -v116, v113, v112
	v_cmp_lt_f32_e64 s[4:5], 0, v113
	s_nop 1
	v_cndmask_b32_e64 v113, v115, v116, s[4:5]
	v_mul_f32_e32 v115, 0x37800000, v113
	v_cndmask_b32_e32 v113, v113, v115, vcc
	v_cmp_class_f32_e32 vcc, v112, v147
	s_nop 1
	v_cndmask_b32_e32 v112, v113, v112, vcc
	v_div_scale_f32 v113, s[4:5], v112, v112, 1.0
	v_rcp_f32_e32 v115, v113
	s_nop 0
	v_fma_f32 v116, -v113, v115, 1.0
	v_fmac_f32_e32 v115, v116, v115
	v_div_scale_f32 v116, vcc, 1.0, v112, 1.0
	v_mul_f32_e32 v117, v116, v115
	v_fma_f32 v119, -v113, v117, v116
	v_fmac_f32_e32 v117, v119, v115
	v_fma_f32 v113, -v113, v117, v116
	v_div_fmas_f32 v113, v113, v115, v117
	s_waitcnt vmcnt(18)
	v_lshlrev_b32_e32 v115, 16, v94
	v_mul_f32_e32 v116, 0xbfb8aa3b, v115
	v_exp_f32_e32 v116, v116
	v_div_fixup_f32 v112, v113, v112, 1.0
	v_mul_f32_e32 v112, 0x41000000, v112
	v_mul_f32_e32 v113, v118, v112
	v_add_f32_e32 v116, 1.0, v116
	v_div_scale_f32 v117, s[4:5], v116, v116, v115
	v_rcp_f32_e32 v118, v117
	v_lshlrev_b32_e32 v119, 16, v90
	v_fma_f32 v102, v144, v119, v102
	v_and_b32_e32 v94, 0xffff0000, v94
	v_fma_f32 v119, -v117, v118, 1.0
	v_fmac_f32_e32 v118, v119, v118
	v_div_scale_f32 v119, vcc, v115, v116, v115
	v_mul_f32_e32 v120, v119, v118
	v_fma_f32 v121, -v117, v120, v119
	v_fmac_f32_e32 v120, v121, v118
	v_fma_f32 v117, -v117, v120, v119
	v_mul_f32_e32 v119, 0xbfb8aa3b, v94
	v_exp_f32_e32 v119, v119
	v_div_fmas_f32 v117, v117, v118, v120
	v_div_fixup_f32 v115, v117, v116, v115
	v_and_b32_e32 v90, 0xffff0000, v90
	v_add_f32_e32 v116, 1.0, v119
	v_div_scale_f32 v117, s[4:5], v116, v116, v94
	v_rcp_f32_e32 v118, v117
	v_fma_f32 v90, v144, v90, v103
	v_mul_f32_e32 v102, v102, v115
	v_mul_f32_e32 v113, v22, v113
	v_fma_f32 v103, -v117, v118, 1.0
	v_fmac_f32_e32 v118, v103, v118
	v_div_scale_f32 v103, vcc, v94, v116, v94
	v_mul_f32_e32 v115, v103, v118
	v_fma_f32 v119, -v117, v115, v103
	v_fmac_f32_e32 v115, v119, v118
	v_fma_f32 v103, -v117, v115, v103
	v_lshlrev_b32_e32 v117, 16, v95
	v_mul_f32_e32 v119, 0xbfb8aa3b, v117
	v_exp_f32_e32 v119, v119
	v_div_fmas_f32 v103, v103, v118, v115
	v_div_fixup_f32 v94, v103, v116, v94
	v_mul_f32_e32 v90, v90, v94
	v_add_f32_e32 v103, 1.0, v119
	v_div_scale_f32 v115, s[4:5], v103, v103, v117
	v_rcp_f32_e32 v116, v115
	v_lshlrev_b32_e32 v94, 16, v91
	v_fma_f32 v94, v144, v94, v104
	v_and_b32_e32 v95, 0xffff0000, v95
	v_fma_f32 v104, -v115, v116, 1.0
	v_fmac_f32_e32 v116, v104, v116
	v_div_scale_f32 v104, vcc, v117, v103, v117
	v_mul_f32_e32 v118, v104, v116
	v_fma_f32 v119, -v115, v118, v104
	v_fmac_f32_e32 v118, v119, v116
	v_fma_f32 v104, -v115, v118, v104
	v_mul_f32_e32 v115, 0xbfb8aa3b, v95
	v_exp_f32_e32 v115, v115
	v_div_fmas_f32 v104, v104, v116, v118
	v_div_fixup_f32 v103, v104, v103, v117
	v_and_b32_e32 v91, 0xffff0000, v91
	v_add_f32_e32 v104, 1.0, v115
	v_div_scale_f32 v115, s[4:5], v104, v104, v95
	v_rcp_f32_e32 v116, v115
	v_fmac_f32_e32 v105, v144, v91
	v_mul_f32_e32 v94, v94, v103
	v_fma_f32 v91, -v115, v116, 1.0
	v_fmac_f32_e32 v116, v91, v116
	v_div_scale_f32 v91, vcc, v95, v104, v95
	v_mul_f32_e32 v103, v91, v116
	v_fma_f32 v117, -v115, v103, v91
	v_fmac_f32_e32 v103, v117, v116
	v_fma_f32 v91, -v115, v103, v91
	v_lshlrev_b32_e32 v115, 16, v96
	v_mul_f32_e32 v117, 0xbfb8aa3b, v115
	v_exp_f32_e32 v117, v117
	v_div_fmas_f32 v91, v91, v116, v103
	v_div_fixup_f32 v91, v91, v104, v95
	v_mul_f32_e32 v91, v105, v91
	v_add_f32_e32 v95, 1.0, v117
	v_div_scale_f32 v103, s[4:5], v95, v95, v115
	v_rcp_f32_e32 v104, v103
	v_lshlrev_b32_e32 v105, 16, v92
	v_fma_f32 v86, v144, v105, v86
	v_and_b32_e32 v96, 0xffff0000, v96
	v_fma_f32 v105, -v103, v104, 1.0
	v_fmac_f32_e32 v104, v105, v104
	v_div_scale_f32 v105, vcc, v115, v95, v115
	v_mul_f32_e32 v116, v105, v104
	v_fma_f32 v117, -v103, v116, v105
	v_fmac_f32_e32 v116, v117, v104
	v_fma_f32 v103, -v103, v116, v105
	v_mul_f32_e32 v105, 0xbfb8aa3b, v96
	v_exp_f32_e32 v105, v105
	v_div_fmas_f32 v103, v103, v104, v116
	v_div_fixup_f32 v95, v103, v95, v115
	v_mul_f32_e32 v95, v86, v95
	v_add_f32_e32 v103, 1.0, v105
	v_div_scale_f32 v104, s[4:5], v103, v103, v96
	v_rcp_f32_e32 v105, v104
	v_and_b32_e32 v86, 0xffff0000, v92
	v_fma_f32 v86, v144, v86, v87
	v_fma_f32 v87, -v104, v105, 1.0
	v_fmac_f32_e32 v105, v87, v105
	v_div_scale_f32 v87, vcc, v96, v103, v96
	v_mul_f32_e32 v92, v87, v105
	v_fma_f32 v115, -v104, v92, v87
	v_fmac_f32_e32 v92, v115, v105
	v_fma_f32 v87, -v104, v92, v87
	v_lshlrev_b32_e32 v104, 16, v97
	v_mul_f32_e32 v115, 0xbfb8aa3b, v104
	v_exp_f32_e32 v115, v115
	v_div_fmas_f32 v87, v87, v105, v92
	v_div_fixup_f32 v87, v87, v103, v96
	v_mul_f32_e32 v105, v86, v87
	v_add_f32_e32 v92, 1.0, v115
	v_div_scale_f32 v96, s[4:5], v92, v92, v104
	v_rcp_f32_e32 v103, v96
	v_lshlrev_b32_e32 v86, 16, v93
	v_fma_f32 v86, v144, v86, v88
	v_fma_f32 v87, -v96, v103, 1.0
	v_fmac_f32_e32 v103, v87, v103
	v_div_scale_f32 v87, vcc, v104, v92, v104
	v_mul_f32_e32 v88, v87, v103
	v_fma_f32 v115, -v96, v88, v87
	v_fmac_f32_e32 v88, v115, v103
	v_fma_f32 v87, -v96, v88, v87
	v_and_b32_e32 v96, 0xffff0000, v97
	v_mul_f32_e32 v97, 0xbfb8aa3b, v96
	v_exp_f32_e32 v97, v97
	v_div_fmas_f32 v87, v87, v103, v88
	v_div_fixup_f32 v87, v87, v92, v104
	v_mul_f32_e32 v103, v86, v87
	v_add_f32_e32 v88, 1.0, v97
	v_div_scale_f32 v92, s[4:5], v88, v88, v96
	v_rcp_f32_e32 v97, v92
	v_and_b32_e32 v86, 0xffff0000, v93
	v_fmac_f32_e32 v89, v144, v86
	v_fma_f32 v86, -v92, v97, 1.0
	v_fmac_f32_e32 v97, v86, v97
	v_div_scale_f32 v86, vcc, v96, v88, v96
	v_mul_f32_e32 v87, v86, v97
	v_fma_f32 v93, -v92, v87, v86
	v_fmac_f32_e32 v87, v93, v97
	v_fma_f32 v86, -v92, v87, v86
	v_div_fmas_f32 v86, v86, v97, v87
	v_div_fixup_f32 v86, v86, v88, v96
	v_mul_f32_e32 v89, v89, v86
	v_mul_f32_e32 v86, v90, v90
	v_fmac_f32_e32 v86, v102, v102
	v_fmac_f32_e32 v86, v94, v94
	v_fmac_f32_e32 v86, v91, v91
	v_fmac_f32_e32 v86, v95, v95
	v_fmac_f32_e32 v86, v105, v105
	v_fmac_f32_e32 v86, v103, v103
	v_fmac_f32_e32 v86, v89, v89
	ds_bpermute_b32 v87, v1, v86
	v_mul_f32_e32 v88, v110, v112
	v_mul_f32_e32 v88, v23, v88
	v_mul_f32_e32 v93, v111, v112
	v_mul_f32_e32 v93, v25, v93
	s_waitcnt lgkmcnt(0)
; __device__ __forceinline__ float bflo(unsigned w) { return __uint_as_float(w << 16); }
; __device__ __forceinline__ float bfhi(unsigned w) { return __uint_as_float(w & 0xffff0000u); }
; __device__ __forceinline__ float siluf(float a) { return a / (1.0f + __expf(-a)); }
; __device__ __forceinline__ void p5_put8(const P5In& I, size_t off, const float (&v)[8], float r, const f32x4& g0, const f32x4& g1) {
;     ...
;     const float r8 = r * pg8::A8_SCALE; v2u o; o.x = pg8::pk4_fp8(v[0] * r8 * g0[0], v[1] * r8 * g0[1], v[2] * r8 * g0[2], v[3] * r8 * g0[3]); o.y = pg8::pk4_fp8(v[4] * r8 * g1[0], v[5] * r8 * g1[1], v[6] * r8 * g1[2], v[7] * r8 * g1[3]);
;     *(v2u*)(I.y + off) = o;
; __device__ __forceinline__ void p5_item(const P5Row& R, const P5In& I, const P5Par& P, int t, int lane) {
;     ...
;     for (int g = 0; g < 2; ++g) { const int ch = g * 512 + 8 * lane;
;         const f32x4 y0 = R.ya[g], y1 = R.yb[g]; const v4u xv = R.xr[g], zv = R.zr[g];
;         const float D = P.D[g];
;         float v[8];
;         v[0] = (y0[0] + D * bflo(xv.x)) * siluf(bflo(zv.x)); v[1] = (y0[1] + D * bfhi(xv.x)) * siluf(bfhi(zv.x));
;         v[2] = (y0[2] + D * bflo(xv.y)) * siluf(bflo(zv.y)); v[3] = (y0[3] + D * bfhi(xv.y)) * siluf(bfhi(zv.y));
;         v[4] = (y1[0] + D * bflo(xv.z)) * siluf(bflo(zv.z)); v[5] = (y1[1] + D * bfhi(xv.z)) * siluf(bfhi(zv.z));
;         v[6] = (y1[2] + D * bflo(xv.w)) * siluf(bflo(zv.w)); v[7] = (y1[3] + D * bfhi(xv.w)) * siluf(bfhi(zv.w));
;         float s = 0.f;
; #pragma unroll
;         for (int i = 0; i < 8; ++i) s += v[i] * v[i];
;         s = wave_sum(s); const float r = 1.0f / sqrtf(s * (1.0f / 512.0f) + EPSF);
;         p5_put8(I, (size_t)t * DM + ch, v, r, P.gs[g][0], P.gs[g][1]); }
;     { const int ch = 8 * lane; const v4u r4 = R.m4;
;       float v[8] = {bflo(r4.x), bfhi(r4.x), bflo(r4.y), bfhi(r4.y), bflo(r4.z), bfhi(r4.z), bflo(r4.w), bfhi(r4.w)}; float s = 0.f;
; #pragma unroll
;       for (int i = 0; i < 8; ++i) s += v[i] * v[i];
;       s += __shfl_xor(s, 1); s += __shfl_xor(s, 2); s += __shfl_xor(s, 4);
;       const float r = 1.0f / sqrtf(s * (1.0f / 64.0f) + EPSF);
;       p5_put8(I, (size_t)t * DM + 1024 + ch, v, r, P.gm[0], P.gm[1]); }
	v_add_f32_e32 v86, v86, v87
	ds_bpermute_b32 v87, v138, v86
	v_med3_f32 v96, v113, s25, v150
	v_med3_f32 v88, v88, s25, v150
	v_mul_f32_e32 v92, v114, v112
	v_mul_f32_e32 v92, v24, v92
	s_waitcnt lgkmcnt(0)
	v_add_f32_e32 v87, v86, v87
	ds_bpermute_b32 v97, v139, v87
	v_mov_b32_e32 v86, 0
	v_cvt_pk_fp8_f32 v86, v96, v88
	v_med3_f32 v88, v93, s25, v150
	v_med3_f32 v92, v92, s25, v150
	s_waitcnt lgkmcnt(0)
	v_add_f32_e32 v87, v87, v97
	ds_bpermute_b32 v93, v140, v87
	v_cvt_pk_fp8_f32 v86, v92, v88 op_sel:[0,0,1]
	v_mul_f32_e32 v88, v106, v112
	v_mul_f32_e32 v92, v107, v112
	v_mul_f32_e32 v88, v30, v88
	s_waitcnt lgkmcnt(0)
	v_add_f32_e32 v87, v87, v93
	ds_bpermute_b32 v93, v141, v87
	v_mul_f32_e32 v92, v31, v92
	v_med3_f32 v88, v88, s25, v150
	v_med3_f32 v92, v92, s25, v150
	v_mul_f32_e32 v96, v108, v112
	s_waitcnt lgkmcnt(0)
	v_add_f32_e32 v87, v87, v93
	ds_bpermute_b32 v93, v142, v87
	v_mul_f32_e32 v97, v109, v112
	v_mul_f32_e32 v96, v32, v96
	v_mul_f32_e32 v97, v33, v97
	v_med3_f32 v96, v96, s25, v150
	s_waitcnt lgkmcnt(0)
	v_add_f32_e32 v87, v87, v93
	v_fmamk_f32 v87, v87, 0x3b000000, v146
	v_mul_f32_e32 v93, 0x4f800000, v87
	v_cmp_gt_f32_e32 vcc, s24, v87
	v_med3_f32 v97, v97, s25, v150
	s_nop 0
	v_cndmask_b32_e32 v93, v87, v93, vcc
	v_sqrt_f32_e32 v104, v93
	v_mov_b32_e32 v87, 0
	v_cvt_pk_fp8_f32 v87, v88, v92
	v_add_u32_e32 v88, -1, v104
	v_fma_f32 v92, -v88, v104, v93
	v_cmp_ge_f32_e64 s[4:5], 0, v92
	v_add_u32_e32 v92, 1, v104
	v_cvt_pk_fp8_f32 v87, v96, v97 op_sel:[0,0,1]
	v_cndmask_b32_e64 v88, v104, v88, s[4:5]
	v_fma_f32 v104, -v92, v104, v93
	v_cmp_lt_f32_e64 s[4:5], 0, v104
	s_nop 1
	v_cndmask_b32_e64 v88, v88, v92, s[4:5]
	v_mul_f32_e32 v92, 0x37800000, v88
	v_cndmask_b32_e32 v88, v88, v92, vcc
	v_cmp_class_f32_e32 vcc, v93, v147
	s_nop 1
	v_cndmask_b32_e32 v88, v88, v93, vcc
	v_div_scale_f32 v92, s[4:5], v88, v88, 1.0
	v_rcp_f32_e32 v93, v92
	s_nop 0
	v_fma_f32 v96, -v92, v93, 1.0
	v_fmac_f32_e32 v93, v96, v93
	v_div_scale_f32 v96, vcc, 1.0, v88, 1.0
	v_mul_f32_e32 v97, v96, v93
	v_fma_f32 v104, -v92, v97, v96
	v_fmac_f32_e32 v97, v104, v93
	v_fma_f32 v92, -v92, v97, v96
	v_div_fmas_f32 v92, v92, v93, v97
	v_div_fixup_f32 v88, v92, v88, 1.0
	v_mul_f32_e32 v92, 0x41000000, v88
	v_mul_f32_e32 v88, v102, v92
	v_mul_f32_e32 v90, v90, v92
	v_mul_f32_e32 v88, v10, v88
	v_mul_f32_e32 v90, v11, v90
	v_mul_f32_e32 v93, v94, v92
	v_med3_f32 v94, v88, s25, v150
	v_med3_f32 v90, v90, s25, v150
	v_mov_b32_e32 v88, 0
	v_cvt_pk_fp8_f32 v88, v94, v90
	v_mul_f32_e32 v91, v91, v92
	v_mul_f32_e32 v93, v12, v93
	v_mul_f32_e32 v90, v13, v91
	v_med3_f32 v91, v93, s25, v150
	v_med3_f32 v90, v90, s25, v150
	v_cvt_pk_fp8_f32 v88, v91, v90 op_sel:[0,0,1]
	s_waitcnt vmcnt(17)
	v_and_b32_e32 v91, 0xffff0000, v70
	v_lshlrev_b32_e32 v90, 16, v70
	v_mul_f32_e32 v70, v91, v91
	v_lshlrev_b32_e32 v93, 16, v71
	v_fmac_f32_e32 v70, v90, v90
	v_and_b32_e32 v94, 0xffff0000, v71
	v_fmac_f32_e32 v70, v93, v93
	v_lshlrev_b32_e32 v96, 16, v72
	v_fmac_f32_e32 v70, v94, v94
	v_and_b32_e32 v72, 0xffff0000, v72
	v_fmac_f32_e32 v70, v96, v96
	v_lshlrev_b32_e32 v97, 16, v73
	v_fmac_f32_e32 v70, v72, v72
	v_and_b32_e32 v73, 0xffff0000, v73
	v_fmac_f32_e32 v70, v97, v97
	v_fmac_f32_e32 v70, v73, v73
	ds_bpermute_b32 v71, v1, v70
	v_mul_f32_e32 v95, v95, v92
	v_mul_f32_e32 v102, v105, v92
	v_mul_f32_e32 v95, v14, v95
	v_mul_f32_e32 v102, v15, v102
	s_waitcnt lgkmcnt(0)
	v_add_f32_e32 v70, v70, v71
	ds_bpermute_b32 v71, v138, v70
	v_mul_f32_e32 v89, v89, v92
	v_mul_f32_e32 v103, v103, v92
	v_mul_f32_e32 v92, v17, v89
	v_med3_f32 v95, v95, s25, v150
	s_waitcnt lgkmcnt(0)
	v_add_f32_e32 v70, v70, v71
	ds_bpermute_b32 v71, v139, v70
	v_med3_f32 v102, v102, s25, v150
	v_mov_b32_e32 v89, 0
	v_cvt_pk_fp8_f32 v89, v95, v102
	v_mul_f32_e32 v103, v16, v103
	s_waitcnt lgkmcnt(0)
	v_add_f32_e32 v70, v70, v71
	v_fmamk_f32 v70, v70, 0x3c800000, v146
	v_mul_f32_e32 v71, 0x4f800000, v70
	v_cmp_gt_f32_e32 vcc, s24, v70
	v_med3_f32 v95, v103, s25, v150
	v_med3_f32 v92, v92, s25, v150
	v_cndmask_b32_e32 v70, v70, v71, vcc
	v_sqrt_f32_e32 v71, v70
	v_cvt_pk_fp8_f32 v89, v95, v92 op_sel:[0,0,1]
	v_add_u32_e32 v92, -1, v71
	v_fma_f32 v95, -v92, v71, v70
	v_cmp_ge_f32_e64 s[4:5], 0, v95
	v_add_u32_e32 v95, 1, v71
	s_nop 0
	v_cndmask_b32_e64 v92, v71, v92, s[4:5]
	v_fma_f32 v71, -v95, v71, v70
	v_cmp_lt_f32_e64 s[4:5], 0, v71
	s_nop 1
	v_cndmask_b32_e64 v71, v92, v95, s[4:5]
	v_mul_f32_e32 v92, 0x37800000, v71
	v_cndmask_b32_e32 v71, v71, v92, vcc
	v_cmp_class_f32_e32 vcc, v70, v147
	s_nop 1
	v_cndmask_b32_e32 v92, v71, v70, vcc
	v_div_scale_f32 v95, s[4:5], v92, v92, 1.0
	v_rcp_f32_e32 v102, v95
	v_lshl_add_u64 v[70:71], s[8:9], 0, v[122:123]
	global_store_dwordx2 v[70:71], v[86:87], off
	global_store_dwordx2 v[70:71], v[88:89], off offset:512
	v_fma_f32 v86, -v95, v102, 1.0
	v_fmac_f32_e32 v102, v86, v102
	v_div_scale_f32 v86, vcc, 1.0, v92, 1.0
	v_mul_f32_e32 v87, v86, v102
	v_fma_f32 v88, -v95, v87, v86
	v_fmac_f32_e32 v87, v88, v102
	v_fma_f32 v86, -v95, v87, v86
	v_div_fmas_f32 v86, v86, v102, v87
	v_div_fixup_f32 v86, v86, v92, 1.0
	v_mul_f32_e32 v86, 0x41000000, v86
	v_mul_f32_e32 v88, v86, v91
	s_waitcnt vmcnt(18)
; __device__ __forceinline__ float bflo(unsigned w) { return __uint_as_float(w << 16); }
; __device__ __forceinline__ float bfhi(unsigned w) { return __uint_as_float(w & 0xffff0000u); }
; __device__ __forceinline__ void p5_item(const P5Row& R, const P5In& I, const P5Par& P, int t, int lane) {
;     ...
;     { const int h = lane >> 4, d = 8 * (lane & 15); const v4u a4 = R.a4, b4 = R.b4; const float lam = P.lam;
;       float v[8] = {bflo(a4.x) - lam * bflo(b4.x), bfhi(a4.x) - lam * bfhi(b4.x), bflo(a4.y) - lam * bflo(b4.y), bfhi(a4.y) - lam * bfhi(b4.y),
;                     bflo(a4.z) - lam * bflo(b4.z), bfhi(a4.z) - lam * bfhi(b4.z), bflo(a4.w) - lam * bflo(b4.w), bfhi(a4.w) - lam * bfhi(b4.w)}; float s = 0.f;
; #pragma unroll
;       for (int i = 0; i < 8; ++i) s += v[i] * v[i];
;       s += __shfl_xor(s, 1); s += __shfl_xor(s, 2); s += __shfl_xor(s, 4); s += __shfl_xor(s, 8);
;       const float r = (1.0f - I.lambda_init) / sqrtf(s * (1.0f / 128.0f) + EPSF);
;       p5_put8(I, (size_t)t * DM + 1536 + h * 128 + d, v, r, P.gd[0], P.gd[1]); }
; __device__ __forceinline__ void p5_finalize(const Ctx& X, const P5In& I) {
;     ...
;     for (int t = X.gw; t < NTOK; t += 2 * X.ngw) { const int t1 = t + X.ngw, t2 = t + 2 * X.ngw;
;         p5_load(B, I, t1 < NTOK ? t1 : NTOK - 1, X.lane);
;         p5_item(A, I, P, t, X.lane);
;         p5_load(A, I, t2 < NTOK ? t2 : NTOK - 1, X.lane);
;         if (t1 < NTOK) p5_item(B, I, P, t1, X.lane); }
	v_lshlrev_b32_e32 v91, 16, v62
	s_waitcnt vmcnt(17)
	v_lshlrev_b32_e32 v92, 16, v66
	v_and_b32_e32 v62, 0xffff0000, v62
	v_and_b32_e32 v66, 0xffff0000, v66
	v_fma_f32 v91, -v145, v92, v91
	v_fma_f32 v66, -v145, v66, v62
	v_lshlrev_b32_e32 v62, 16, v63
	v_lshlrev_b32_e32 v92, 16, v67
	v_fma_f32 v92, -v145, v92, v62
	v_and_b32_e32 v62, 0xffff0000, v63
	v_and_b32_e32 v63, 0xffff0000, v67
	v_fma_f32 v67, -v145, v63, v62
	v_lshlrev_b32_e32 v62, 16, v64
	v_lshlrev_b32_e32 v63, 16, v68
	v_mul_f32_e32 v89, v86, v93
	v_fma_f32 v93, -v145, v63, v62
	v_and_b32_e32 v62, 0xffff0000, v64
	v_and_b32_e32 v63, 0xffff0000, v68
	v_fma_f32 v68, -v145, v63, v62
	v_lshlrev_b32_e32 v62, 16, v65
	v_lshlrev_b32_e32 v63, 16, v69
	v_mul_f32_e32 v87, v86, v90
	v_mul_f32_e32 v90, v86, v94
	v_fma_f32 v94, -v145, v63, v62
	v_and_b32_e32 v62, 0xffff0000, v65
	v_and_b32_e32 v63, 0xffff0000, v69
	v_fma_f32 v65, -v145, v63, v62
	v_mul_f32_e32 v63, v66, v66
	v_fmac_f32_e32 v63, v91, v91
	v_fmac_f32_e32 v63, v92, v92
	v_fmac_f32_e32 v63, v67, v67
	v_fmac_f32_e32 v63, v93, v93
	v_fmac_f32_e32 v63, v68, v68
	v_fmac_f32_e32 v63, v94, v94
	v_fmac_f32_e32 v63, v65, v65
	ds_bpermute_b32 v64, v1, v63
	v_mul_f32_e32 v87, v18, v87
	v_mul_f32_e32 v88, v19, v88
	v_med3_f32 v69, v87, s25, v150
	v_med3_f32 v87, v88, s25, v150
	s_waitcnt lgkmcnt(0)
	v_add_f32_e32 v63, v63, v64
	ds_bpermute_b32 v64, v138, v63
	v_mov_b32_e32 v62, 0
	v_cvt_pk_fp8_f32 v62, v69, v87
	v_mul_f32_e32 v89, v20, v89
	v_mul_f32_e32 v90, v21, v90
	s_waitcnt lgkmcnt(0)
	v_add_f32_e32 v63, v63, v64
	ds_bpermute_b32 v64, v139, v63
	v_med3_f32 v69, v89, s25, v150
	v_med3_f32 v87, v90, s25, v150
	v_cvt_pk_fp8_f32 v62, v69, v87 op_sel:[0,0,1]
	v_mul_f32_e32 v69, v86, v96
	s_waitcnt lgkmcnt(0)
	v_add_f32_e32 v63, v63, v64
	ds_bpermute_b32 v64, v140, v63
	v_mul_f32_e32 v72, v86, v72
	v_mul_f32_e32 v87, v86, v97
	v_mul_f32_e32 v73, v86, v73
	v_mul_f32_e32 v69, v26, v69
	s_waitcnt lgkmcnt(0)
	v_add_f32_e32 v63, v63, v64
	v_fmamk_f32 v63, v63, 0x3c000000, v146
	v_mul_f32_e32 v64, 0x4f800000, v63
	v_cmp_gt_f32_e32 vcc, s24, v63
	v_mul_f32_e32 v72, v27, v72
	v_med3_f32 v69, v69, s25, v150
	v_cndmask_b32_e32 v64, v63, v64, vcc
	v_sqrt_f32_e32 v86, v64
	v_med3_f32 v72, v72, s25, v150
	v_mov_b32_e32 v63, 0
	v_cvt_pk_fp8_f32 v63, v69, v72
	v_add_u32_e32 v69, -1, v86
	v_fma_f32 v72, -v69, v86, v64
	v_cmp_ge_f32_e64 s[4:5], 0, v72
	v_add_u32_e32 v72, 1, v86
	v_mul_f32_e32 v87, v28, v87
	v_cndmask_b32_e64 v69, v86, v69, s[4:5]
	v_fma_f32 v86, -v72, v86, v64
	v_cmp_lt_f32_e64 s[4:5], 0, v86
	v_mul_f32_e32 v73, v29, v73
	v_med3_f32 v86, v87, s25, v150
	v_cndmask_b32_e64 v69, v69, v72, s[4:5]
	v_mul_f32_e32 v72, 0x37800000, v69
	v_cndmask_b32_e32 v69, v69, v72, vcc
	v_cmp_class_f32_e32 vcc, v64, v147
	v_med3_f32 v73, v73, s25, v150
	v_cvt_pk_fp8_f32 v63, v86, v73 op_sel:[0,0,1]
	v_cndmask_b32_e32 v64, v69, v64, vcc
	v_div_scale_f32 v69, s[4:5], v64, v64, s26
	v_rcp_f32_e32 v72, v69
	global_store_dwordx2 v[70:71], v[62:63], off offset:1024
	v_lshl_add_u64 v[62:63], s[8:9], 0, v[128:129]
	v_lshl_add_u64 v[62:63], v[62:63], 0, v[124:125]
	v_fma_f32 v73, -v69, v72, 1.0
	v_fmac_f32_e32 v72, v73, v72
	v_div_scale_f32 v73, vcc, s26, v64, s26
	v_mul_f32_e32 v86, v73, v72
	v_fma_f32 v87, -v69, v86, v73
	v_fmac_f32_e32 v86, v87, v72
	v_fma_f32 v69, -v69, v86, v73
	v_div_fmas_f32 v69, v69, v72, v86
	v_div_fixup_f32 v64, v69, v64, s26
	v_mul_f32_e32 v69, 0x41000000, v64
	v_mul_f32_e32 v64, v91, v69
	v_mul_f32_e32 v66, v66, v69
	v_mul_f32_e32 v64, v2, v64
	v_mul_f32_e32 v66, v3, v66
	v_med3_f32 v73, v64, s25, v150
	v_med3_f32 v66, v66, s25, v150
	v_mov_b32_e32 v64, 0
	v_cvt_pk_fp8_f32 v64, v73, v66
	v_mul_f32_e32 v72, v92, v69
	v_mul_f32_e32 v67, v67, v69
	v_mul_f32_e32 v72, v4, v72
	v_mul_f32_e32 v66, v5, v67
	v_med3_f32 v67, v72, s25, v150
	v_med3_f32 v66, v66, s25, v150
	v_cvt_pk_fp8_f32 v64, v67, v66 op_sel:[0,0,1]
	v_mul_f32_e32 v66, v93, v69
	v_mul_f32_e32 v67, v68, v69
	v_mul_f32_e32 v66, v6, v66
	v_mul_f32_e32 v67, v7, v67
	v_mul_f32_e32 v68, v94, v69
	v_mul_f32_e32 v69, v65, v69
	v_med3_f32 v66, v66, s25, v150
	v_med3_f32 v67, v67, s25, v150
	v_mov_b32_e32 v65, 0
	v_cvt_pk_fp8_f32 v65, v66, v67
	v_mul_f32_e32 v68, v8, v68
	v_mul_f32_e32 v66, v9, v69
	v_med3_f32 v67, v68, s25, v150
	v_med3_f32 v66, v66, s25, v150
	v_cvt_pk_fp8_f32 v65, v67, v66 op_sel:[0,0,1]
	global_store_dwordx2 v[62:63], v[64:65], off offset:1536
	s_branch .LBB0_1774
.Lfin_skip0:
	s_waitcnt vmcnt(0)
	s_branch .LBB0_1774

; #define REPS(P) for (int rep_ = 0; rep_ < ((P) == PROBE_REP ? 2 : 1); ++rep_)
; #define REPBAR() do { if (rep_) GRID_BAR(); } while (0)
; __device__ __forceinline__ void p5_finalize(const Ctx& X, const P5In& I) {
;     P5Par P;
;     { const float a = wave_sum(I.lamp[X.lane] * I.lamp[64 + X.lane]), b = wave_sum(I.lamp[128 + X.lane] * I.lamp[192 + X.lane]); P.lam = __expf(a) - __expf(b) + I.lambda_init; }
; template <int l>
; __device__ __forceinline__ void layer_body(unsigned char* lds_raw, const Args& args, const XcdBarrier& bar, const int lo, const int hi) {
;     ...
;         if (IN(pb + 6)) REPS(pb + 6) { REPBAR(); const Ctx X = make_ctx(lds_raw);
;             P5In I{YRAW, XC, PROJ, MOBA, DIFF, (const float*)args.in[12] + l * 16, (const float*)args.in[13] + (size_t)l * 1024, (const float*)args.in[14] + (size_t)l * 512,
.LBB0_3408:
	s_cmp_lt_i32 s40, 19
	s_cselect_b64 s[0:1], -1, 0
	s_and_b64 s[4:5], s[0:1], s[4:5]
	s_andn2_b64 vcc, exec, s[4:5]
	s_cbranch_vccnz .LBB0_3414
	s_waitcnt lgkmcnt(0)
	v_readlane_b32 s44, v254, 60
	v_mov_b32_e32 v1, v0
	v_readlane_b32 s52, v255, 4
	v_readlane_b32 s53, v255, 5
	v_readlane_b32 s54, v255, 6
	s_waitcnt vmcnt(0)
	v_and_b32_e32 v34, 63, v1
	v_readlane_b32 s55, v255, 7
	v_readlane_b32 s56, v255, 8
	v_readlane_b32 s57, v255, 9
	v_readlane_b32 s58, v255, 10
	v_readlane_b32 s59, v255, 11
	s_mov_b64 s[8:9], s[52:53]
	v_lshlrev_b32_e32 v2, 2, v34
	s_mov_b64 s[14:15], s[58:59]
	global_load_dword v3, v2, s[14:15] offset:1024
	global_load_dword v4, v2, s[14:15] offset:1280
	global_load_dword v5, v2, s[14:15] offset:1536
	global_load_dword v6, v2, s[14:15] offset:1792
	v_mbcnt_lo_u32_b32 v2, -1, 0
	v_mbcnt_hi_u32_b32 v2, -1, v2
	v_readfirstlane_b32 s5, v1
	v_and_b32_e32 v1, 64, v2
	v_xor_b32_e32 v7, 1, v2
	v_add_u32_e32 v13, 64, v1
	v_cmp_lt_i32_e32 vcc, v7, v13
	v_xor_b32_e32 v8, 2, v2
	v_xor_b32_e32 v9, 4, v2
	v_cndmask_b32_e32 v1, v2, v7, vcc
	v_lshlrev_b32_e32 v1, 2, v1
	v_cmp_lt_i32_e32 vcc, v8, v13
	v_xor_b32_e32 v10, 8, v2
	v_xor_b32_e32 v11, 16, v2
	v_cndmask_b32_e32 v8, v2, v8, vcc
	v_lshlrev_b32_e32 v138, 2, v8
	v_cmp_lt_i32_e32 vcc, v9, v13
	v_xor_b32_e32 v12, 32, v2
	s_lshl_b32 s4, s2, 3
	s_ashr_i32 s5, s5, 6
	s_add_i32 s4, s5, s4
	s_cmpk_gt_i32 s4, 0x1fff
	v_readlane_b32 s45, v254, 61
	v_readlane_b32 s46, v254, 62
	v_readlane_b32 s47, v254, 63
	v_readlane_b32 s48, v255, 0
	v_readlane_b32 s49, v255, 1
	v_readlane_b32 s50, v255, 2
	v_readlane_b32 s51, v255, 3
	s_mov_b64 s[10:11], s[54:55]
	s_mov_b64 s[12:13], s[56:57]
	s_waitcnt vmcnt(2)
	v_mul_f32_e32 v7, v3, v4
	ds_bpermute_b32 v7, v1, v7
	s_waitcnt vmcnt(0)
	v_mul_f32_e32 v14, v5, v6
	ds_bpermute_b32 v14, v1, v14
	s_waitcnt lgkmcnt(1)
	v_fmac_f32_e32 v7, v3, v4
	ds_bpermute_b32 v3, v138, v7
	s_waitcnt lgkmcnt(1)
	v_fmac_f32_e32 v14, v5, v6
	ds_bpermute_b32 v4, v138, v14
	v_cndmask_b32_e32 v5, v2, v9, vcc
	v_lshlrev_b32_e32 v139, 2, v5
	s_waitcnt lgkmcnt(1)
	v_add_f32_e32 v3, v7, v3
	ds_bpermute_b32 v5, v139, v3
	s_waitcnt lgkmcnt(1)
	v_add_f32_e32 v4, v14, v4
	ds_bpermute_b32 v6, v139, v4
	v_cmp_lt_i32_e32 vcc, v10, v13
	s_waitcnt lgkmcnt(1)
	v_add_f32_e32 v3, v3, v5
	v_cndmask_b32_e32 v7, v2, v10, vcc
	v_lshlrev_b32_e32 v140, 2, v7
	s_waitcnt lgkmcnt(0)
	v_add_f32_e32 v4, v4, v6
	ds_bpermute_b32 v5, v140, v3
	ds_bpermute_b32 v6, v140, v4
	v_cmp_lt_i32_e32 vcc, v11, v13
	s_waitcnt lgkmcnt(1)
	v_add_f32_e32 v3, v3, v5
	v_cndmask_b32_e32 v7, v2, v11, vcc
	v_lshlrev_b32_e32 v141, 2, v7
	s_waitcnt lgkmcnt(0)
	v_add_f32_e32 v4, v4, v6
	ds_bpermute_b32 v5, v141, v3
	ds_bpermute_b32 v6, v141, v4
	v_cmp_lt_i32_e32 vcc, v12, v13
	s_waitcnt lgkmcnt(1)
	v_add_f32_e32 v63, v3, v5
	v_cndmask_b32_e32 v2, v2, v12, vcc
	v_lshlrev_b32_e32 v142, 2, v2
	s_waitcnt lgkmcnt(0)
	v_add_f32_e32 v62, v4, v6
	ds_bpermute_b32 v65, v142, v63
	ds_bpermute_b32 v64, v142, v62
	s_cbranch_scc1 .LBB0_3414
; __device__ __forceinline__ void p5_load(P5Row& R, const P5In& I, int t, int lane) {
; #pragma unroll
;     for (int g = 0; g < 2; ++g) { const int ch = g * 512 + 8 * lane;
;         R.ya[g] = *(const f32x4*)(I.yraw + (size_t)t * 1024 + ch); R.yb[g] = *(const f32x4*)(I.yraw + (size_t)t * 1024 + ch + 4);
;         R.xr[g] = *(const v4u*)(I.xc + (size_t)t * 1536 + ch); R.zr[g] = *(const v4u*)(I.proj + (size_t)t * NPROJ + C_Z + ch); }
;     R.m4 = *(const v4u*)(I.moba + (size_t)t * 512 + 8 * lane);
;     const int dh = lane >> 4, dd = 8 * (lane & 15);
;     R.a4 = *(const v4u*)(I.diff + (size_t)t * 1024 + (dh * 2 + 0) * 128 + dd); R.b4 = *(const v4u*)(I.diff + (size_t)t * 1024 + (dh * 2 + 1) * 128 + dd);
; }
; __device__ __forceinline__ void p5_finalize(const Ctx& X, const P5In& I) {
;     ...
;     { const float a = wave_sum(I.lamp[X.lane] * I.lamp[64 + X.lane]), b = wave_sum(I.lamp[128 + X.lane] * I.lamp[192 + X.lane]); P.lam = __expf(a) - __expf(b) + I.lambda_init; }
; #pragma unroll
;     for (int g = 0; g < 2; ++g) { const int ch = g * 512 + 8 * X.lane; P.D[g] = I.d_skip[ch >> 6]; P.gs[g][0] = *(const f32x4*)(I.ssd_g + ch); P.gs[g][1] = *(const f32x4*)(I.ssd_g + ch + 4); }
;     P.gm[0] = *(const f32x4*)(I.moba_g + 8 * X.lane); P.gm[1] = *(const f32x4*)(I.moba_g + 8 * X.lane + 4);
;     P.gd[0] = *(const f32x4*)(I.subln_g + 8 * (X.lane & 15)); P.gd[1] = *(const f32x4*)(I.subln_g + 8 * (X.lane & 15) + 4);
;     P5Row A, B;
;     p5_load(A, I, X.gw < NTOK ? X.gw : NTOK - 1, X.lane);
	s_load_dword s14, s[96:97], 0xf8
	v_readlane_b32 s44, v254, 60
	v_readlane_b32 s52, v255, 4
	v_readlane_b32 s53, v255, 5
	v_lshlrev_b32_e32 v122, 3, v34
	v_readlane_b32 s45, v254, 61
	v_readlane_b32 s46, v254, 62
	v_readlane_b32 s47, v254, 63
	v_readlane_b32 s48, v255, 0
	v_readlane_b32 s49, v255, 1
	v_readlane_b32 s50, v255, 2
	v_readlane_b32 s51, v255, 3
	v_readlane_b32 s54, v255, 6
	v_readlane_b32 s55, v255, 7
	v_readlane_b32 s56, v255, 8
	v_readlane_b32 s57, v255, 9
	v_readlane_b32 s58, v255, 10
	v_readlane_b32 s59, v255, 11
	s_mov_b64 s[24:25], s[52:53]
	v_or_b32_e32 v18, 0x200, v122
	s_waitcnt lgkmcnt(0)
	s_lshl_b32 s22, s14, 3
	s_mov_b64 s[26:27], s[54:55]
	s_mov_b64 s[28:29], s[56:57]
	v_readlane_b32 s44, v254, 31
	v_lshrrev_b32_e32 v2, 1, v34
	v_lshrrev_b32_e32 v3, 4, v18
	s_add_u32 s6, s26, 0x1000
	v_and_b32_e32 v124, 0x78, v122
	v_readlane_b32 s45, v254, 32
	v_and_b32_e32 v2, 28, v2
	v_and_b32_e32 v3, 60, v3
	s_addc_u32 s7, s27, 0
	v_lshlrev_b32_e32 v10, 2, v124
	s_mov_b64 s[8:9], s[44:45]
	v_lshlrev_b32_e32 v66, 5, v34
	v_lshlrev_b32_e32 v35, 2, v18
	s_ashr_i32 s5, s4, 31
	global_load_dword v143, v2, s[24:25] offset:64
	global_load_dword v144, v3, s[24:25] offset:64
	s_nop 0
	global_load_dwordx4 v[2:5], v10, s[44:45] offset:512
	global_load_dwordx4 v[6:9], v10, s[44:45] offset:528
	s_nop 0
	global_load_dwordx4 v[10:13], v66, s[28:29] offset:2048
	global_load_dwordx4 v[14:17], v66, s[28:29] offset:2064
	global_load_dwordx4 v[18:21], v35, s[6:7]
	global_load_dwordx4 v[22:25], v35, s[6:7] offset:16
	global_load_dwordx4 v[26:29], v66, s[6:7]
	global_load_dwordx4 v[30:33], v66, s[6:7] offset:16
	s_lshl_b64 s[6:7], s[4:5], 10
	s_lshl_b64 s[8:9], s[4:5], 11
	s_add_u32 s8, s86, s8
	v_mov_b32_e32 v125, 0
	s_addc_u32 s9, s87, s9
	v_and_b32_e32 v70, 0x600, v66
	v_mov_b32_e32 v71, v125
	s_add_u32 s6, s90, s6
	v_lshlrev_b32_e32 v68, 4, v34
	v_lshl_add_u64 v[34:35], s[8:9], 0, v[70:71]
	s_addc_u32 s7, s91, s7
	s_mul_i32 s8, s4, 0x2c00
	s_mul_hi_i32 s9, s4, 0x2c00
	s_add_u32 s8, s42, s8
	s_addc_u32 s9, s43, s9
	s_mul_i32 s10, s4, 0xc00
	v_readlane_b32 s16, v254, 49
	s_mul_hi_i32 s11, s4, 0xc00
	v_readlane_b32 s17, v254, 50
	s_add_u32 s10, s16, s10
	s_addc_u32 s11, s17, s11
	s_lshl_b64 s[12:13], s[4:5], 12
	v_readlane_b32 s20, v254, 53
	v_lshlrev_b32_e32 v72, 1, v124
	v_mov_b32_e32 v73, v125
	v_readlane_b32 s21, v254, 54
	s_add_u32 s12, s20, s12
	v_lshl_add_u64 v[42:43], v[34:35], 0, v[72:73]
	s_addc_u32 s13, s21, s13
	global_load_dwordx4 v[34:37], v[42:43], off offset:256
	global_load_dwordx4 v[38:41], v[42:43], off
	global_load_dwordx4 v[50:53], v68, s[10:11] offset:1024
	global_load_dwordx4 v[46:49], v66, s[12:13] offset:2064
	global_load_dwordx4 v[58:61], v66, s[12:13] offset:2048
	s_nop 0
	global_load_dwordx4 v[42:45], v68, s[6:7]
	global_load_dwordx4 v[82:85], v68, s[8:9]
	global_load_dwordx4 v[54:57], v68, s[8:9] offset:1024
	global_load_dwordx4 v[78:81], v68, s[10:11]
	global_load_dwordx4 v[74:77], v66, s[12:13] offset:16
	global_load_dwordx4 v[94:97], v66, s[12:13]
	v_add_f32_e32 v63, v63, v65
	v_add_f32_e32 v62, v62, v64
	v_mul_f32_e32 v63, 0x3fb8aa3b, v63
	v_mul_f32_e32 v62, 0x3fb8aa3b, v62
	v_exp_f32_e32 v63, v63
	v_exp_f32_e32 v62, v62
	v_mov_b32_e32 v67, v125
	v_mov_b32_e32 v69, v125
	v_mov_b32_e32 v123, v125
	v_sub_f32_e32 v62, v63, v62
	v_add_f32_e32 v145, 0x3eb60549, v62
	v_lshl_add_u64 v[62:63], s[86:87], 0, v[70:71]
	v_lshl_add_u64 v[126:127], s[90:91], 0, v[68:69]
	v_and_b32_e32 v128, 0x180, v122
	v_mov_b32_e32 v129, v125
	v_lshl_add_u64 v[130:131], s[20:21], 0, v[66:67]
	v_lshl_add_u64 v[132:133], s[16:17], 0, v[68:69]
	v_lshl_add_u64 v[134:135], s[42:43], 0, v[68:69]
	v_lshl_add_u64 v[136:137], v[62:63], 0, v[72:73]
	s_lshl_b32 s23, s14, 4
	v_mov_b32_e32 v146, 0x358637bd
	s_mov_b32 s24, 0xf800000
	v_mov_b32_e32 v147, 0x260
	s_mov_b32 s25, 0xc3e00000
	s_mov_b32 s26, 0x3f24fd5c
	v_mov_b32_e32 v148, 0xc00
	v_mov_b32_e32 v149, 0x2c00
	v_mov_b32_e32 v150, 0x43e00000
	v_readlane_b32 s46, v254, 33
	v_readlane_b32 s47, v254, 34
	v_readlane_b32 s48, v254, 35
	v_readlane_b32 s49, v254, 36
	v_readlane_b32 s50, v254, 37
	v_readlane_b32 s51, v254, 38
	v_readlane_b32 s52, v254, 39
	v_readlane_b32 s53, v254, 40
	v_readlane_b32 s54, v254, 41
	v_readlane_b32 s55, v254, 42
	v_readlane_b32 s56, v254, 43
	v_readlane_b32 s57, v254, 44
	v_readlane_b32 s58, v254, 45
	v_readlane_b32 s59, v254, 46
	s_waitcnt vmcnt(0)
	s_branch .LBB0_3412

; __device__ __forceinline__ float bflo(unsigned w) { return __uint_as_float(w << 16); }
; __device__ __forceinline__ float bfhi(unsigned w) { return __uint_as_float(w & 0xffff0000u); }
; __device__ __forceinline__ float siluf(float a) { return a / (1.0f + __expf(-a)); }
; __device__ __forceinline__ void p5_item(const P5Row& R, const P5In& I, const P5Par& P, int t, int lane) {
;     ...
;     for (int g = 0; g < 2; ++g) { const int ch = g * 512 + 8 * lane;
;         const f32x4 y0 = R.ya[g], y1 = R.yb[g]; const v4u xv = R.xr[g], zv = R.zr[g];
;         const float D = P.D[g];
;         float v[8];
;         v[0] = (y0[0] + D * bflo(xv.x)) * siluf(bflo(zv.x)); v[1] = (y0[1] + D * bfhi(xv.x)) * siluf(bfhi(zv.x));
;         v[2] = (y0[2] + D * bflo(xv.y)) * siluf(bflo(zv.y)); v[3] = (y0[3] + D * bfhi(xv.y)) * siluf(bfhi(zv.y));
;         v[4] = (y1[0] + D * bflo(xv.z)) * siluf(bflo(zv.z)); v[5] = (y1[1] + D * bfhi(xv.z)) * siluf(bfhi(zv.z));
;         v[6] = (y1[2] + D * bflo(xv.w)) * siluf(bflo(zv.w)); v[7] = (y1[3] + D * bfhi(xv.w)) * siluf(bfhi(zv.w));
;         float s = 0.f;
; #pragma unroll
;         for (int i = 0; i < 8; ++i) s += v[i] * v[i];
;         s = wave_sum(s); const float r = 1.0f / sqrtf(s * (1.0f / 512.0f) + EPSF);
; __device__ __forceinline__ void p5_finalize(const Ctx& X, const P5In& I) {
;     ...
;     for (int t = X.gw; t < NTOK; t += 2 * X.ngw) { const int t1 = t + X.ngw, t2 = t + 2 * X.ngw;
;         p5_load(B, I, t1 < NTOK ? t1 : NTOK - 1, X.lane);
.LBB0_3412:
	s_waitcnt vmcnt(4)
	v_lshlrev_b32_e32 v62, 16, v82
	v_mul_f32_e32 v63, 0xbfb8aa3b, v62
	v_exp_f32_e32 v63, v63
	s_waitcnt vmcnt(4)
	v_lshlrev_b32_e32 v66, 16, v78
	s_waitcnt vmcnt(4)
	v_fma_f32 v66, v143, v66, v94
	s_add_i32 s6, s4, s22
	v_add_f32_e32 v63, 1.0, v63
	v_div_scale_f32 v64, s[8:9], v63, v63, v62
	v_rcp_f32_e32 v65, v64
	s_add_i32 s7, s23, s4
	s_cmpk_lt_i32 s6, 0x2000
	s_cselect_b32 s20, s6, 0x1fff
	v_fma_f32 v67, -v64, v65, 1.0
	v_fmac_f32_e32 v65, v67, v65
	v_div_scale_f32 v67, vcc, v62, v63, v62
	v_mul_f32_e32 v68, v67, v65
	v_fma_f32 v69, -v64, v68, v67
	v_fmac_f32_e32 v68, v69, v65
	v_fma_f32 v64, -v64, v68, v67
	v_and_b32_e32 v67, 0xffff0000, v82
	v_mul_f32_e32 v69, 0xbfb8aa3b, v67
	v_exp_f32_e32 v69, v69
	v_div_fmas_f32 v64, v64, v65, v68
	v_div_fixup_f32 v62, v64, v63, v62
	v_mul_f32_e32 v82, v62, v66
	v_add_f32_e32 v63, 1.0, v69
	v_div_scale_f32 v64, s[8:9], v63, v63, v67
	v_rcp_f32_e32 v65, v64
	v_and_b32_e32 v62, 0xffff0000, v78
	v_fma_f32 v62, v143, v62, v95
	s_ashr_i32 s21, s20, 31
	v_fma_f32 v66, -v64, v65, 1.0
	v_fmac_f32_e32 v65, v66, v65
	v_div_scale_f32 v66, vcc, v67, v63, v67
	v_mul_f32_e32 v68, v66, v65
	v_fma_f32 v69, -v64, v68, v66
	v_fmac_f32_e32 v68, v69, v65
	v_fma_f32 v64, -v64, v68, v66
	v_lshlrev_b32_e32 v66, 16, v83
	v_mul_f32_e32 v69, 0xbfb8aa3b, v66
	v_exp_f32_e32 v69, v69
	v_div_fmas_f32 v64, v64, v65, v68
	v_div_fixup_f32 v63, v64, v63, v67
	v_mul_f32_e32 v78, v63, v62
	v_add_f32_e32 v64, 1.0, v69
	v_div_scale_f32 v65, s[8:9], v64, v64, v66
	v_rcp_f32_e32 v67, v65
	v_lshlrev_b32_e32 v62, 16, v79
	v_fma_f32 v62, v143, v62, v96
	s_ashr_i32 s5, s4, 31
	v_fma_f32 v63, -v65, v67, 1.0
	v_fmac_f32_e32 v67, v63, v67
	v_div_scale_f32 v63, vcc, v66, v64, v66
	v_mul_f32_e32 v68, v63, v67
	v_fma_f32 v69, -v65, v68, v63
	v_fmac_f32_e32 v68, v69, v67
	v_fma_f32 v63, -v65, v68, v63
	v_and_b32_e32 v65, 0xffff0000, v83
	v_mul_f32_e32 v69, 0xbfb8aa3b, v65
	v_exp_f32_e32 v69, v69
	v_div_fmas_f32 v63, v63, v67, v68
	v_div_fixup_f32 v63, v63, v64, v66
	v_mul_f32_e32 v83, v63, v62
	v_add_f32_e32 v64, 1.0, v69
	v_div_scale_f32 v66, s[8:9], v64, v64, v65
	v_rcp_f32_e32 v67, v66
	v_and_b32_e32 v62, 0xffff0000, v79
	v_fmac_f32_e32 v97, v143, v62
	s_lshl_b64 s[28:29], s[20:21], 10
	v_fma_f32 v62, -v66, v67, 1.0
	v_fmac_f32_e32 v67, v62, v67
	v_div_scale_f32 v62, vcc, v65, v64, v65
	v_mul_f32_e32 v63, v62, v67
	v_fma_f32 v68, -v66, v63, v62
	v_fmac_f32_e32 v63, v68, v67
	v_fma_f32 v62, -v66, v63, v62
	v_lshlrev_b32_e32 v66, 16, v84
	v_mul_f32_e32 v68, 0xbfb8aa3b, v66
	v_exp_f32_e32 v68, v68
	v_div_fmas_f32 v62, v62, v67, v63
	v_div_fixup_f32 v62, v62, v64, v65
	v_mul_f32_e32 v79, v62, v97
	v_add_f32_e32 v63, 1.0, v68
	v_div_scale_f32 v64, s[8:9], v63, v63, v66
	v_rcp_f32_e32 v65, v64
	v_lshlrev_b32_e32 v62, 16, v80
	v_fma_f32 v62, v143, v62, v74
	s_lshl_b64 s[30:31], s[20:21], 12
	v_fma_f32 v67, -v64, v65, 1.0
	v_fmac_f32_e32 v65, v67, v65
	v_div_scale_f32 v67, vcc, v66, v63, v66
	v_mul_f32_e32 v68, v67, v65
	v_fma_f32 v69, -v64, v68, v67
	v_fmac_f32_e32 v68, v69, v65
	v_fma_f32 v64, -v64, v68, v67
	v_and_b32_e32 v67, 0xffff0000, v84
	v_mul_f32_e32 v69, 0xbfb8aa3b, v67
	v_exp_f32_e32 v69, v69
	v_div_fmas_f32 v64, v64, v65, v68
	v_div_fixup_f32 v63, v64, v63, v66
	v_mul_f32_e32 v74, v63, v62
	v_add_f32_e32 v64, 1.0, v69
	v_div_scale_f32 v65, s[8:9], v64, v64, v67
	v_rcp_f32_e32 v66, v65
	v_and_b32_e32 v62, 0xffff0000, v80
	v_fma_f32 v62, v143, v62, v75
	s_lshl_b64 s[34:35], s[20:21], 11
	v_fma_f32 v63, -v65, v66, 1.0
	v_fmac_f32_e32 v66, v63, v66
	v_div_scale_f32 v63, vcc, v67, v64, v67
	v_mul_f32_e32 v68, v63, v66
	v_fma_f32 v69, -v65, v68, v63
	v_fmac_f32_e32 v68, v69, v66
	v_fma_f32 v63, -v65, v68, v63
	v_lshlrev_b32_e32 v65, 16, v85
	v_mul_f32_e32 v69, 0xbfb8aa3b, v65
	v_exp_f32_e32 v69, v69
	v_div_fmas_f32 v63, v63, v66, v68
	v_div_fixup_f32 v63, v63, v64, v67
	v_mul_f32_e32 v75, v63, v62
	v_add_f32_e32 v64, 1.0, v69
	v_div_scale_f32 v66, s[8:9], v64, v64, v65
	v_rcp_f32_e32 v67, v66
	v_lshlrev_b32_e32 v62, 16, v81
	v_fma_f32 v62, v143, v62, v76
	s_lshl_b64 s[4:5], s[4:5], 11
	v_fma_f32 v63, -v66, v67, 1.0
	v_fmac_f32_e32 v67, v63, v67
	v_div_scale_f32 v63, vcc, v65, v64, v65
	v_mul_f32_e32 v68, v63, v67
	v_fma_f32 v69, -v66, v68, v63
	v_fmac_f32_e32 v68, v69, v67
	v_fma_f32 v63, -v66, v68, v63
	v_and_b32_e32 v66, 0xffff0000, v85
	v_mul_f32_e32 v69, 0xbfb8aa3b, v66
	v_exp_f32_e32 v69, v69
	v_div_fmas_f32 v63, v63, v67, v68
	v_div_fixup_f32 v63, v63, v64, v65
	v_mul_f32_e32 v76, v63, v62
	v_add_f32_e32 v64, 1.0, v69
	v_div_scale_f32 v65, s[8:9], v64, v64, v66
	v_rcp_f32_e32 v67, v65
	v_and_b32_e32 v62, 0xffff0000, v81
	v_fmac_f32_e32 v77, v143, v62
	s_add_u32 s14, s64, s4
	v_fma_f32 v62, -v65, v67, 1.0
	v_fmac_f32_e32 v67, v62, v67
	v_div_scale_f32 v62, vcc, v66, v64, v66
	v_mul_f32_e32 v63, v62, v67
	v_fma_f32 v68, -v65, v63, v62
	v_fmac_f32_e32 v63, v68, v67
	v_fma_f32 v62, -v65, v63, v62
	v_div_fmas_f32 v62, v62, v67, v63
	v_div_fixup_f32 v62, v62, v64, v66
	v_mul_f32_e32 v77, v62, v77
	v_mul_f32_e32 v62, v78, v78
	v_fmac_f32_e32 v62, v82, v82
	v_fmac_f32_e32 v62, v83, v83
	v_fmac_f32_e32 v62, v79, v79
	v_fmac_f32_e32 v62, v74, v74
	v_fmac_f32_e32 v62, v75, v75
	v_fmac_f32_e32 v62, v76, v76
	v_fmac_f32_e32 v62, v77, v77
	ds_bpermute_b32 v63, v1, v62
	s_addc_u32 s15, s65, s5
	v_mad_i64_i32 v[66:67], s[4:5], s20, v149, v[134:135]
	s_min_i32 s12, s7, 0x1fff
	s_waitcnt lgkmcnt(0)
	v_add_f32_e32 v62, v62, v63
	ds_bpermute_b32 v63, v138, v62
	s_ashr_i32 s13, s12, 31
	s_lshl_b64 s[16:17], s[12:13], 12
	s_lshl_b64 s[8:9], s[12:13], 10
	s_lshl_b64 s[10:11], s[12:13], 11
	s_waitcnt lgkmcnt(0)
; __device__ __forceinline__ float bflo(unsigned w) { return __uint_as_float(w << 16); }
; __device__ __forceinline__ float bfhi(unsigned w) { return __uint_as_float(w & 0xffff0000u); }
; __device__ __forceinline__ float siluf(float a) { return a / (1.0f + __expf(-a)); }
; __device__ __forceinline__ void p5_load(P5Row& R, const P5In& I, int t, int lane) {
; #pragma unroll
;     for (int g = 0; g < 2; ++g) { const int ch = g * 512 + 8 * lane;
;         R.ya[g] = *(const f32x4*)(I.yraw + (size_t)t * 1024 + ch); R.yb[g] = *(const f32x4*)(I.yraw + (size_t)t * 1024 + ch + 4);
;         R.xr[g] = *(const v4u*)(I.xc + (size_t)t * 1536 + ch); R.zr[g] = *(const v4u*)(I.proj + (size_t)t * NPROJ + C_Z + ch); }
;     R.m4 = *(const v4u*)(I.moba + (size_t)t * 512 + 8 * lane);
;     const int dh = lane >> 4, dd = 8 * (lane & 15);
;     R.a4 = *(const v4u*)(I.diff + (size_t)t * 1024 + (dh * 2 + 0) * 128 + dd); R.b4 = *(const v4u*)(I.diff + (size_t)t * 1024 + (dh * 2 + 1) * 128 + dd);
; }
; __device__ __forceinline__ void p5_item(const P5Row& R, const P5In& I, const P5Par& P, int t, int lane) {
;     ...
;     for (int g = 0; g < 2; ++g) { const int ch = g * 512 + 8 * lane;
;         const f32x4 y0 = R.ya[g], y1 = R.yb[g]; const v4u xv = R.xr[g], zv = R.zr[g];
;         const float D = P.D[g];
;         float v[8];
;         v[0] = (y0[0] + D * bflo(xv.x)) * siluf(bflo(zv.x)); v[1] = (y0[1] + D * bfhi(xv.x)) * siluf(bfhi(zv.x));
;         v[2] = (y0[2] + D * bflo(xv.y)) * siluf(bflo(zv.y)); v[3] = (y0[3] + D * bfhi(xv.y)) * siluf(bfhi(zv.y));
;         v[4] = (y1[0] + D * bflo(xv.z)) * siluf(bflo(zv.z)); v[5] = (y1[1] + D * bfhi(xv.z)) * siluf(bfhi(zv.z));
;         v[6] = (y1[2] + D * bflo(xv.w)) * siluf(bflo(zv.w)); v[7] = (y1[3] + D * bfhi(xv.w)) * siluf(bfhi(zv.w));
;         float s = 0.f;
; #pragma unroll
;         for (int i = 0; i < 8; ++i) s += v[i] * v[i];
;         s = wave_sum(s); const float r = 1.0f / sqrtf(s * (1.0f / 512.0f) + EPSF);
;         p5_put8(I, (size_t)t * DM + ch, v, r, P.gs[g][0], P.gs[g][1]); }
	v_add_f32_e32 v62, v62, v63
	ds_bpermute_b32 v63, v139, v62
	s_cmpk_gt_i32 s6, 0x1fff
	s_waitcnt lgkmcnt(0)
	v_add_f32_e32 v64, v62, v63
	ds_bpermute_b32 v65, v140, v64
	v_lshl_add_u64 v[62:63], v[130:131], 0, s[30:31]
	global_load_dwordx4 v[106:109], v[62:63], off offset:16
	global_load_dwordx4 v[118:121], v[62:63], off
	s_waitcnt lgkmcnt(0)
	v_add_f32_e32 v68, v64, v65
	ds_bpermute_b32 v69, v141, v68
	v_mad_i64_i32 v[64:65], s[4:5], s20, v148, v[132:133]
	global_load_dwordx4 v[86:89], v[62:63], off offset:2064
	global_load_dwordx4 v[102:105], v[62:63], off offset:2048
	global_load_dwordx4 v[110:113], v[64:65], off
	global_load_dwordx4 v[90:93], v[64:65], off offset:1024
	global_load_dwordx4 v[114:117], v[66:67], off
	global_load_dwordx4 v[98:101], v[66:67], off offset:1024
	s_waitcnt lgkmcnt(0)
	v_add_f32_e32 v68, v68, v69
	ds_bpermute_b32 v69, v142, v68
	v_lshl_add_u64 v[66:67], v[136:137], 0, s[34:35]
	s_waitcnt lgkmcnt(0)
	v_add_f32_e32 v62, v68, v69
	v_fmamk_f32 v62, v62, 0x3b000000, v146
	v_mul_f32_e32 v63, 0x4f800000, v62
	v_cmp_gt_f32_e32 vcc, s24, v62
	s_nop 1
	v_cndmask_b32_e32 v64, v62, v63, vcc
	v_sqrt_f32_e32 v65, v64
	v_lshl_add_u64 v[62:63], v[126:127], 0, s[28:29]
	v_add_u32_e32 v68, -1, v65
	v_fma_f32 v69, -v68, v65, v64
	v_cmp_ge_f32_e64 s[4:5], 0, v69
	v_add_u32_e32 v69, 1, v65
	s_nop 0
	v_cndmask_b32_e64 v68, v65, v68, s[4:5]
	v_fma_f32 v65, -v69, v65, v64
	v_cmp_lt_f32_e64 s[4:5], 0, v65
	s_nop 1
	v_cndmask_b32_e64 v65, v68, v69, s[4:5]
	v_mul_f32_e32 v68, 0x37800000, v65
	v_cndmask_b32_e32 v65, v65, v68, vcc
	v_cmp_class_f32_e32 vcc, v64, v147
	s_nop 1
	v_cndmask_b32_e32 v80, v65, v64, vcc
	v_div_scale_f32 v81, s[4:5], v80, v80, 1.0
	v_rcp_f32_e32 v84, v81
	global_load_dwordx4 v[70:73], v[62:63], off
	s_nop 0
	global_load_dwordx4 v[62:65], v[66:67], off
	s_nop 0
	global_load_dwordx4 v[66:69], v[66:67], off offset:256
	v_fma_f32 v85, -v81, v84, 1.0
	v_fmac_f32_e32 v84, v85, v84
	v_div_scale_f32 v85, vcc, 1.0, v80, 1.0
	v_mul_f32_e32 v94, v85, v84
	v_fma_f32 v95, -v81, v94, v85
	v_fmac_f32_e32 v94, v95, v84
	v_fma_f32 v81, -v81, v94, v85
	v_lshlrev_b32_e32 v85, 16, v54
	v_mul_f32_e32 v95, 0xbfb8aa3b, v85
	v_exp_f32_e32 v95, v95
	v_div_fmas_f32 v81, v81, v84, v94
	v_div_fixup_f32 v80, v81, v80, 1.0
	v_and_b32_e32 v54, 0xffff0000, v54
	v_add_f32_e32 v81, 1.0, v95
	v_div_scale_f32 v84, s[4:5], v81, v81, v85
	v_rcp_f32_e32 v94, v84
	v_lshlrev_b32_e32 v95, 16, v50
	v_fma_f32 v58, v144, v95, v58
	v_and_b32_e32 v50, 0xffff0000, v50
	v_fma_f32 v95, -v84, v94, 1.0
	v_fmac_f32_e32 v94, v95, v94
	v_div_scale_f32 v95, vcc, v85, v81, v85
	v_mul_f32_e32 v96, v95, v94
	v_fma_f32 v97, -v84, v96, v95
	v_fmac_f32_e32 v96, v97, v94
	v_fma_f32 v84, -v84, v96, v95
	v_mul_f32_e32 v95, 0xbfb8aa3b, v54
	v_exp_f32_e32 v95, v95
	v_div_fmas_f32 v84, v84, v94, v96
	v_div_fixup_f32 v81, v84, v81, v85
	v_fma_f32 v50, v144, v50, v59
	v_add_f32_e32 v84, 1.0, v95
	v_div_scale_f32 v85, s[4:5], v84, v84, v54
	v_rcp_f32_e32 v94, v85
	v_mul_f32_e32 v58, v81, v58
	v_mul_f32_e32 v80, 0x41000000, v80
	v_fma_f32 v59, -v85, v94, 1.0
	v_fmac_f32_e32 v94, v59, v94
	v_div_scale_f32 v59, vcc, v54, v84, v54
	v_mul_f32_e32 v81, v59, v94
	v_fma_f32 v95, -v85, v81, v59
	v_fmac_f32_e32 v81, v95, v94
	v_fma_f32 v59, -v85, v81, v59
	v_lshlrev_b32_e32 v85, 16, v55
	v_mul_f32_e32 v95, 0xbfb8aa3b, v85
	v_exp_f32_e32 v95, v95
	v_div_fmas_f32 v59, v59, v94, v81
	v_div_fixup_f32 v54, v59, v84, v54
	v_mul_f32_e32 v50, v54, v50
	v_add_f32_e32 v59, 1.0, v95
	v_div_scale_f32 v81, s[4:5], v59, v59, v85
	v_rcp_f32_e32 v84, v81
	v_lshlrev_b32_e32 v54, 16, v51
	v_fma_f32 v54, v144, v54, v60
	v_and_b32_e32 v55, 0xffff0000, v55
	v_fma_f32 v60, -v81, v84, 1.0
	v_fmac_f32_e32 v84, v60, v84
	v_div_scale_f32 v60, vcc, v85, v59, v85
	v_mul_f32_e32 v94, v60, v84
	v_fma_f32 v95, -v81, v94, v60
	v_fmac_f32_e32 v94, v95, v84
	v_fma_f32 v60, -v81, v94, v60
	v_mul_f32_e32 v81, 0xbfb8aa3b, v55
	v_exp_f32_e32 v81, v81
	v_div_fmas_f32 v60, v60, v84, v94
	v_div_fixup_f32 v59, v60, v59, v85
	v_and_b32_e32 v51, 0xffff0000, v51
	v_add_f32_e32 v60, 1.0, v81
	v_div_scale_f32 v81, s[4:5], v60, v60, v55
	v_rcp_f32_e32 v84, v81
	v_fmac_f32_e32 v61, v144, v51
	v_mul_f32_e32 v54, v59, v54
	v_fma_f32 v51, -v81, v84, 1.0
	v_fmac_f32_e32 v84, v51, v84
	v_div_scale_f32 v51, vcc, v55, v60, v55
	v_mul_f32_e32 v59, v51, v84
	v_fma_f32 v85, -v81, v59, v51
	v_fmac_f32_e32 v59, v85, v84
	v_fma_f32 v51, -v81, v59, v51
	v_lshlrev_b32_e32 v81, 16, v56
	v_mul_f32_e32 v85, 0xbfb8aa3b, v81
	v_exp_f32_e32 v85, v85
	v_div_fmas_f32 v51, v51, v84, v59
	v_div_fixup_f32 v51, v51, v60, v55
	v_mul_f32_e32 v51, v51, v61
	v_add_f32_e32 v55, 1.0, v85
	v_div_scale_f32 v59, s[4:5], v55, v55, v81
	v_rcp_f32_e32 v60, v59
	v_lshlrev_b32_e32 v61, 16, v52
	v_fma_f32 v46, v144, v61, v46
	v_and_b32_e32 v56, 0xffff0000, v56
	v_fma_f32 v61, -v59, v60, 1.0
	v_fmac_f32_e32 v60, v61, v60
	v_div_scale_f32 v61, vcc, v81, v55, v81
	v_mul_f32_e32 v84, v61, v60
	v_fma_f32 v85, -v59, v84, v61
	v_fmac_f32_e32 v84, v85, v60
	v_fma_f32 v59, -v59, v84, v61
	v_mul_f32_e32 v61, 0xbfb8aa3b, v56
	v_exp_f32_e32 v61, v61
	v_div_fmas_f32 v59, v59, v60, v84
	v_div_fixup_f32 v55, v59, v55, v81
	v_mul_f32_e32 v55, v55, v46
	v_add_f32_e32 v59, 1.0, v61
	v_div_scale_f32 v60, s[4:5], v59, v59, v56
	v_rcp_f32_e32 v61, v60
	v_and_b32_e32 v46, 0xffff0000, v52
	v_fma_f32 v46, v144, v46, v47
	v_fma_f32 v47, -v60, v61, 1.0
	v_fmac_f32_e32 v61, v47, v61
	v_div_scale_f32 v47, vcc, v56, v59, v56
	v_mul_f32_e32 v52, v47, v61
	v_fma_f32 v81, -v60, v52, v47
	v_fmac_f32_e32 v52, v81, v61
	v_fma_f32 v47, -v60, v52, v47
	v_lshlrev_b32_e32 v60, 16, v57
	v_mul_f32_e32 v81, 0xbfb8aa3b, v60
; __device__ __forceinline__ float bflo(unsigned w) { return __uint_as_float(w << 16); }
; __device__ __forceinline__ float bfhi(unsigned w) { return __uint_as_float(w & 0xffff0000u); }
; __device__ __forceinline__ float siluf(float a) { return a / (1.0f + __expf(-a)); }
; __device__ __forceinline__ void p5_item(const P5Row& R, const P5In& I, const P5Par& P, int t, int lane) {
;     ...
;     for (int g = 0; g < 2; ++g) { const int ch = g * 512 + 8 * lane;
;         const f32x4 y0 = R.ya[g], y1 = R.yb[g]; const v4u xv = R.xr[g], zv = R.zr[g];
;         const float D = P.D[g];
;         float v[8];
;         v[0] = (y0[0] + D * bflo(xv.x)) * siluf(bflo(zv.x)); v[1] = (y0[1] + D * bfhi(xv.x)) * siluf(bfhi(zv.x));
;         v[2] = (y0[2] + D * bflo(xv.y)) * siluf(bflo(zv.y)); v[3] = (y0[3] + D * bfhi(xv.y)) * siluf(bfhi(zv.y));
;         v[4] = (y1[0] + D * bflo(xv.z)) * siluf(bflo(zv.z)); v[5] = (y1[1] + D * bfhi(xv.z)) * siluf(bfhi(zv.z));
;         v[6] = (y1[2] + D * bflo(xv.w)) * siluf(bflo(zv.w)); v[7] = (y1[3] + D * bfhi(xv.w)) * siluf(bfhi(zv.w));
;         float s = 0.f;
; #pragma unroll
;         for (int i = 0; i < 8; ++i) s += v[i] * v[i];
;         s = wave_sum(s); const float r = 1.0f / sqrtf(s * (1.0f / 512.0f) + EPSF);
;         p5_put8(I, (size_t)t * DM + ch, v, r, P.gs[g][0], P.gs[g][1]); }
;     { const int ch = 8 * lane; const v4u r4 = R.m4;
;       float v[8] = {bflo(r4.x), bfhi(r4.x), bflo(r4.y), bfhi(r4.y), bflo(r4.z), bfhi(r4.z), bflo(r4.w), bfhi(r4.w)}; float s = 0.f;
; #pragma unroll
;       for (int i = 0; i < 8; ++i) s += v[i] * v[i];
;       s += __shfl_xor(s, 1); s += __shfl_xor(s, 2); s += __shfl_xor(s, 4);
;       const float r = 1.0f / sqrtf(s * (1.0f / 64.0f) + EPSF);
;       p5_put8(I, (size_t)t * DM + 1024 + ch, v, r, P.gm[0], P.gm[1]); }
	v_exp_f32_e32 v81, v81
	v_div_fmas_f32 v47, v47, v61, v52
	v_div_fixup_f32 v47, v47, v59, v56
	v_mul_f32_e32 v61, v47, v46
	v_add_f32_e32 v52, 1.0, v81
	v_div_scale_f32 v56, s[4:5], v52, v52, v60
	v_rcp_f32_e32 v59, v56
	v_lshlrev_b32_e32 v46, 16, v53
	v_fma_f32 v46, v144, v46, v48
	v_fma_f32 v47, -v56, v59, 1.0
	v_fmac_f32_e32 v59, v47, v59
	v_div_scale_f32 v47, vcc, v60, v52, v60
	v_mul_f32_e32 v48, v47, v59
	v_fma_f32 v81, -v56, v48, v47
	v_fmac_f32_e32 v48, v81, v59
	v_fma_f32 v47, -v56, v48, v47
	v_and_b32_e32 v56, 0xffff0000, v57
	v_mul_f32_e32 v57, 0xbfb8aa3b, v56
	v_exp_f32_e32 v57, v57
	v_div_fmas_f32 v47, v47, v59, v48
	v_div_fixup_f32 v47, v47, v52, v60
	v_mul_f32_e32 v59, v47, v46
	v_add_f32_e32 v48, 1.0, v57
	v_div_scale_f32 v52, s[4:5], v48, v48, v56
	v_rcp_f32_e32 v57, v52
	v_and_b32_e32 v46, 0xffff0000, v53
	v_fmac_f32_e32 v49, v144, v46
	v_fma_f32 v46, -v52, v57, 1.0
	v_fmac_f32_e32 v57, v46, v57
	v_div_scale_f32 v46, vcc, v56, v48, v56
	v_mul_f32_e32 v47, v46, v57
	v_fma_f32 v53, -v52, v47, v46
	v_fmac_f32_e32 v47, v53, v57
	v_fma_f32 v46, -v52, v47, v46
	v_div_fmas_f32 v46, v46, v57, v47
	v_div_fixup_f32 v46, v46, v48, v56
	v_mul_f32_e32 v49, v46, v49
	v_mul_f32_e32 v46, v50, v50
	v_fmac_f32_e32 v46, v58, v58
	v_fmac_f32_e32 v46, v54, v54
	v_fmac_f32_e32 v46, v51, v51
	v_fmac_f32_e32 v46, v55, v55
	v_fmac_f32_e32 v46, v61, v61
	v_fmac_f32_e32 v46, v59, v59
	v_fmac_f32_e32 v46, v49, v49
	ds_bpermute_b32 v47, v1, v46
	v_mul_f32_e32 v48, v82, v80
	v_mul_f32_e32 v52, v78, v80
	v_mul_f32_e32 v48, v26, v48
	v_mul_f32_e32 v52, v27, v52
	s_waitcnt lgkmcnt(0)
	v_add_f32_e32 v46, v46, v47
	ds_bpermute_b32 v47, v138, v46
	v_med3_f32 v48, v48, s25, v150
	v_med3_f32 v52, v52, s25, v150
	v_mul_f32_e32 v53, v83, v80
	v_mul_f32_e32 v56, v79, v80
	s_waitcnt lgkmcnt(0)
	v_add_f32_e32 v47, v46, v47
	ds_bpermute_b32 v57, v139, v47
	v_mov_b32_e32 v46, 0
	v_cvt_pk_fp8_f32 v46, v48, v52
	v_mul_f32_e32 v53, v28, v53
	v_mul_f32_e32 v56, v29, v56
	s_waitcnt lgkmcnt(0)
	v_add_f32_e32 v47, v47, v57
	ds_bpermute_b32 v48, v140, v47
	v_med3_f32 v52, v53, s25, v150
	v_med3_f32 v53, v56, s25, v150
	v_cvt_pk_fp8_f32 v46, v52, v53 op_sel:[0,0,1]
	v_mul_f32_e32 v52, v74, v80
	s_waitcnt lgkmcnt(0)
	v_add_f32_e32 v47, v47, v48
	ds_bpermute_b32 v48, v141, v47
	v_mul_f32_e32 v53, v75, v80
	v_mul_f32_e32 v52, v30, v52
	v_mul_f32_e32 v53, v31, v53
	v_med3_f32 v52, v52, s25, v150
	s_waitcnt lgkmcnt(0)
	v_add_f32_e32 v47, v47, v48
	ds_bpermute_b32 v48, v142, v47
	v_med3_f32 v53, v53, s25, v150
	v_mul_f32_e32 v56, v76, v80
	v_mul_f32_e32 v57, v77, v80
	v_mul_f32_e32 v56, v32, v56
	s_waitcnt lgkmcnt(0)
	v_add_f32_e32 v47, v47, v48
	v_fmamk_f32 v47, v47, 0x3b000000, v146
	v_mul_f32_e32 v48, 0x4f800000, v47
	v_cmp_gt_f32_e32 vcc, s24, v47
	v_mul_f32_e32 v57, v33, v57
	v_med3_f32 v56, v56, s25, v150
	v_cndmask_b32_e32 v48, v47, v48, vcc
	v_sqrt_f32_e32 v60, v48
	v_mov_b32_e32 v47, 0
	v_cvt_pk_fp8_f32 v47, v52, v53
	v_med3_f32 v57, v57, s25, v150
	v_add_u32_e32 v52, -1, v60
	v_fma_f32 v53, -v52, v60, v48
	v_cmp_ge_f32_e64 s[4:5], 0, v53
	v_add_u32_e32 v53, 1, v60
	v_cvt_pk_fp8_f32 v47, v56, v57 op_sel:[0,0,1]
	v_cndmask_b32_e64 v52, v60, v52, s[4:5]
	v_fma_f32 v60, -v53, v60, v48
	v_cmp_lt_f32_e64 s[4:5], 0, v60
	s_nop 1
	v_cndmask_b32_e64 v52, v52, v53, s[4:5]
	v_mul_f32_e32 v53, 0x37800000, v52
	v_cndmask_b32_e32 v52, v52, v53, vcc
	v_cmp_class_f32_e32 vcc, v48, v147
	s_nop 1
	v_cndmask_b32_e32 v48, v52, v48, vcc
	v_div_scale_f32 v52, s[4:5], v48, v48, 1.0
	v_rcp_f32_e32 v53, v52
	s_nop 0
	v_fma_f32 v56, -v52, v53, 1.0
	v_fmac_f32_e32 v53, v56, v53
	v_div_scale_f32 v56, vcc, 1.0, v48, 1.0
	v_mul_f32_e32 v57, v56, v53
	v_fma_f32 v60, -v52, v57, v56
	v_fmac_f32_e32 v57, v60, v53
	v_fma_f32 v52, -v52, v57, v56
	v_div_fmas_f32 v52, v52, v53, v57
	v_div_fixup_f32 v48, v52, v48, 1.0
	v_mul_f32_e32 v52, 0x41000000, v48
	v_mul_f32_e32 v48, v58, v52
	v_mul_f32_e32 v50, v50, v52
	v_mul_f32_e32 v48, v18, v48
	v_mul_f32_e32 v50, v19, v50
	v_mul_f32_e32 v53, v54, v52
	v_med3_f32 v54, v48, s25, v150
	v_med3_f32 v50, v50, s25, v150
	v_mov_b32_e32 v48, 0
	v_cvt_pk_fp8_f32 v48, v54, v50
	v_mul_f32_e32 v51, v51, v52
	v_mul_f32_e32 v53, v20, v53
	v_mul_f32_e32 v50, v21, v51
	v_med3_f32 v51, v53, s25, v150
	v_med3_f32 v50, v50, s25, v150
	v_cvt_pk_fp8_f32 v48, v51, v50 op_sel:[0,0,1]
	v_and_b32_e32 v51, 0xffff0000, v42
	v_lshlrev_b32_e32 v50, 16, v42
	v_mul_f32_e32 v42, v51, v51
	v_lshlrev_b32_e32 v53, 16, v43
	v_fmac_f32_e32 v42, v50, v50
	v_and_b32_e32 v54, 0xffff0000, v43
	v_fmac_f32_e32 v42, v53, v53
	v_lshlrev_b32_e32 v56, 16, v44
	v_fmac_f32_e32 v42, v54, v54
	v_and_b32_e32 v44, 0xffff0000, v44
	v_fmac_f32_e32 v42, v56, v56
	v_lshlrev_b32_e32 v57, 16, v45
	v_fmac_f32_e32 v42, v44, v44
	v_and_b32_e32 v45, 0xffff0000, v45
	v_fmac_f32_e32 v42, v57, v57
	v_fmac_f32_e32 v42, v45, v45
	ds_bpermute_b32 v43, v1, v42
	v_mul_f32_e32 v55, v55, v52
	v_mul_f32_e32 v58, v61, v52
	v_mul_f32_e32 v55, v22, v55
	v_mul_f32_e32 v58, v23, v58
	s_waitcnt lgkmcnt(0)
	v_add_f32_e32 v42, v42, v43
	ds_bpermute_b32 v43, v138, v42
	v_mul_f32_e32 v49, v49, v52
	v_mul_f32_e32 v59, v59, v52
	v_mul_f32_e32 v52, v25, v49
	v_med3_f32 v55, v55, s25, v150
	s_waitcnt lgkmcnt(0)
	v_add_f32_e32 v42, v42, v43
	ds_bpermute_b32 v43, v139, v42
	v_med3_f32 v58, v58, s25, v150
	v_mov_b32_e32 v49, 0
	v_cvt_pk_fp8_f32 v49, v55, v58
	v_mul_f32_e32 v59, v24, v59
	s_waitcnt lgkmcnt(0)
; __device__ __forceinline__ float bflo(unsigned w) { return __uint_as_float(w << 16); }
; __device__ __forceinline__ float bfhi(unsigned w) { return __uint_as_float(w & 0xffff0000u); }
; __device__ __forceinline__ void p5_item(const P5Row& R, const P5In& I, const P5Par& P, int t, int lane) {
;     ...
;     { const int ch = 8 * lane; const v4u r4 = R.m4;
;       float v[8] = {bflo(r4.x), bfhi(r4.x), bflo(r4.y), bfhi(r4.y), bflo(r4.z), bfhi(r4.z), bflo(r4.w), bfhi(r4.w)}; float s = 0.f;
; #pragma unroll
;       for (int i = 0; i < 8; ++i) s += v[i] * v[i];
;       s += __shfl_xor(s, 1); s += __shfl_xor(s, 2); s += __shfl_xor(s, 4);
;       const float r = 1.0f / sqrtf(s * (1.0f / 64.0f) + EPSF);
;       p5_put8(I, (size_t)t * DM + 1024 + ch, v, r, P.gm[0], P.gm[1]); }
;     { const int h = lane >> 4, d = 8 * (lane & 15); const v4u a4 = R.a4, b4 = R.b4; const float lam = P.lam;
;       float v[8] = {bflo(a4.x) - lam * bflo(b4.x), bfhi(a4.x) - lam * bfhi(b4.x), bflo(a4.y) - lam * bflo(b4.y), bfhi(a4.y) - lam * bfhi(b4.y),
;                     bflo(a4.z) - lam * bflo(b4.z), bfhi(a4.z) - lam * bfhi(b4.z), bflo(a4.w) - lam * bflo(b4.w), bfhi(a4.w) - lam * bfhi(b4.w)}; float s = 0.f;
; #pragma unroll
;       for (int i = 0; i < 8; ++i) s += v[i] * v[i];
;       s += __shfl_xor(s, 1); s += __shfl_xor(s, 2); s += __shfl_xor(s, 4); s += __shfl_xor(s, 8);
;       const float r = (1.0f - I.lambda_init) / sqrtf(s * (1.0f / 128.0f) + EPSF);
;       p5_put8(I, (size_t)t * DM + 1536 + h * 128 + d, v, r, P.gd[0], P.gd[1]); }
; __device__ __forceinline__ void p5_finalize(const Ctx& X, const P5In& I) {
;     ...
;         p5_load(A, I, t2 < NTOK ? t2 : NTOK - 1, X.lane);
;         if (t1 < NTOK) p5_item(B, I, P, t1, X.lane); }
	v_add_f32_e32 v42, v42, v43
	v_fmamk_f32 v42, v42, 0x3c800000, v146
	v_mul_f32_e32 v43, 0x4f800000, v42
	v_cmp_gt_f32_e32 vcc, s24, v42
	v_med3_f32 v55, v59, s25, v150
	v_med3_f32 v52, v52, s25, v150
	v_cndmask_b32_e32 v42, v42, v43, vcc
	v_sqrt_f32_e32 v43, v42
	v_cvt_pk_fp8_f32 v49, v55, v52 op_sel:[0,0,1]
	v_add_u32_e32 v52, -1, v43
	v_fma_f32 v55, -v52, v43, v42
	v_cmp_ge_f32_e64 s[4:5], 0, v55
	v_add_u32_e32 v55, 1, v43
	s_nop 0
	v_cndmask_b32_e64 v52, v43, v52, s[4:5]
	v_fma_f32 v43, -v55, v43, v42
	v_cmp_lt_f32_e64 s[4:5], 0, v43
	s_nop 1
	v_cndmask_b32_e64 v43, v52, v55, s[4:5]
	v_mul_f32_e32 v52, 0x37800000, v43
	v_cndmask_b32_e32 v43, v43, v52, vcc
	v_cmp_class_f32_e32 vcc, v42, v147
	s_nop 1
	v_cndmask_b32_e32 v52, v43, v42, vcc
	v_div_scale_f32 v55, s[4:5], v52, v52, 1.0
	v_rcp_f32_e32 v58, v55
	v_lshl_add_u64 v[42:43], s[14:15], 0, v[122:123]
	global_store_dwordx2 v[42:43], v[46:47], off
	global_store_dwordx2 v[42:43], v[48:49], off offset:512
	v_fma_f32 v46, -v55, v58, 1.0
	v_fmac_f32_e32 v58, v46, v58
	v_div_scale_f32 v46, vcc, 1.0, v52, 1.0
	v_mul_f32_e32 v47, v46, v58
	v_fma_f32 v48, -v55, v47, v46
	v_fmac_f32_e32 v47, v48, v58
	v_fma_f32 v46, -v55, v47, v46
	v_div_fmas_f32 v46, v46, v58, v47
	v_div_fixup_f32 v46, v46, v52, 1.0
	v_mul_f32_e32 v46, 0x41000000, v46
	v_mul_f32_e32 v48, v46, v51
	v_lshlrev_b32_e32 v51, 16, v38
	v_lshlrev_b32_e32 v52, 16, v34
	v_and_b32_e32 v38, 0xffff0000, v38
	v_and_b32_e32 v34, 0xffff0000, v34
	v_fma_f32 v51, -v145, v52, v51
	v_fma_f32 v38, -v145, v34, v38
	v_lshlrev_b32_e32 v34, 16, v39
	v_lshlrev_b32_e32 v52, 16, v35
	v_fma_f32 v52, -v145, v52, v34
	v_and_b32_e32 v34, 0xffff0000, v39
	v_and_b32_e32 v35, 0xffff0000, v35
	v_fma_f32 v39, -v145, v35, v34
	v_lshlrev_b32_e32 v34, 16, v40
	v_lshlrev_b32_e32 v35, 16, v36
	v_mul_f32_e32 v49, v46, v53
	v_fma_f32 v53, -v145, v35, v34
	v_and_b32_e32 v34, 0xffff0000, v40
	v_and_b32_e32 v35, 0xffff0000, v36
	v_fma_f32 v40, -v145, v35, v34
	v_lshlrev_b32_e32 v34, 16, v41
	v_lshlrev_b32_e32 v35, 16, v37
	v_mul_f32_e32 v47, v46, v50
	v_mul_f32_e32 v50, v46, v54
	v_fma_f32 v54, -v145, v35, v34
	v_and_b32_e32 v34, 0xffff0000, v41
	v_and_b32_e32 v35, 0xffff0000, v37
	v_fma_f32 v37, -v145, v35, v34
	v_mul_f32_e32 v35, v38, v38
	v_fmac_f32_e32 v35, v51, v51
	v_fmac_f32_e32 v35, v52, v52
	v_fmac_f32_e32 v35, v39, v39
	v_fmac_f32_e32 v35, v53, v53
	v_fmac_f32_e32 v35, v40, v40
	v_fmac_f32_e32 v35, v54, v54
	v_fmac_f32_e32 v35, v37, v37
	ds_bpermute_b32 v36, v1, v35
	v_mul_f32_e32 v47, v10, v47
	v_mul_f32_e32 v48, v11, v48
	v_med3_f32 v41, v47, s25, v150
	v_med3_f32 v47, v48, s25, v150
	s_waitcnt lgkmcnt(0)
	v_add_f32_e32 v35, v35, v36
	ds_bpermute_b32 v36, v138, v35
	v_mov_b32_e32 v34, 0
	v_cvt_pk_fp8_f32 v34, v41, v47
	v_mul_f32_e32 v49, v12, v49
	v_mul_f32_e32 v50, v13, v50
	s_waitcnt lgkmcnt(0)
	v_add_f32_e32 v35, v35, v36
	ds_bpermute_b32 v36, v139, v35
	v_med3_f32 v41, v49, s25, v150
	v_med3_f32 v47, v50, s25, v150
	v_cvt_pk_fp8_f32 v34, v41, v47 op_sel:[0,0,1]
	v_mul_f32_e32 v41, v46, v56
	s_waitcnt lgkmcnt(0)
	v_add_f32_e32 v35, v35, v36
	ds_bpermute_b32 v36, v140, v35
	v_mul_f32_e32 v44, v46, v44
	v_mul_f32_e32 v47, v46, v57
	v_mul_f32_e32 v45, v46, v45
	v_mul_f32_e32 v41, v14, v41
	s_waitcnt lgkmcnt(0)
	v_add_f32_e32 v35, v35, v36
	v_fmamk_f32 v35, v35, 0x3c000000, v146
	v_mul_f32_e32 v36, 0x4f800000, v35
	v_cmp_gt_f32_e32 vcc, s24, v35
	v_mul_f32_e32 v44, v15, v44
	v_med3_f32 v41, v41, s25, v150
	v_cndmask_b32_e32 v36, v35, v36, vcc
	v_sqrt_f32_e32 v46, v36
	v_med3_f32 v44, v44, s25, v150
	v_mov_b32_e32 v35, 0
	v_cvt_pk_fp8_f32 v35, v41, v44
	v_add_u32_e32 v41, -1, v46
	v_fma_f32 v44, -v41, v46, v36
	v_cmp_ge_f32_e64 s[4:5], 0, v44
	v_add_u32_e32 v44, 1, v46
	v_mul_f32_e32 v47, v16, v47
	v_cndmask_b32_e64 v41, v46, v41, s[4:5]
	v_fma_f32 v46, -v44, v46, v36
	v_cmp_lt_f32_e64 s[4:5], 0, v46
	v_mul_f32_e32 v45, v17, v45
	v_med3_f32 v46, v47, s25, v150
	v_cndmask_b32_e64 v41, v41, v44, s[4:5]
	v_mul_f32_e32 v44, 0x37800000, v41
	v_cndmask_b32_e32 v41, v41, v44, vcc
	v_cmp_class_f32_e32 vcc, v36, v147
	v_med3_f32 v45, v45, s25, v150
	v_cvt_pk_fp8_f32 v35, v46, v45 op_sel:[0,0,1]
	v_cndmask_b32_e32 v36, v41, v36, vcc
	v_div_scale_f32 v41, s[4:5], v36, v36, s26
	v_rcp_f32_e32 v44, v41
	global_store_dwordx2 v[42:43], v[34:35], off offset:1024
	v_lshl_add_u64 v[34:35], s[14:15], 0, v[128:129]
	v_lshl_add_u64 v[34:35], v[34:35], 0, v[124:125]
	v_fma_f32 v45, -v41, v44, 1.0
	v_fmac_f32_e32 v44, v45, v44
	v_div_scale_f32 v45, vcc, s26, v36, s26
	v_mul_f32_e32 v46, v45, v44
	v_fma_f32 v47, -v41, v46, v45
	v_fmac_f32_e32 v46, v47, v44
	v_fma_f32 v41, -v41, v46, v45
	v_div_fmas_f32 v41, v41, v44, v46
	v_div_fixup_f32 v36, v41, v36, s26
	v_mul_f32_e32 v41, 0x41000000, v36
	v_mul_f32_e32 v36, v51, v41
	v_mul_f32_e32 v38, v38, v41
	v_mul_f32_e32 v36, v2, v36
	v_mul_f32_e32 v38, v3, v38
	v_med3_f32 v45, v36, s25, v150
	v_med3_f32 v38, v38, s25, v150
	v_mov_b32_e32 v36, 0
	v_cvt_pk_fp8_f32 v36, v45, v38
	v_mul_f32_e32 v44, v52, v41
	v_mul_f32_e32 v39, v39, v41
	v_mul_f32_e32 v44, v4, v44
	v_mul_f32_e32 v38, v5, v39
	v_med3_f32 v39, v44, s25, v150
	v_med3_f32 v38, v38, s25, v150
	v_cvt_pk_fp8_f32 v36, v39, v38 op_sel:[0,0,1]
	v_mul_f32_e32 v38, v53, v41
	v_mul_f32_e32 v39, v40, v41
	v_mul_f32_e32 v38, v6, v38
	v_mul_f32_e32 v39, v7, v39
	v_mul_f32_e32 v40, v54, v41
	v_mul_f32_e32 v41, v37, v41
	v_med3_f32 v38, v38, s25, v150
	v_med3_f32 v39, v39, s25, v150
	v_mov_b32_e32 v37, 0
	v_cvt_pk_fp8_f32 v37, v38, v39
	v_mul_f32_e32 v40, v8, v40
	v_mul_f32_e32 v38, v9, v41
	v_med3_f32 v39, v40, s25, v150
	v_med3_f32 v38, v38, s25, v150
	v_cvt_pk_fp8_f32 v37, v39, v38 op_sel:[0,0,1]
	v_mad_i64_i32 v[38:39], s[4:5], s12, v149, v[134:135]
	global_store_dwordx2 v[34:35], v[36:37], off offset:1536
	v_lshl_add_u64 v[34:35], v[130:131], 0, s[16:17]
	global_load_dwordx4 v[74:77], v[34:35], off offset:16
	global_load_dwordx4 v[94:97], v[34:35], off
	v_mad_i64_i32 v[36:37], s[4:5], s12, v148, v[132:133]
	global_load_dwordx4 v[46:49], v[34:35], off offset:2064
	global_load_dwordx4 v[58:61], v[34:35], off offset:2048
	global_load_dwordx4 v[78:81], v[36:37], off
	global_load_dwordx4 v[50:53], v[36:37], off offset:1024
	global_load_dwordx4 v[82:85], v[38:39], off
	global_load_dwordx4 v[54:57], v[38:39], off offset:1024
	v_lshl_add_u64 v[34:35], v[126:127], 0, s[8:9]
	v_lshl_add_u64 v[36:37], v[136:137], 0, s[10:11]
	global_load_dwordx4 v[42:45], v[34:35], off
	global_load_dwordx4 v[38:41], v[36:37], off
	s_nop 0
	global_load_dwordx4 v[34:37], v[36:37], off offset:256
	s_cbranch_scc1 .Lfin_skip1
; __device__ __forceinline__ float bflo(unsigned w) { return __uint_as_float(w << 16); }
; __device__ __forceinline__ float bfhi(unsigned w) { return __uint_as_float(w & 0xffff0000u); }
; __device__ __forceinline__ float siluf(float a) { return a / (1.0f + __expf(-a)); }
; __device__ __forceinline__ void p5_item(const P5Row& R, const P5In& I, const P5Par& P, int t, int lane) {
;     ...
;     for (int g = 0; g < 2; ++g) { const int ch = g * 512 + 8 * lane;
;         const f32x4 y0 = R.ya[g], y1 = R.yb[g]; const v4u xv = R.xr[g], zv = R.zr[g];
;         const float D = P.D[g];
;         float v[8];
;         v[0] = (y0[0] + D * bflo(xv.x)) * siluf(bflo(zv.x)); v[1] = (y0[1] + D * bfhi(xv.x)) * siluf(bfhi(zv.x));
;         v[2] = (y0[2] + D * bflo(xv.y)) * siluf(bflo(zv.y)); v[3] = (y0[3] + D * bfhi(xv.y)) * siluf(bfhi(zv.y));
;         v[4] = (y1[0] + D * bflo(xv.z)) * siluf(bflo(zv.z)); v[5] = (y1[1] + D * bfhi(xv.z)) * siluf(bfhi(zv.z));
;         v[6] = (y1[2] + D * bflo(xv.w)) * siluf(bflo(zv.w)); v[7] = (y1[3] + D * bfhi(xv.w)) * siluf(bfhi(zv.w));
;         float s = 0.f;
; #pragma unroll
;         for (int i = 0; i < 8; ++i) s += v[i] * v[i];
;         s = wave_sum(s); const float r = 1.0f / sqrtf(s * (1.0f / 512.0f) + EPSF);
	s_waitcnt vmcnt(19)
	v_lshlrev_b32_e32 v151, 16, v114
	v_mul_f32_e32 v152, 0xbfb8aa3b, v151
	v_exp_f32_e32 v152, v152
	v_lshlrev_b32_e32 v153, 16, v110
	v_fma_f32 v118, v143, v153, v118
	v_and_b32_e32 v114, 0xffff0000, v114
	v_add_f32_e32 v152, 1.0, v152
	v_div_scale_f32 v154, s[4:5], v152, v152, v151
	v_rcp_f32_e32 v155, v154
	v_div_scale_f32 v153, vcc, v151, v152, v151
	v_and_b32_e32 v110, 0xffff0000, v110
	v_fma_f32 v156, -v154, v155, 1.0
	v_fmac_f32_e32 v155, v156, v155
	v_mul_f32_e32 v156, v153, v155
	v_fma_f32 v157, -v154, v156, v153
	v_fmac_f32_e32 v156, v157, v155
	v_fma_f32 v153, -v154, v156, v153
	v_mul_f32_e32 v154, 0xbfb8aa3b, v114
	v_exp_f32_e32 v154, v154
	v_div_fmas_f32 v153, v153, v155, v156
	v_div_fixup_f32 v151, v153, v152, v151
	v_fma_f32 v110, v143, v110, v119
	v_add_f32_e32 v152, 1.0, v154
	v_div_scale_f32 v153, s[4:5], v152, v152, v114
	v_rcp_f32_e32 v154, v153
	v_mul_f32_e32 v118, v118, v151
	s_ashr_i32 s7, s6, 31
	s_lshl_b64 s[8:9], s[6:7], 11
	v_fma_f32 v119, -v153, v154, 1.0
	v_fmac_f32_e32 v154, v119, v154
	v_div_scale_f32 v119, vcc, v114, v152, v114
	v_mul_f32_e32 v151, v119, v154
	v_fma_f32 v155, -v153, v151, v119
	v_fmac_f32_e32 v151, v155, v154
	v_fma_f32 v119, -v153, v151, v119
	v_lshlrev_b32_e32 v153, 16, v115
	v_mul_f32_e32 v155, 0xbfb8aa3b, v153
	v_exp_f32_e32 v155, v155
	v_div_fmas_f32 v119, v119, v154, v151
	v_div_fixup_f32 v114, v119, v152, v114
	v_mul_f32_e32 v110, v110, v114
	v_add_f32_e32 v119, 1.0, v155
	v_div_scale_f32 v151, s[4:5], v119, v119, v153
	v_rcp_f32_e32 v152, v151
	v_lshlrev_b32_e32 v114, 16, v111
	v_fma_f32 v114, v143, v114, v120
	v_and_b32_e32 v115, 0xffff0000, v115
	v_fma_f32 v120, -v151, v152, 1.0
	v_fmac_f32_e32 v152, v120, v152
	v_div_scale_f32 v120, vcc, v153, v119, v153
	v_mul_f32_e32 v154, v120, v152
	v_fma_f32 v155, -v151, v154, v120
	v_fmac_f32_e32 v154, v155, v152
	v_fma_f32 v120, -v151, v154, v120
	v_mul_f32_e32 v151, 0xbfb8aa3b, v115
	v_exp_f32_e32 v151, v151
	v_div_fmas_f32 v120, v120, v152, v154
	v_div_fixup_f32 v119, v120, v119, v153
	v_and_b32_e32 v111, 0xffff0000, v111
	v_add_f32_e32 v120, 1.0, v151
	v_div_scale_f32 v151, s[4:5], v120, v120, v115
	v_rcp_f32_e32 v152, v151
	v_fmac_f32_e32 v121, v143, v111
	v_mul_f32_e32 v114, v114, v119
	s_add_u32 s8, s64, s8
	v_fma_f32 v111, -v151, v152, 1.0
	v_fmac_f32_e32 v152, v111, v152
	v_div_scale_f32 v111, vcc, v115, v120, v115
	v_mul_f32_e32 v119, v111, v152
	v_fma_f32 v153, -v151, v119, v111
	v_fmac_f32_e32 v119, v153, v152
	v_fma_f32 v111, -v151, v119, v111
	v_lshlrev_b32_e32 v151, 16, v116
	v_mul_f32_e32 v153, 0xbfb8aa3b, v151
	v_exp_f32_e32 v153, v153
	v_div_fmas_f32 v111, v111, v152, v119
	v_div_fixup_f32 v111, v111, v120, v115
	v_mul_f32_e32 v111, v121, v111
	v_add_f32_e32 v115, 1.0, v153
	v_div_scale_f32 v119, s[4:5], v115, v115, v151
	v_rcp_f32_e32 v120, v119
	v_lshlrev_b32_e32 v121, 16, v112
	v_fma_f32 v106, v143, v121, v106
	v_and_b32_e32 v116, 0xffff0000, v116
	v_fma_f32 v121, -v119, v120, 1.0
	v_fmac_f32_e32 v120, v121, v120
	v_div_scale_f32 v121, vcc, v151, v115, v151
	v_mul_f32_e32 v152, v121, v120
	v_fma_f32 v153, -v119, v152, v121
	v_fmac_f32_e32 v152, v153, v120
	v_fma_f32 v119, -v119, v152, v121
	v_mul_f32_e32 v121, 0xbfb8aa3b, v116
	v_exp_f32_e32 v121, v121
	v_div_fmas_f32 v119, v119, v120, v152
	v_div_fixup_f32 v115, v119, v115, v151
	v_and_b32_e32 v112, 0xffff0000, v112
	v_add_f32_e32 v119, 1.0, v121
	v_div_scale_f32 v120, s[4:5], v119, v119, v116
	v_rcp_f32_e32 v121, v120
	v_fma_f32 v107, v143, v112, v107
	v_mul_f32_e32 v106, v106, v115
	s_addc_u32 s9, s65, s9
	v_fma_f32 v112, -v120, v121, 1.0
	v_fmac_f32_e32 v121, v112, v121
	v_div_scale_f32 v112, vcc, v116, v119, v116
	v_mul_f32_e32 v115, v112, v121
	v_fma_f32 v151, -v120, v115, v112
	v_fmac_f32_e32 v115, v151, v121
	v_fma_f32 v112, -v120, v115, v112
	v_lshlrev_b32_e32 v120, 16, v117
	v_mul_f32_e32 v151, 0xbfb8aa3b, v120
	v_exp_f32_e32 v151, v151
	v_div_fmas_f32 v112, v112, v121, v115
	v_div_fixup_f32 v112, v112, v119, v116
	v_mul_f32_e32 v107, v107, v112
	v_add_f32_e32 v115, 1.0, v151
	v_div_scale_f32 v116, s[4:5], v115, v115, v120
	v_rcp_f32_e32 v119, v116
	v_lshlrev_b32_e32 v112, 16, v113
	v_fma_f32 v108, v143, v112, v108
	v_fma_f32 v112, -v116, v119, 1.0
	v_fmac_f32_e32 v119, v112, v119
	v_div_scale_f32 v112, vcc, v120, v115, v120
	v_mul_f32_e32 v121, v112, v119
	v_fma_f32 v151, -v116, v121, v112
	v_fmac_f32_e32 v121, v151, v119
	v_fma_f32 v112, -v116, v121, v112
	v_and_b32_e32 v116, 0xffff0000, v117
	v_mul_f32_e32 v117, 0xbfb8aa3b, v116
	v_exp_f32_e32 v117, v117
	v_div_fmas_f32 v112, v112, v119, v121
	v_div_fixup_f32 v112, v112, v115, v120
	v_mul_f32_e32 v108, v108, v112
	v_add_f32_e32 v115, 1.0, v117
	v_div_scale_f32 v117, s[4:5], v115, v115, v116
	v_rcp_f32_e32 v119, v117
	v_and_b32_e32 v112, 0xffff0000, v113
	v_fmac_f32_e32 v109, v143, v112
	v_fma_f32 v112, -v117, v119, 1.0
	v_fmac_f32_e32 v119, v112, v119
	v_div_scale_f32 v112, vcc, v116, v115, v116
	v_mul_f32_e32 v113, v112, v119
	v_fma_f32 v120, -v117, v113, v112
	v_fmac_f32_e32 v113, v120, v119
	v_fma_f32 v112, -v117, v113, v112
	v_div_fmas_f32 v112, v112, v119, v113
	v_div_fixup_f32 v112, v112, v115, v116
	v_mul_f32_e32 v109, v109, v112
	v_mul_f32_e32 v112, v110, v110
	v_fmac_f32_e32 v112, v118, v118
	v_fmac_f32_e32 v112, v114, v114
	v_fmac_f32_e32 v112, v111, v111
	v_fmac_f32_e32 v112, v106, v106
	v_fmac_f32_e32 v112, v107, v107
	v_fmac_f32_e32 v112, v108, v108
	v_fmac_f32_e32 v112, v109, v109
	ds_bpermute_b32 v113, v1, v112
	s_waitcnt lgkmcnt(0)
	v_add_f32_e32 v112, v112, v113
	ds_bpermute_b32 v113, v138, v112
	s_waitcnt lgkmcnt(0)
	v_add_f32_e32 v112, v112, v113
	ds_bpermute_b32 v113, v139, v112
	s_waitcnt lgkmcnt(0)
; __device__ __forceinline__ float bflo(unsigned w) { return __uint_as_float(w << 16); }
; __device__ __forceinline__ float bfhi(unsigned w) { return __uint_as_float(w & 0xffff0000u); }
; __device__ __forceinline__ float siluf(float a) { return a / (1.0f + __expf(-a)); }
; __device__ __forceinline__ void p5_item(const P5Row& R, const P5In& I, const P5Par& P, int t, int lane) {
;     ...
;     for (int g = 0; g < 2; ++g) { const int ch = g * 512 + 8 * lane;
;         const f32x4 y0 = R.ya[g], y1 = R.yb[g]; const v4u xv = R.xr[g], zv = R.zr[g];
;         const float D = P.D[g];
;         float v[8];
;         v[0] = (y0[0] + D * bflo(xv.x)) * siluf(bflo(zv.x)); v[1] = (y0[1] + D * bfhi(xv.x)) * siluf(bfhi(zv.x));
;         v[2] = (y0[2] + D * bflo(xv.y)) * siluf(bflo(zv.y)); v[3] = (y0[3] + D * bfhi(xv.y)) * siluf(bfhi(zv.y));
;         v[4] = (y1[0] + D * bflo(xv.z)) * siluf(bflo(zv.z)); v[5] = (y1[1] + D * bfhi(xv.z)) * siluf(bfhi(zv.z));
;         v[6] = (y1[2] + D * bflo(xv.w)) * siluf(bflo(zv.w)); v[7] = (y1[3] + D * bfhi(xv.w)) * siluf(bfhi(zv.w));
;         float s = 0.f;
; #pragma unroll
;         for (int i = 0; i < 8; ++i) s += v[i] * v[i];
;         s = wave_sum(s); const float r = 1.0f / sqrtf(s * (1.0f / 512.0f) + EPSF);
;         p5_put8(I, (size_t)t * DM + ch, v, r, P.gs[g][0], P.gs[g][1]); }
	v_add_f32_e32 v112, v112, v113
	ds_bpermute_b32 v113, v140, v112
	s_waitcnt lgkmcnt(0)
	v_add_f32_e32 v112, v112, v113
	ds_bpermute_b32 v113, v141, v112
	s_waitcnt lgkmcnt(0)
	v_add_f32_e32 v112, v112, v113
	ds_bpermute_b32 v113, v142, v112
	s_waitcnt lgkmcnt(0)
	v_add_f32_e32 v112, v112, v113
	v_fmamk_f32 v112, v112, 0x3b000000, v146
	v_mul_f32_e32 v113, 0x4f800000, v112
	v_cmp_gt_f32_e32 vcc, s24, v112
	s_nop 1
	v_cndmask_b32_e32 v112, v112, v113, vcc
	v_sqrt_f32_e32 v113, v112
	s_nop 0
	v_add_u32_e32 v115, -1, v113
	v_fma_f32 v116, -v115, v113, v112
	v_cmp_ge_f32_e64 s[4:5], 0, v116
	v_add_u32_e32 v116, 1, v113
	s_nop 0
	v_cndmask_b32_e64 v115, v113, v115, s[4:5]
	v_fma_f32 v113, -v116, v113, v112
	v_cmp_lt_f32_e64 s[4:5], 0, v113
	s_nop 1
	v_cndmask_b32_e64 v113, v115, v116, s[4:5]
	v_mul_f32_e32 v115, 0x37800000, v113
	v_cndmask_b32_e32 v113, v113, v115, vcc
	v_cmp_class_f32_e32 vcc, v112, v147
	s_nop 1
	v_cndmask_b32_e32 v112, v113, v112, vcc
	v_div_scale_f32 v113, s[4:5], v112, v112, 1.0
	v_rcp_f32_e32 v115, v113
	s_nop 0
	v_fma_f32 v116, -v113, v115, 1.0
	v_fmac_f32_e32 v115, v116, v115
	v_div_scale_f32 v116, vcc, 1.0, v112, 1.0
	v_mul_f32_e32 v117, v116, v115
	v_fma_f32 v119, -v113, v117, v116
	v_fmac_f32_e32 v117, v119, v115
	v_fma_f32 v113, -v113, v117, v116
	v_div_fmas_f32 v113, v113, v115, v117
	s_waitcnt vmcnt(18)
	v_lshlrev_b32_e32 v115, 16, v98
	v_mul_f32_e32 v116, 0xbfb8aa3b, v115
	v_exp_f32_e32 v116, v116
	v_div_fixup_f32 v112, v113, v112, 1.0
	v_mul_f32_e32 v112, 0x41000000, v112
	v_mul_f32_e32 v113, v118, v112
	v_add_f32_e32 v116, 1.0, v116
	v_div_scale_f32 v117, s[4:5], v116, v116, v115
	v_rcp_f32_e32 v118, v117
	v_lshlrev_b32_e32 v119, 16, v90
	v_fma_f32 v102, v144, v119, v102
	v_and_b32_e32 v98, 0xffff0000, v98
	v_fma_f32 v119, -v117, v118, 1.0
	v_fmac_f32_e32 v118, v119, v118
	v_div_scale_f32 v119, vcc, v115, v116, v115
	v_mul_f32_e32 v120, v119, v118
	v_fma_f32 v121, -v117, v120, v119
	v_fmac_f32_e32 v120, v121, v118
	v_fma_f32 v117, -v117, v120, v119
	v_mul_f32_e32 v119, 0xbfb8aa3b, v98
	v_exp_f32_e32 v119, v119
	v_div_fmas_f32 v117, v117, v118, v120
	v_div_fixup_f32 v115, v117, v116, v115
	v_and_b32_e32 v90, 0xffff0000, v90
	v_add_f32_e32 v116, 1.0, v119
	v_div_scale_f32 v117, s[4:5], v116, v116, v98
	v_rcp_f32_e32 v118, v117
	v_fma_f32 v90, v144, v90, v103
	v_mul_f32_e32 v102, v102, v115
	v_mul_f32_e32 v113, v26, v113
	v_fma_f32 v103, -v117, v118, 1.0
	v_fmac_f32_e32 v118, v103, v118
	v_div_scale_f32 v103, vcc, v98, v116, v98
	v_mul_f32_e32 v115, v103, v118
	v_fma_f32 v119, -v117, v115, v103
	v_fmac_f32_e32 v115, v119, v118
	v_fma_f32 v103, -v117, v115, v103
	v_lshlrev_b32_e32 v117, 16, v99
	v_mul_f32_e32 v119, 0xbfb8aa3b, v117
	v_exp_f32_e32 v119, v119
	v_div_fmas_f32 v103, v103, v118, v115
	v_div_fixup_f32 v98, v103, v116, v98
	v_mul_f32_e32 v90, v90, v98
	v_add_f32_e32 v103, 1.0, v119
	v_div_scale_f32 v115, s[4:5], v103, v103, v117
	v_rcp_f32_e32 v116, v115
	v_lshlrev_b32_e32 v98, 16, v91
	v_fma_f32 v98, v144, v98, v104
	v_and_b32_e32 v99, 0xffff0000, v99
	v_fma_f32 v104, -v115, v116, 1.0
	v_fmac_f32_e32 v116, v104, v116
	v_div_scale_f32 v104, vcc, v117, v103, v117
	v_mul_f32_e32 v118, v104, v116
	v_fma_f32 v119, -v115, v118, v104
	v_fmac_f32_e32 v118, v119, v116
	v_fma_f32 v104, -v115, v118, v104
	v_mul_f32_e32 v115, 0xbfb8aa3b, v99
	v_exp_f32_e32 v115, v115
	v_div_fmas_f32 v104, v104, v116, v118
	v_div_fixup_f32 v103, v104, v103, v117
	v_and_b32_e32 v91, 0xffff0000, v91
	v_add_f32_e32 v104, 1.0, v115
	v_div_scale_f32 v115, s[4:5], v104, v104, v99
	v_rcp_f32_e32 v116, v115
	v_fmac_f32_e32 v105, v144, v91
	v_mul_f32_e32 v98, v98, v103
	v_fma_f32 v91, -v115, v116, 1.0
	v_fmac_f32_e32 v116, v91, v116
	v_div_scale_f32 v91, vcc, v99, v104, v99
	v_mul_f32_e32 v103, v91, v116
	v_fma_f32 v117, -v115, v103, v91
	v_fmac_f32_e32 v103, v117, v116
	v_fma_f32 v91, -v115, v103, v91
	v_lshlrev_b32_e32 v115, 16, v100
	v_mul_f32_e32 v117, 0xbfb8aa3b, v115
	v_exp_f32_e32 v117, v117
	v_div_fmas_f32 v91, v91, v116, v103
	v_div_fixup_f32 v91, v91, v104, v99
	v_mul_f32_e32 v91, v105, v91
	v_add_f32_e32 v99, 1.0, v117
	v_div_scale_f32 v103, s[4:5], v99, v99, v115
	v_rcp_f32_e32 v104, v103
	v_lshlrev_b32_e32 v105, 16, v92
	v_fma_f32 v86, v144, v105, v86
	v_and_b32_e32 v100, 0xffff0000, v100
	v_fma_f32 v105, -v103, v104, 1.0
	v_fmac_f32_e32 v104, v105, v104
	v_div_scale_f32 v105, vcc, v115, v99, v115
	v_mul_f32_e32 v116, v105, v104
	v_fma_f32 v117, -v103, v116, v105
	v_fmac_f32_e32 v116, v117, v104
	v_fma_f32 v103, -v103, v116, v105
	v_mul_f32_e32 v105, 0xbfb8aa3b, v100
	v_exp_f32_e32 v105, v105
	v_div_fmas_f32 v103, v103, v104, v116
	v_div_fixup_f32 v99, v103, v99, v115
	v_mul_f32_e32 v99, v86, v99
	v_add_f32_e32 v103, 1.0, v105
	v_div_scale_f32 v104, s[4:5], v103, v103, v100
	v_rcp_f32_e32 v105, v104
	v_and_b32_e32 v86, 0xffff0000, v92
	v_fma_f32 v86, v144, v86, v87
	v_fma_f32 v87, -v104, v105, 1.0
	v_fmac_f32_e32 v105, v87, v105
	v_div_scale_f32 v87, vcc, v100, v103, v100
	v_mul_f32_e32 v92, v87, v105
	v_fma_f32 v115, -v104, v92, v87
	v_fmac_f32_e32 v92, v115, v105
	v_fma_f32 v87, -v104, v92, v87
	v_lshlrev_b32_e32 v104, 16, v101
	v_mul_f32_e32 v115, 0xbfb8aa3b, v104
	v_exp_f32_e32 v115, v115
	v_div_fmas_f32 v87, v87, v105, v92
	v_div_fixup_f32 v87, v87, v103, v100
	v_mul_f32_e32 v105, v86, v87
	v_add_f32_e32 v92, 1.0, v115
	v_div_scale_f32 v100, s[4:5], v92, v92, v104
	v_rcp_f32_e32 v103, v100
	v_lshlrev_b32_e32 v86, 16, v93
	v_fma_f32 v86, v144, v86, v88
	v_fma_f32 v87, -v100, v103, 1.0
	v_fmac_f32_e32 v103, v87, v103
	v_div_scale_f32 v87, vcc, v104, v92, v104
	v_mul_f32_e32 v88, v87, v103
	v_fma_f32 v115, -v100, v88, v87
	v_fmac_f32_e32 v88, v115, v103
	v_fma_f32 v87, -v100, v88, v87
	v_and_b32_e32 v100, 0xffff0000, v101
	v_mul_f32_e32 v101, 0xbfb8aa3b, v100
	v_exp_f32_e32 v101, v101
	v_div_fmas_f32 v87, v87, v103, v88
	v_div_fixup_f32 v87, v87, v92, v104
	v_mul_f32_e32 v103, v86, v87
	v_add_f32_e32 v88, 1.0, v101
	v_div_scale_f32 v92, s[4:5], v88, v88, v100
	v_rcp_f32_e32 v101, v92
	v_and_b32_e32 v86, 0xffff0000, v93
	v_fmac_f32_e32 v89, v144, v86
	v_fma_f32 v86, -v92, v101, 1.0
	v_fmac_f32_e32 v101, v86, v101
	v_div_scale_f32 v86, vcc, v100, v88, v100
	v_mul_f32_e32 v87, v86, v101
	v_fma_f32 v93, -v92, v87, v86
	v_fmac_f32_e32 v87, v93, v101
	v_fma_f32 v86, -v92, v87, v86
	v_div_fmas_f32 v86, v86, v101, v87
	v_div_fixup_f32 v86, v86, v88, v100
	v_mul_f32_e32 v89, v89, v86
	v_mul_f32_e32 v86, v90, v90
	v_fmac_f32_e32 v86, v102, v102
	v_fmac_f32_e32 v86, v98, v98
	v_fmac_f32_e32 v86, v91, v91
	v_fmac_f32_e32 v86, v99, v99
	v_fmac_f32_e32 v86, v105, v105
	v_fmac_f32_e32 v86, v103, v103
	v_fmac_f32_e32 v86, v89, v89
	ds_bpermute_b32 v87, v1, v86
	v_mul_f32_e32 v88, v110, v112
	v_mul_f32_e32 v88, v27, v88
	v_mul_f32_e32 v93, v111, v112
	v_mul_f32_e32 v93, v29, v93
	s_waitcnt lgkmcnt(0)
; __device__ __forceinline__ float bflo(unsigned w) { return __uint_as_float(w << 16); }
; __device__ __forceinline__ float bfhi(unsigned w) { return __uint_as_float(w & 0xffff0000u); }
; __device__ __forceinline__ float siluf(float a) { return a / (1.0f + __expf(-a)); }
; __device__ __forceinline__ void p5_item(const P5Row& R, const P5In& I, const P5Par& P, int t, int lane) {
;     ...
;     for (int g = 0; g < 2; ++g) { const int ch = g * 512 + 8 * lane;
;         const f32x4 y0 = R.ya[g], y1 = R.yb[g]; const v4u xv = R.xr[g], zv = R.zr[g];
;         const float D = P.D[g];
;         float v[8];
;         v[0] = (y0[0] + D * bflo(xv.x)) * siluf(bflo(zv.x)); v[1] = (y0[1] + D * bfhi(xv.x)) * siluf(bfhi(zv.x));
;         v[2] = (y0[2] + D * bflo(xv.y)) * siluf(bflo(zv.y)); v[3] = (y0[3] + D * bfhi(xv.y)) * siluf(bfhi(zv.y));
;         v[4] = (y1[0] + D * bflo(xv.z)) * siluf(bflo(zv.z)); v[5] = (y1[1] + D * bfhi(xv.z)) * siluf(bfhi(zv.z));
;         v[6] = (y1[2] + D * bflo(xv.w)) * siluf(bflo(zv.w)); v[7] = (y1[3] + D * bfhi(xv.w)) * siluf(bfhi(zv.w));
;         float s = 0.f;
; #pragma unroll
;         for (int i = 0; i < 8; ++i) s += v[i] * v[i];
;         s = wave_sum(s); const float r = 1.0f / sqrtf(s * (1.0f / 512.0f) + EPSF);
;         p5_put8(I, (size_t)t * DM + ch, v, r, P.gs[g][0], P.gs[g][1]); }
;     { const int ch = 8 * lane; const v4u r4 = R.m4;
;       float v[8] = {bflo(r4.x), bfhi(r4.x), bflo(r4.y), bfhi(r4.y), bflo(r4.z), bfhi(r4.z), bflo(r4.w), bfhi(r4.w)}; float s = 0.f;
; #pragma unroll
;       for (int i = 0; i < 8; ++i) s += v[i] * v[i];
;       s += __shfl_xor(s, 1); s += __shfl_xor(s, 2); s += __shfl_xor(s, 4);
;       const float r = 1.0f / sqrtf(s * (1.0f / 64.0f) + EPSF);
;       p5_put8(I, (size_t)t * DM + 1024 + ch, v, r, P.gm[0], P.gm[1]); }
	v_add_f32_e32 v86, v86, v87
	ds_bpermute_b32 v87, v138, v86
	v_med3_f32 v100, v113, s25, v150
	v_med3_f32 v88, v88, s25, v150
	v_mul_f32_e32 v92, v114, v112
	v_mul_f32_e32 v92, v28, v92
	s_waitcnt lgkmcnt(0)
	v_add_f32_e32 v87, v86, v87
	ds_bpermute_b32 v101, v139, v87
	v_mov_b32_e32 v86, 0
	v_cvt_pk_fp8_f32 v86, v100, v88
	v_med3_f32 v88, v93, s25, v150
	v_med3_f32 v92, v92, s25, v150
	s_waitcnt lgkmcnt(0)
	v_add_f32_e32 v87, v87, v101
	ds_bpermute_b32 v93, v140, v87
	v_cvt_pk_fp8_f32 v86, v92, v88 op_sel:[0,0,1]
	v_mul_f32_e32 v88, v106, v112
	v_mul_f32_e32 v92, v107, v112
	v_mul_f32_e32 v88, v30, v88
	s_waitcnt lgkmcnt(0)
	v_add_f32_e32 v87, v87, v93
	ds_bpermute_b32 v93, v141, v87
	v_mul_f32_e32 v92, v31, v92
	v_med3_f32 v88, v88, s25, v150
	v_med3_f32 v92, v92, s25, v150
	v_mul_f32_e32 v100, v108, v112
	s_waitcnt lgkmcnt(0)
	v_add_f32_e32 v87, v87, v93
	ds_bpermute_b32 v93, v142, v87
	v_mul_f32_e32 v101, v109, v112
	v_mul_f32_e32 v100, v32, v100
	v_mul_f32_e32 v101, v33, v101
	v_med3_f32 v100, v100, s25, v150
	s_waitcnt lgkmcnt(0)
	v_add_f32_e32 v87, v87, v93
	v_fmamk_f32 v87, v87, 0x3b000000, v146
	v_mul_f32_e32 v93, 0x4f800000, v87
	v_cmp_gt_f32_e32 vcc, s24, v87
	v_med3_f32 v101, v101, s25, v150
	s_nop 0
	v_cndmask_b32_e32 v93, v87, v93, vcc
	v_sqrt_f32_e32 v104, v93
	v_mov_b32_e32 v87, 0
	v_cvt_pk_fp8_f32 v87, v88, v92
	v_add_u32_e32 v88, -1, v104
	v_fma_f32 v92, -v88, v104, v93
	v_cmp_ge_f32_e64 s[4:5], 0, v92
	v_add_u32_e32 v92, 1, v104
	v_cvt_pk_fp8_f32 v87, v100, v101 op_sel:[0,0,1]
	v_cndmask_b32_e64 v88, v104, v88, s[4:5]
	v_fma_f32 v104, -v92, v104, v93
	v_cmp_lt_f32_e64 s[4:5], 0, v104
	s_nop 1
	v_cndmask_b32_e64 v88, v88, v92, s[4:5]
	v_mul_f32_e32 v92, 0x37800000, v88
	v_cndmask_b32_e32 v88, v88, v92, vcc
	v_cmp_class_f32_e32 vcc, v93, v147
	s_nop 1
	v_cndmask_b32_e32 v88, v88, v93, vcc
	v_div_scale_f32 v92, s[4:5], v88, v88, 1.0
	v_rcp_f32_e32 v93, v92
	s_nop 0
	v_fma_f32 v100, -v92, v93, 1.0
	v_fmac_f32_e32 v93, v100, v93
	v_div_scale_f32 v100, vcc, 1.0, v88, 1.0
	v_mul_f32_e32 v101, v100, v93
	v_fma_f32 v104, -v92, v101, v100
	v_fmac_f32_e32 v101, v104, v93
	v_fma_f32 v92, -v92, v101, v100
	v_div_fmas_f32 v92, v92, v93, v101
	v_div_fixup_f32 v88, v92, v88, 1.0
	v_mul_f32_e32 v92, 0x41000000, v88
	v_mul_f32_e32 v88, v102, v92
	v_mul_f32_e32 v90, v90, v92
	v_mul_f32_e32 v88, v18, v88
	v_mul_f32_e32 v90, v19, v90
	v_mul_f32_e32 v93, v98, v92
	v_med3_f32 v98, v88, s25, v150
	v_med3_f32 v90, v90, s25, v150
	v_mov_b32_e32 v88, 0
	v_cvt_pk_fp8_f32 v88, v98, v90
	v_mul_f32_e32 v91, v91, v92
	v_mul_f32_e32 v93, v20, v93
	v_mul_f32_e32 v90, v21, v91
	v_med3_f32 v91, v93, s25, v150
	v_med3_f32 v90, v90, s25, v150
	v_cvt_pk_fp8_f32 v88, v91, v90 op_sel:[0,0,1]
	s_waitcnt vmcnt(17)
	v_and_b32_e32 v91, 0xffff0000, v70
	v_lshlrev_b32_e32 v90, 16, v70
	v_mul_f32_e32 v70, v91, v91
	v_lshlrev_b32_e32 v93, 16, v71
	v_fmac_f32_e32 v70, v90, v90
	v_and_b32_e32 v98, 0xffff0000, v71
	v_fmac_f32_e32 v70, v93, v93
	v_lshlrev_b32_e32 v100, 16, v72
	v_fmac_f32_e32 v70, v98, v98
	v_and_b32_e32 v72, 0xffff0000, v72
	v_fmac_f32_e32 v70, v100, v100
	v_lshlrev_b32_e32 v101, 16, v73
	v_fmac_f32_e32 v70, v72, v72
	v_and_b32_e32 v73, 0xffff0000, v73
	v_fmac_f32_e32 v70, v101, v101
	v_fmac_f32_e32 v70, v73, v73
	ds_bpermute_b32 v71, v1, v70
	v_mul_f32_e32 v99, v99, v92
	v_mul_f32_e32 v102, v105, v92
	v_mul_f32_e32 v99, v22, v99
	v_mul_f32_e32 v102, v23, v102
	s_waitcnt lgkmcnt(0)
	v_add_f32_e32 v70, v70, v71
	ds_bpermute_b32 v71, v138, v70
	v_mul_f32_e32 v89, v89, v92
	v_mul_f32_e32 v103, v103, v92
	v_mul_f32_e32 v92, v25, v89
	v_med3_f32 v99, v99, s25, v150
	s_waitcnt lgkmcnt(0)
	v_add_f32_e32 v70, v70, v71
	ds_bpermute_b32 v71, v139, v70
	v_med3_f32 v102, v102, s25, v150
	v_mov_b32_e32 v89, 0
	v_cvt_pk_fp8_f32 v89, v99, v102
	v_mul_f32_e32 v103, v24, v103
	s_waitcnt lgkmcnt(0)
	v_add_f32_e32 v70, v70, v71
	v_fmamk_f32 v70, v70, 0x3c800000, v146
	v_mul_f32_e32 v71, 0x4f800000, v70
	v_cmp_gt_f32_e32 vcc, s24, v70
	v_med3_f32 v99, v103, s25, v150
	v_med3_f32 v92, v92, s25, v150
	v_cndmask_b32_e32 v70, v70, v71, vcc
	v_sqrt_f32_e32 v71, v70
	v_cvt_pk_fp8_f32 v89, v99, v92 op_sel:[0,0,1]
	v_add_u32_e32 v92, -1, v71
	v_fma_f32 v99, -v92, v71, v70
	v_cmp_ge_f32_e64 s[4:5], 0, v99
	v_add_u32_e32 v99, 1, v71
	s_nop 0
	v_cndmask_b32_e64 v92, v71, v92, s[4:5]
	v_fma_f32 v71, -v99, v71, v70
	v_cmp_lt_f32_e64 s[4:5], 0, v71
	s_nop 1
	v_cndmask_b32_e64 v71, v92, v99, s[4:5]
	v_mul_f32_e32 v92, 0x37800000, v71
	v_cndmask_b32_e32 v71, v71, v92, vcc
	v_cmp_class_f32_e32 vcc, v70, v147
	s_nop 1
	v_cndmask_b32_e32 v92, v71, v70, vcc
	v_div_scale_f32 v99, s[4:5], v92, v92, 1.0
	v_rcp_f32_e32 v102, v99
	v_lshl_add_u64 v[70:71], s[8:9], 0, v[122:123]
	global_store_dwordx2 v[70:71], v[86:87], off
	global_store_dwordx2 v[70:71], v[88:89], off offset:512
	v_fma_f32 v86, -v99, v102, 1.0
	v_fmac_f32_e32 v102, v86, v102
	v_div_scale_f32 v86, vcc, 1.0, v92, 1.0
	v_mul_f32_e32 v87, v86, v102
	v_fma_f32 v88, -v99, v87, v86
	v_fmac_f32_e32 v87, v88, v102
	v_fma_f32 v86, -v99, v87, v86
	v_div_fmas_f32 v86, v86, v102, v87
	v_div_fixup_f32 v86, v86, v92, 1.0
	v_mul_f32_e32 v86, 0x41000000, v86
	v_mul_f32_e32 v88, v86, v91
	s_waitcnt vmcnt(18)
; __device__ __forceinline__ float bflo(unsigned w) { return __uint_as_float(w << 16); }
; __device__ __forceinline__ float bfhi(unsigned w) { return __uint_as_float(w & 0xffff0000u); }
; __device__ __forceinline__ void p5_item(const P5Row& R, const P5In& I, const P5Par& P, int t, int lane) {
;     ...
;     { const int h = lane >> 4, d = 8 * (lane & 15); const v4u a4 = R.a4, b4 = R.b4; const float lam = P.lam;
;       float v[8] = {bflo(a4.x) - lam * bflo(b4.x), bfhi(a4.x) - lam * bfhi(b4.x), bflo(a4.y) - lam * bflo(b4.y), bfhi(a4.y) - lam * bfhi(b4.y),
;                     bflo(a4.z) - lam * bflo(b4.z), bfhi(a4.z) - lam * bfhi(b4.z), bflo(a4.w) - lam * bflo(b4.w), bfhi(a4.w) - lam * bfhi(b4.w)}; float s = 0.f;
; #pragma unroll
;       for (int i = 0; i < 8; ++i) s += v[i] * v[i];
;       s += __shfl_xor(s, 1); s += __shfl_xor(s, 2); s += __shfl_xor(s, 4); s += __shfl_xor(s, 8);
;       const float r = (1.0f - I.lambda_init) / sqrtf(s * (1.0f / 128.0f) + EPSF);
;       p5_put8(I, (size_t)t * DM + 1536 + h * 128 + d, v, r, P.gd[0], P.gd[1]); }
; __device__ __forceinline__ void p5_finalize(const Ctx& X, const P5In& I) {
;     ...
;     for (int t = X.gw; t < NTOK; t += 2 * X.ngw) { const int t1 = t + X.ngw, t2 = t + 2 * X.ngw;
;         p5_load(B, I, t1 < NTOK ? t1 : NTOK - 1, X.lane);
;         p5_item(A, I, P, t, X.lane);
;         p5_load(A, I, t2 < NTOK ? t2 : NTOK - 1, X.lane);
;         if (t1 < NTOK) p5_item(B, I, P, t1, X.lane); }
	v_lshlrev_b32_e32 v91, 16, v62
	s_waitcnt vmcnt(17)
	v_lshlrev_b32_e32 v92, 16, v66
	v_and_b32_e32 v62, 0xffff0000, v62
	v_and_b32_e32 v66, 0xffff0000, v66
	v_fma_f32 v91, -v145, v92, v91
	v_fma_f32 v66, -v145, v66, v62
	v_lshlrev_b32_e32 v62, 16, v63
	v_lshlrev_b32_e32 v92, 16, v67
	v_fma_f32 v92, -v145, v92, v62
	v_and_b32_e32 v62, 0xffff0000, v63
	v_and_b32_e32 v63, 0xffff0000, v67
	v_fma_f32 v67, -v145, v63, v62
	v_lshlrev_b32_e32 v62, 16, v64
	v_lshlrev_b32_e32 v63, 16, v68
	v_mul_f32_e32 v89, v86, v93
	v_fma_f32 v93, -v145, v63, v62
	v_and_b32_e32 v62, 0xffff0000, v64
	v_and_b32_e32 v63, 0xffff0000, v68
	v_fma_f32 v68, -v145, v63, v62
	v_lshlrev_b32_e32 v62, 16, v65
	v_lshlrev_b32_e32 v63, 16, v69
	v_mul_f32_e32 v87, v86, v90
	v_mul_f32_e32 v90, v86, v98
	v_fma_f32 v98, -v145, v63, v62
	v_and_b32_e32 v62, 0xffff0000, v65
	v_and_b32_e32 v63, 0xffff0000, v69
	v_fma_f32 v65, -v145, v63, v62
	v_mul_f32_e32 v63, v66, v66
	v_fmac_f32_e32 v63, v91, v91
	v_fmac_f32_e32 v63, v92, v92
	v_fmac_f32_e32 v63, v67, v67
	v_fmac_f32_e32 v63, v93, v93
	v_fmac_f32_e32 v63, v68, v68
	v_fmac_f32_e32 v63, v98, v98
	v_fmac_f32_e32 v63, v65, v65
	ds_bpermute_b32 v64, v1, v63
	v_mul_f32_e32 v87, v10, v87
	v_mul_f32_e32 v88, v11, v88
	v_med3_f32 v69, v87, s25, v150
	v_med3_f32 v87, v88, s25, v150
	s_waitcnt lgkmcnt(0)
	v_add_f32_e32 v63, v63, v64
	ds_bpermute_b32 v64, v138, v63
	v_mov_b32_e32 v62, 0
	v_cvt_pk_fp8_f32 v62, v69, v87
	v_mul_f32_e32 v89, v12, v89
	v_mul_f32_e32 v90, v13, v90
	s_waitcnt lgkmcnt(0)
	v_add_f32_e32 v63, v63, v64
	ds_bpermute_b32 v64, v139, v63
	v_med3_f32 v69, v89, s25, v150
	v_med3_f32 v87, v90, s25, v150
	v_cvt_pk_fp8_f32 v62, v69, v87 op_sel:[0,0,1]
	v_mul_f32_e32 v69, v86, v100
	s_waitcnt lgkmcnt(0)
	v_add_f32_e32 v63, v63, v64
	ds_bpermute_b32 v64, v140, v63
	v_mul_f32_e32 v72, v86, v72
	v_mul_f32_e32 v87, v86, v101
	v_mul_f32_e32 v73, v86, v73
	v_mul_f32_e32 v69, v14, v69
	s_waitcnt lgkmcnt(0)
	v_add_f32_e32 v63, v63, v64
	v_fmamk_f32 v63, v63, 0x3c000000, v146
	v_mul_f32_e32 v64, 0x4f800000, v63
	v_cmp_gt_f32_e32 vcc, s24, v63
	v_mul_f32_e32 v72, v15, v72
	v_med3_f32 v69, v69, s25, v150
	v_cndmask_b32_e32 v64, v63, v64, vcc
	v_sqrt_f32_e32 v86, v64
	v_med3_f32 v72, v72, s25, v150
	v_mov_b32_e32 v63, 0
	v_cvt_pk_fp8_f32 v63, v69, v72
	v_add_u32_e32 v69, -1, v86
	v_fma_f32 v72, -v69, v86, v64
	v_cmp_ge_f32_e64 s[4:5], 0, v72
	v_add_u32_e32 v72, 1, v86
	v_mul_f32_e32 v87, v16, v87
	v_cndmask_b32_e64 v69, v86, v69, s[4:5]
	v_fma_f32 v86, -v72, v86, v64
	v_cmp_lt_f32_e64 s[4:5], 0, v86
	v_mul_f32_e32 v73, v17, v73
	v_med3_f32 v86, v87, s25, v150
	v_cndmask_b32_e64 v69, v69, v72, s[4:5]
	v_mul_f32_e32 v72, 0x37800000, v69
	v_cndmask_b32_e32 v69, v69, v72, vcc
	v_cmp_class_f32_e32 vcc, v64, v147
	v_med3_f32 v73, v73, s25, v150
	v_cvt_pk_fp8_f32 v63, v86, v73 op_sel:[0,0,1]
	v_cndmask_b32_e32 v64, v69, v64, vcc
	v_div_scale_f32 v69, s[4:5], v64, v64, s26
	v_rcp_f32_e32 v72, v69
	global_store_dwordx2 v[70:71], v[62:63], off offset:1024
	v_lshl_add_u64 v[62:63], s[8:9], 0, v[128:129]
	v_lshl_add_u64 v[62:63], v[62:63], 0, v[124:125]
	v_fma_f32 v73, -v69, v72, 1.0
	v_fmac_f32_e32 v72, v73, v72
	v_div_scale_f32 v73, vcc, s26, v64, s26
	v_mul_f32_e32 v86, v73, v72
	v_fma_f32 v87, -v69, v86, v73
	v_fmac_f32_e32 v86, v87, v72
	v_fma_f32 v69, -v69, v86, v73
	v_div_fmas_f32 v69, v69, v72, v86
	v_div_fixup_f32 v64, v69, v64, s26
	v_mul_f32_e32 v69, 0x41000000, v64
	v_mul_f32_e32 v64, v91, v69
	v_mul_f32_e32 v66, v66, v69
	v_mul_f32_e32 v64, v2, v64
	v_mul_f32_e32 v66, v3, v66
	v_med3_f32 v73, v64, s25, v150
	v_med3_f32 v66, v66, s25, v150
	v_mov_b32_e32 v64, 0
	v_cvt_pk_fp8_f32 v64, v73, v66
	v_mul_f32_e32 v72, v92, v69
	v_mul_f32_e32 v67, v67, v69
	v_mul_f32_e32 v72, v4, v72
	v_mul_f32_e32 v66, v5, v67
	v_med3_f32 v67, v72, s25, v150
	v_med3_f32 v66, v66, s25, v150
	v_cvt_pk_fp8_f32 v64, v67, v66 op_sel:[0,0,1]
	v_mul_f32_e32 v66, v93, v69
	v_mul_f32_e32 v67, v68, v69
	v_mul_f32_e32 v66, v6, v66
	v_mul_f32_e32 v67, v7, v67
	v_mul_f32_e32 v68, v98, v69
	v_mul_f32_e32 v69, v65, v69
	v_med3_f32 v66, v66, s25, v150
	v_med3_f32 v67, v67, s25, v150
	v_mov_b32_e32 v65, 0
	v_cvt_pk_fp8_f32 v65, v66, v67
	v_mul_f32_e32 v68, v8, v68
	v_mul_f32_e32 v66, v9, v69
	v_med3_f32 v67, v68, s25, v150
	v_med3_f32 v66, v66, s25, v150
	v_cvt_pk_fp8_f32 v65, v67, v66 op_sel:[0,0,1]
	global_store_dwordx2 v[62:63], v[64:65], off offset:1536
	s_branch .LBB0_3411
